# GEMM loops: first 4 bf16 / 2 fp8 MFMAs of each super-phase issued before the pre-MFMA barrier (overlap hand-over between wave halves)
# baseline (speedup 1.0000x reference)
.LBB0_261:
	ds_read_b128 v[144:147], v170
	ds_read_b128 v[148:151], v170 offset:1024
	ds_read_b128 v[174:177], v170 offset:2048
	ds_read_b128 v[178:181], v170 offset:3072
	ds_read_b128 v[182:185], v171
	ds_read_b128 v[186:189], v171 offset:1024
	ds_read_b128 v[190:193], v171 offset:2048
	ds_read_b128 v[194:197], v171 offset:3072
	s_add_u32 s26, s80, 0xfff80080
	s_addc_u32 s27, s81, -1
	s_cmp_eq_u32 vcc_hi, 28
	s_cselect_b32 s83, s69, s27
	s_cselect_b32 s82, s75, s26
	s_cselect_b32 s27, s57, vcc_lo
	s_cselect_b32 s26, s96, s97
	v_lshl_add_u64 v[152:153], s[80:81], 0, v[134:135]
	s_add_i32 m0, s87, 0xc000
	ds_read_b128 v[198:201], v172
	ds_read_b128 v[202:205], v172 offset:1024
	ds_read_b128 v[206:209], v172 offset:2048
	ds_read_b128 v[210:213], v172 offset:3072
	ds_read_b128 v[214:217], v172 offset:4096
	ds_read_b128 v[220:223], v172 offset:5120
	ds_read_b128 v[224:227], v172 offset:6144
	ds_read_b128 v[228:231], v172 offset:7168
	global_load_lds_dwordx4 v[152:153], off
	v_lshl_add_u64 v[152:153], s[80:81], 0, v[138:139]
	s_add_i32 m0, s87, 0xe000
	s_nop 0
	global_load_lds_dwordx4 v[152:153], off
	s_waitcnt vmcnt(8)
	s_waitcnt lgkmcnt(0)
	v_mfma_f32_16x16x32_bf16 v[122:125], v[144:147], v[198:201], v[122:125]
	v_mfma_f32_16x16x32_bf16 v[118:121], v[174:177], v[198:201], v[118:121]
	v_mfma_f32_16x16x32_bf16 v[106:109], v[144:147], v[206:209], v[106:109]
	v_mfma_f32_16x16x32_bf16 v[102:105], v[174:177], v[206:209], v[102:105]
	s_barrier
	s_setprio 1
	s_waitcnt lgkmcnt(0)
	v_mfma_f32_16x16x32_bf16 v[90:93], v[144:147], v[214:217], v[90:93]
	v_mfma_f32_16x16x32_bf16 v[86:89], v[174:177], v[214:217], v[86:89]
	v_mfma_f32_16x16x32_bf16 v[74:77], v[144:147], v[224:227], v[74:77]
	v_mfma_f32_16x16x32_bf16 v[70:73], v[174:177], v[224:227], v[70:73]
	v_mfma_f32_16x16x32_bf16 v[122:125], v[148:151], v[202:205], v[122:125]
	v_mfma_f32_16x16x32_bf16 v[118:121], v[178:181], v[202:205], v[118:121]
	v_mfma_f32_16x16x32_bf16 v[106:109], v[148:151], v[210:213], v[106:109]
	v_mfma_f32_16x16x32_bf16 v[102:105], v[178:181], v[210:213], v[102:105]
	v_mfma_f32_16x16x32_bf16 v[90:93], v[148:151], v[220:223], v[90:93]
	v_mfma_f32_16x16x32_bf16 v[86:89], v[178:181], v[220:223], v[86:89]
	v_mfma_f32_16x16x32_bf16 v[74:77], v[148:151], v[228:231], v[74:77]
	v_mfma_f32_16x16x32_bf16 v[70:73], v[178:181], v[228:231], v[70:73]
	s_setprio 0
	s_setprio 1
	v_mfma_f32_16x16x32_bf16 v[126:129], v[182:185], v[198:201], v[126:129]
	v_mfma_f32_16x16x32_bf16 v[114:117], v[190:193], v[198:201], v[114:117]
	v_mfma_f32_16x16x32_bf16 v[110:113], v[182:185], v[206:209], v[110:113]
	v_mfma_f32_16x16x32_bf16 v[98:101], v[190:193], v[206:209], v[98:101]
	v_mfma_f32_16x16x32_bf16 v[94:97], v[182:185], v[214:217], v[94:97]
	v_mfma_f32_16x16x32_bf16 v[82:85], v[190:193], v[214:217], v[82:85]
	v_mfma_f32_16x16x32_bf16 v[78:81], v[182:185], v[224:227], v[78:81]
	v_mfma_f32_16x16x32_bf16 v[66:69], v[190:193], v[224:227], v[66:69]
	v_mfma_f32_16x16x32_bf16 v[126:129], v[186:189], v[202:205], v[126:129]
	v_mfma_f32_16x16x32_bf16 v[114:117], v[194:197], v[202:205], v[114:117]
	v_mfma_f32_16x16x32_bf16 v[110:113], v[186:189], v[210:213], v[110:113]
	v_mfma_f32_16x16x32_bf16 v[98:101], v[194:197], v[210:213], v[98:101]
	v_mfma_f32_16x16x32_bf16 v[94:97], v[186:189], v[220:223], v[94:97]
	v_mfma_f32_16x16x32_bf16 v[82:85], v[194:197], v[220:223], v[82:85]
	v_mfma_f32_16x16x32_bf16 v[78:81], v[186:189], v[228:231], v[78:81]
	v_mfma_f32_16x16x32_bf16 v[66:69], v[194:197], v[228:231], v[66:69]
	s_setprio 0
	s_barrier
	v_lshl_add_u64 v[152:153], s[26:27], 0, v[162:163]
	s_add_i32 s26, s94, s86
	s_mov_b32 m0, s26
	ds_read_b128 v[198:201], v172 offset:16384
	ds_read_b128 v[202:205], v172 offset:17408
	ds_read_b128 v[206:209], v172 offset:18432
	ds_read_b128 v[210:213], v172 offset:19456
	ds_read_b128 v[214:217], v172 offset:20480
	ds_read_b128 v[220:223], v172 offset:21504
	ds_read_b128 v[224:227], v172 offset:22528
	ds_read_b128 v[228:231], v172 offset:23552
	global_load_lds_dwordx4 v[152:153], off
	v_lshl_add_u64 v[232:233], v[152:153], 0, s[10:11]
	s_add_i32 m0, s26, 0x2000
	s_add_i32 s26, s95, s86
	global_load_lds_dwordx4 v[232:233], off
	v_lshl_add_u64 v[232:233], v[152:153], 0, s[12:13]
	s_mov_b32 m0, s26
	v_lshl_add_u64 v[234:235], s[82:83], 0, v[132:133]
	global_load_lds_dwordx4 v[232:233], off
	v_lshl_add_u64 v[232:233], v[152:153], 0, s[14:15]
	s_add_i32 m0, s26, 0x2000
	s_nop 0
	global_load_lds_dwordx4 v[232:233], off
	v_lshl_add_u64 v[232:233], s[82:83], 0, v[130:131]
	s_mov_b32 m0, s87
	s_nop 0
	global_load_lds_dwordx4 v[232:233], off
	s_mov_b32 m0, s88
	s_nop 0
	global_load_lds_dwordx4 v[234:235], off
	s_waitcnt vmcnt(8)
	s_waitcnt lgkmcnt(0)
	v_mfma_f32_16x16x32_bf16 v[58:61], v[144:147], v[198:201], v[58:61]
	v_mfma_f32_16x16x32_bf16 v[54:57], v[174:177], v[198:201], v[54:57]
	v_mfma_f32_16x16x32_bf16 v[42:45], v[144:147], v[206:209], v[42:45]
	v_mfma_f32_16x16x32_bf16 v[38:41], v[174:177], v[206:209], v[38:41]
	s_barrier
	s_setprio 1
	s_waitcnt lgkmcnt(0)
	v_mfma_f32_16x16x32_bf16 v[26:29], v[144:147], v[214:217], v[26:29]
	v_mfma_f32_16x16x32_bf16 v[22:25], v[174:177], v[214:217], v[22:25]
	v_mfma_f32_16x16x32_bf16 v[10:13], v[144:147], v[224:227], v[10:13]
	v_mfma_f32_16x16x32_bf16 v[6:9], v[174:177], v[224:227], v[6:9]
	v_mfma_f32_16x16x32_bf16 v[58:61], v[148:151], v[202:205], v[58:61]
	v_mfma_f32_16x16x32_bf16 v[54:57], v[178:181], v[202:205], v[54:57]
	v_mfma_f32_16x16x32_bf16 v[42:45], v[148:151], v[210:213], v[42:45]
	v_mfma_f32_16x16x32_bf16 v[38:41], v[178:181], v[210:213], v[38:41]
	v_mfma_f32_16x16x32_bf16 v[26:29], v[148:151], v[220:223], v[26:29]
	v_mfma_f32_16x16x32_bf16 v[22:25], v[178:181], v[220:223], v[22:25]
	v_mfma_f32_16x16x32_bf16 v[10:13], v[148:151], v[228:231], v[10:13]
	v_mfma_f32_16x16x32_bf16 v[6:9], v[178:181], v[228:231], v[6:9]
	s_setprio 0
	s_setprio 1
	v_mfma_f32_16x16x32_bf16 v[62:65], v[182:185], v[198:201], v[62:65]
	v_mfma_f32_16x16x32_bf16 v[50:53], v[190:193], v[198:201], v[50:53]
	v_mfma_f32_16x16x32_bf16 v[46:49], v[182:185], v[206:209], v[46:49]
	v_mfma_f32_16x16x32_bf16 v[34:37], v[190:193], v[206:209], v[34:37]
	v_mfma_f32_16x16x32_bf16 v[30:33], v[182:185], v[214:217], v[30:33]
	v_mfma_f32_16x16x32_bf16 v[18:21], v[190:193], v[214:217], v[18:21]
	v_mfma_f32_16x16x32_bf16 v[14:17], v[182:185], v[224:227], v[14:17]
	v_mfma_f32_16x16x32_bf16 v[2:5], v[190:193], v[224:227], v[2:5]
	v_mfma_f32_16x16x32_bf16 v[62:65], v[186:189], v[202:205], v[62:65]
	v_mfma_f32_16x16x32_bf16 v[50:53], v[194:197], v[202:205], v[50:53]
	v_mfma_f32_16x16x32_bf16 v[46:49], v[186:189], v[210:213], v[46:49]
	v_mfma_f32_16x16x32_bf16 v[34:37], v[194:197], v[210:213], v[34:37]
	v_mfma_f32_16x16x32_bf16 v[30:33], v[186:189], v[220:223], v[30:33]
	v_mfma_f32_16x16x32_bf16 v[18:21], v[194:197], v[220:223], v[18:21]
	v_mfma_f32_16x16x32_bf16 v[14:17], v[186:189], v[228:231], v[14:17]
	v_mfma_f32_16x16x32_bf16 v[2:5], v[194:197], v[228:231], v[2:5]
	s_setprio 0
	s_barrier
	s_add_i32 s33, 0, 0x18000
	v_add_u32_e32 v136, s33, v167
	s_add_i32 s8, 0, 0x1c000
	ds_read_b128 v[144:147], v136
	ds_read_b128 v[148:151], v136 offset:1024
	ds_read_b128 v[174:177], v136 offset:2048
	ds_read_b128 v[178:181], v136 offset:3072
	v_add_u32_e32 v136, s8, v167
	ds_read_b128 v[182:185], v136
	ds_read_b128 v[186:189], v136 offset:1024
	ds_read_b128 v[190:193], v136 offset:2048
	ds_read_b128 v[194:197], v136 offset:3072
	s_add_u32 s26, s82, 0x80000
	s_addc_u32 s27, s83, 0
	s_mov_b32 m0, s89
	v_lshl_add_u64 v[236:237], s[26:27], 0, v[130:131]
	ds_read_b128 v[198:201], v172 offset:32768
	ds_read_b128 v[202:205], v172 offset:33792
	ds_read_b128 v[206:209], v172 offset:34816
	ds_read_b128 v[210:213], v172 offset:35840
	ds_read_b128 v[214:217], v172 offset:36864
	ds_read_b128 v[220:223], v172 offset:37888
	ds_read_b128 v[224:227], v172 offset:38912
	ds_read_b128 v[228:231], v172 offset:39936
	global_load_lds_dwordx4 v[236:237], off
	v_lshl_add_u64 v[236:237], s[26:27], 0, v[132:133]
	s_mov_b32 m0, s90
	s_nop 0
	global_load_lds_dwordx4 v[236:237], off
	s_waitcnt vmcnt(8)
	s_waitcnt lgkmcnt(0)
	v_mfma_f32_16x16x32_bf16 v[122:125], v[144:147], v[198:201], v[122:125]
	v_mfma_f32_16x16x32_bf16 v[118:121], v[174:177], v[198:201], v[118:121]
	v_mfma_f32_16x16x32_bf16 v[106:109], v[144:147], v[206:209], v[106:109]
	v_mfma_f32_16x16x32_bf16 v[102:105], v[174:177], v[206:209], v[102:105]
	s_barrier
	s_setprio 1
	s_waitcnt lgkmcnt(0)
	v_mfma_f32_16x16x32_bf16 v[90:93], v[144:147], v[214:217], v[90:93]
	v_mfma_f32_16x16x32_bf16 v[86:89], v[174:177], v[214:217], v[86:89]
	v_mfma_f32_16x16x32_bf16 v[74:77], v[144:147], v[224:227], v[74:77]
	v_mfma_f32_16x16x32_bf16 v[70:73], v[174:177], v[224:227], v[70:73]
	v_mfma_f32_16x16x32_bf16 v[122:125], v[148:151], v[202:205], v[122:125]
	v_mfma_f32_16x16x32_bf16 v[118:121], v[178:181], v[202:205], v[118:121]
	v_mfma_f32_16x16x32_bf16 v[106:109], v[148:151], v[210:213], v[106:109]
	v_mfma_f32_16x16x32_bf16 v[102:105], v[178:181], v[210:213], v[102:105]
	v_mfma_f32_16x16x32_bf16 v[90:93], v[148:151], v[220:223], v[90:93]
	v_mfma_f32_16x16x32_bf16 v[86:89], v[178:181], v[220:223], v[86:89]
	v_mfma_f32_16x16x32_bf16 v[74:77], v[148:151], v[228:231], v[74:77]
	v_mfma_f32_16x16x32_bf16 v[70:73], v[178:181], v[228:231], v[70:73]
	s_setprio 0
	s_setprio 1
	v_mfma_f32_16x16x32_bf16 v[126:129], v[182:185], v[198:201], v[126:129]
	v_mfma_f32_16x16x32_bf16 v[114:117], v[190:193], v[198:201], v[114:117]
	v_mfma_f32_16x16x32_bf16 v[110:113], v[182:185], v[206:209], v[110:113]
	v_mfma_f32_16x16x32_bf16 v[98:101], v[190:193], v[206:209], v[98:101]
	v_mfma_f32_16x16x32_bf16 v[94:97], v[182:185], v[214:217], v[94:97]
	v_mfma_f32_16x16x32_bf16 v[82:85], v[190:193], v[214:217], v[82:85]
	v_mfma_f32_16x16x32_bf16 v[78:81], v[182:185], v[224:227], v[78:81]
	v_mfma_f32_16x16x32_bf16 v[66:69], v[190:193], v[224:227], v[66:69]
	v_mfma_f32_16x16x32_bf16 v[126:129], v[186:189], v[202:205], v[126:129]
	v_mfma_f32_16x16x32_bf16 v[114:117], v[194:197], v[202:205], v[114:117]
	v_mfma_f32_16x16x32_bf16 v[110:113], v[186:189], v[210:213], v[110:113]
	v_mfma_f32_16x16x32_bf16 v[98:101], v[194:197], v[210:213], v[98:101]
	v_mfma_f32_16x16x32_bf16 v[94:97], v[186:189], v[220:223], v[94:97]
	v_mfma_f32_16x16x32_bf16 v[82:85], v[194:197], v[220:223], v[82:85]
	v_mfma_f32_16x16x32_bf16 v[78:81], v[186:189], v[228:231], v[78:81]
	v_mfma_f32_16x16x32_bf16 v[66:69], v[194:197], v[228:231], v[66:69]
	s_setprio 0
	s_barrier
	s_add_i32 s9, s33, s86
	v_lshl_add_u64 v[236:237], v[152:153], 0, s[20:21]
	s_mov_b32 m0, s9
	ds_read_b128 v[198:201], v172 offset:49152
	ds_read_b128 v[202:205], v172 offset:50176
	ds_read_b128 v[206:209], v172 offset:51200
	ds_read_b128 v[210:213], v172 offset:52224
	ds_read_b128 v[214:217], v172 offset:53248
	ds_read_b128 v[220:223], v172 offset:54272
	ds_read_b128 v[224:227], v172 offset:55296
	ds_read_b128 v[228:231], v172 offset:56320
	global_load_lds_dwordx4 v[236:237], off
	v_lshl_add_u64 v[236:237], v[152:153], 0, s[22:23]
	s_add_i32 m0, s9, 0x2000
	s_add_i32 s8, s8, s86
	global_load_lds_dwordx4 v[236:237], off
	v_lshl_add_u64 v[236:237], v[152:153], 0, s[40:41]
	s_mov_b32 m0, s8
	v_lshl_add_u64 v[152:153], v[152:153], 0, s[44:45]
	global_load_lds_dwordx4 v[236:237], off
	s_add_i32 m0, s8, 0x2000
	s_nop 0
	global_load_lds_dwordx4 v[152:153], off
	v_lshl_add_u64 v[152:153], v[232:233], 0, s[24:25]
	s_mov_b32 m0, s91
	s_nop 0
	global_load_lds_dwordx4 v[152:153], off
	v_lshl_add_u64 v[152:153], v[234:235], 0, s[24:25]
	s_mov_b32 m0, s92
	s_nop 0
	global_load_lds_dwordx4 v[152:153], off
	s_waitcnt vmcnt(8)
	s_waitcnt lgkmcnt(0)
	v_mfma_f32_16x16x32_bf16 v[58:61], v[144:147], v[198:201], v[58:61]
	v_mfma_f32_16x16x32_bf16 v[54:57], v[174:177], v[198:201], v[54:57]
	v_mfma_f32_16x16x32_bf16 v[42:45], v[144:147], v[206:209], v[42:45]
	v_mfma_f32_16x16x32_bf16 v[38:41], v[174:177], v[206:209], v[38:41]
	s_barrier
	s_setprio 1
	s_waitcnt lgkmcnt(0)
	v_mfma_f32_16x16x32_bf16 v[26:29], v[144:147], v[214:217], v[26:29]
	v_mfma_f32_16x16x32_bf16 v[22:25], v[174:177], v[214:217], v[22:25]
	v_mfma_f32_16x16x32_bf16 v[10:13], v[144:147], v[224:227], v[10:13]
	v_mfma_f32_16x16x32_bf16 v[6:9], v[174:177], v[224:227], v[6:9]
	v_mfma_f32_16x16x32_bf16 v[58:61], v[148:151], v[202:205], v[58:61]
	v_mfma_f32_16x16x32_bf16 v[54:57], v[178:181], v[202:205], v[54:57]
	v_mfma_f32_16x16x32_bf16 v[42:45], v[148:151], v[210:213], v[42:45]
	v_mfma_f32_16x16x32_bf16 v[38:41], v[178:181], v[210:213], v[38:41]
	v_mfma_f32_16x16x32_bf16 v[26:29], v[148:151], v[220:223], v[26:29]
	v_mfma_f32_16x16x32_bf16 v[22:25], v[178:181], v[220:223], v[22:25]
	v_mfma_f32_16x16x32_bf16 v[10:13], v[148:151], v[228:231], v[10:13]
	v_mfma_f32_16x16x32_bf16 v[6:9], v[178:181], v[228:231], v[6:9]
	s_setprio 0
	s_setprio 1
	v_mfma_f32_16x16x32_bf16 v[62:65], v[182:185], v[198:201], v[62:65]
	v_mfma_f32_16x16x32_bf16 v[50:53], v[190:193], v[198:201], v[50:53]
	v_mfma_f32_16x16x32_bf16 v[46:49], v[182:185], v[206:209], v[46:49]
	v_mfma_f32_16x16x32_bf16 v[34:37], v[190:193], v[206:209], v[34:37]
	v_mfma_f32_16x16x32_bf16 v[30:33], v[182:185], v[214:217], v[30:33]
	v_mfma_f32_16x16x32_bf16 v[18:21], v[190:193], v[214:217], v[18:21]
	v_mfma_f32_16x16x32_bf16 v[14:17], v[182:185], v[224:227], v[14:17]
	v_mfma_f32_16x16x32_bf16 v[2:5], v[190:193], v[224:227], v[2:5]
	v_mfma_f32_16x16x32_bf16 v[62:65], v[186:189], v[202:205], v[62:65]
	v_mfma_f32_16x16x32_bf16 v[50:53], v[194:197], v[202:205], v[50:53]
	v_mfma_f32_16x16x32_bf16 v[46:49], v[186:189], v[210:213], v[46:49]
	v_mfma_f32_16x16x32_bf16 v[34:37], v[194:197], v[210:213], v[34:37]
	v_mfma_f32_16x16x32_bf16 v[30:33], v[186:189], v[220:223], v[30:33]
	v_mfma_f32_16x16x32_bf16 v[18:21], v[194:197], v[220:223], v[18:21]
	v_mfma_f32_16x16x32_bf16 v[14:17], v[186:189], v[228:231], v[14:17]
	v_mfma_f32_16x16x32_bf16 v[2:5], v[194:197], v[228:231], v[2:5]
	s_setprio 0
	s_barrier
	s_add_i32 vcc_hi, vcc_hi, 2
	s_add_u32 s97, s97, 0x10000
	s_addc_u32 vcc_lo, vcc_lo, 0
	s_add_u32 s80, s80, 0x100
	s_addc_u32 s81, s81, 0
	s_cmp_gt_u32 vcc_hi, 29
	s_cbranch_scc0 .LBB0_261
	s_and_b64 vcc, exec, s[50:51]
	s_cbranch_vccz .LBB0_264
	s_barrier

.LBB0_285:
	ds_read_b128 v[26:29], v1
	ds_read_b128 v[30:33], v1 offset:1024
	ds_read_b128 v[18:21], v1 offset:2048
	ds_read_b128 v[22:25], v1 offset:3072
	ds_read_b128 v[10:13], v185
	ds_read_b128 v[14:17], v185 offset:1024
	ds_read_b128 v[2:5], v185 offset:2048
	ds_read_b128 v[6:9], v185 offset:3072
	s_add_u32 s26, s70, 0xfffc0080
	s_addc_u32 s27, s71, -1
	s_cmp_eq_u32 s94, 12
	s_cselect_b32 s73, s51, s27
	s_cselect_b32 s72, s90, s26
	s_cselect_b32 s75, s45, s93
	s_cselect_b32 s74, s91, s92
	v_lshl_add_u64 v[176:177], s[70:71], 0, v[168:169]
	s_add_i32 m0, s33, 0xc000
	ds_read_b128 v[190:193], v186
	ds_read_b128 v[194:197], v186 offset:1024
	ds_read_b128 v[198:201], v186 offset:2048
	ds_read_b128 v[202:205], v186 offset:3072
	ds_read_b128 v[206:209], v186 offset:4096
	ds_read_b128 v[210:213], v186 offset:5120
	ds_read_b128 v[220:223], v186 offset:6144
	ds_read_b128 v[224:227], v186 offset:7168
	global_load_lds_dwordx4 v[176:177], off
	v_lshl_add_u64 v[176:177], s[70:71], 0, v[170:171]
	s_add_i32 m0, s33, 0xe000
	s_nop 0
	global_load_lds_dwordx4 v[176:177], off
	s_waitcnt vmcnt(8)
	s_waitcnt lgkmcnt(0)
	v_mfma_scale_f32_16x16x128_f8f6f4 v[158:161], v[26:33], v[190:197], v[158:161], v187, v188 op_sel_hi:[0,0,0]
	v_mfma_scale_f32_16x16x128_f8f6f4 v[154:157], v[18:25], v[190:197], v[154:157], v187, v188 op_sel_hi:[0,0,0]
	s_barrier
	s_setprio 1
	s_waitcnt lgkmcnt(0)
	v_mfma_scale_f32_16x16x128_f8f6f4 v[150:153], v[26:33], v[198:205], v[150:153], v187, v188 op_sel_hi:[0,0,0]
	v_mfma_scale_f32_16x16x128_f8f6f4 v[142:145], v[18:25], v[198:205], v[142:145], v187, v188 op_sel_hi:[0,0,0]
	v_mfma_scale_f32_16x16x128_f8f6f4 v[134:137], v[26:33], v[206:213], v[134:137], v187, v188 op_sel_hi:[0,0,0]
	v_mfma_scale_f32_16x16x128_f8f6f4 v[126:129], v[18:25], v[206:213], v[126:129], v187, v188 op_sel_hi:[0,0,0]
	v_mfma_scale_f32_16x16x128_f8f6f4 v[118:121], v[26:33], v[220:227], v[118:121], v187, v188 op_sel_hi:[0,0,0]
	v_mfma_scale_f32_16x16x128_f8f6f4 v[110:113], v[18:25], v[220:227], v[110:113], v187, v188 op_sel_hi:[0,0,0]
	s_setprio 0
	s_setprio 1
	v_mfma_scale_f32_16x16x128_f8f6f4 v[146:149], v[10:17], v[190:197], v[146:149], v187, v188 op_sel_hi:[0,0,0]
	v_mfma_scale_f32_16x16x128_f8f6f4 v[138:141], v[2:9], v[190:197], v[138:141], v187, v188 op_sel_hi:[0,0,0]
	v_mfma_scale_f32_16x16x128_f8f6f4 v[130:133], v[10:17], v[198:205], v[130:133], v187, v188 op_sel_hi:[0,0,0]
	v_mfma_scale_f32_16x16x128_f8f6f4 v[122:125], v[2:9], v[198:205], v[122:125], v187, v188 op_sel_hi:[0,0,0]
	v_mfma_scale_f32_16x16x128_f8f6f4 v[114:117], v[10:17], v[206:213], v[114:117], v187, v188 op_sel_hi:[0,0,0]
	v_mfma_scale_f32_16x16x128_f8f6f4 v[106:109], v[2:9], v[206:213], v[106:109], v187, v188 op_sel_hi:[0,0,0]
	v_mfma_scale_f32_16x16x128_f8f6f4 v[102:105], v[10:17], v[220:227], v[102:105], v187, v188 op_sel_hi:[0,0,0]
	v_mfma_scale_f32_16x16x128_f8f6f4 v[98:101], v[2:9], v[220:227], v[98:101], v187, v188 op_sel_hi:[0,0,0]
	s_setprio 0
	s_barrier
	s_add_i32 s26, s88, s80
	v_lshl_add_u64 v[176:177], s[74:75], 0, v[162:163]
	s_mov_b32 m0, s26
	ds_read_b128 v[190:193], v186 offset:16384
	ds_read_b128 v[194:197], v186 offset:17408
	ds_read_b128 v[198:201], v186 offset:18432
	ds_read_b128 v[202:205], v186 offset:19456
	ds_read_b128 v[206:209], v186 offset:20480
	ds_read_b128 v[210:213], v186 offset:21504
	ds_read_b128 v[220:223], v186 offset:22528
	ds_read_b128 v[224:227], v186 offset:23552
	global_load_lds_dwordx4 v[176:177], off
	v_lshl_add_u64 v[178:179], v[176:177], 0, s[8:9]
	s_add_i32 m0, s26, 0x2000
	s_add_i32 s26, s89, s80
	global_load_lds_dwordx4 v[178:179], off
	v_lshl_add_u64 v[178:179], v[176:177], 0, s[10:11]
	s_mov_b32 m0, s26
	v_lshl_add_u64 v[180:181], s[72:73], 0, v[166:167]
	global_load_lds_dwordx4 v[178:179], off
	v_lshl_add_u64 v[178:179], v[176:177], 0, s[12:13]
	s_add_i32 m0, s26, 0x2000
	s_nop 0
	global_load_lds_dwordx4 v[178:179], off
	v_lshl_add_u64 v[178:179], s[72:73], 0, v[164:165]
	s_mov_b32 m0, s33
	s_nop 0
	global_load_lds_dwordx4 v[178:179], off
	s_mov_b32 m0, s69
	s_nop 0
	global_load_lds_dwordx4 v[180:181], off
	s_waitcnt vmcnt(8)
	s_waitcnt lgkmcnt(0)
	v_mfma_scale_f32_16x16x128_f8f6f4 v[94:97], v[26:33], v[190:197], v[94:97], v187, v188 op_sel_hi:[0,0,0]
	v_mfma_scale_f32_16x16x128_f8f6f4 v[90:93], v[18:25], v[190:197], v[90:93], v187, v188 op_sel_hi:[0,0,0]
	s_barrier
	s_setprio 1
	s_waitcnt lgkmcnt(0)
	v_mfma_scale_f32_16x16x128_f8f6f4 v[86:89], v[26:33], v[198:205], v[86:89], v187, v188 op_sel_hi:[0,0,0]
	v_mfma_scale_f32_16x16x128_f8f6f4 v[78:81], v[18:25], v[198:205], v[78:81], v187, v188 op_sel_hi:[0,0,0]
	v_mfma_scale_f32_16x16x128_f8f6f4 v[70:73], v[26:33], v[206:213], v[70:73], v187, v188 op_sel_hi:[0,0,0]
	v_mfma_scale_f32_16x16x128_f8f6f4 v[62:65], v[18:25], v[206:213], v[62:65], v187, v188 op_sel_hi:[0,0,0]
	v_mfma_scale_f32_16x16x128_f8f6f4 v[54:57], v[26:33], v[220:227], v[54:57], v187, v188 op_sel_hi:[0,0,0]
	v_mfma_scale_f32_16x16x128_f8f6f4 v[46:49], v[18:25], v[220:227], v[46:49], v187, v188 op_sel_hi:[0,0,0]
	s_setprio 0
	s_setprio 1
	v_mfma_scale_f32_16x16x128_f8f6f4 v[82:85], v[10:17], v[190:197], v[82:85], v187, v188 op_sel_hi:[0,0,0]
	v_mfma_scale_f32_16x16x128_f8f6f4 v[74:77], v[2:9], v[190:197], v[74:77], v187, v188 op_sel_hi:[0,0,0]
	v_mfma_scale_f32_16x16x128_f8f6f4 v[66:69], v[10:17], v[198:205], v[66:69], v187, v188 op_sel_hi:[0,0,0]
	v_mfma_scale_f32_16x16x128_f8f6f4 v[58:61], v[2:9], v[198:205], v[58:61], v187, v188 op_sel_hi:[0,0,0]
	v_mfma_scale_f32_16x16x128_f8f6f4 v[50:53], v[10:17], v[206:213], v[50:53], v187, v188 op_sel_hi:[0,0,0]
	v_mfma_scale_f32_16x16x128_f8f6f4 v[42:45], v[2:9], v[206:213], v[42:45], v187, v188 op_sel_hi:[0,0,0]
	v_mfma_scale_f32_16x16x128_f8f6f4 v[38:41], v[10:17], v[220:227], v[38:41], v187, v188 op_sel_hi:[0,0,0]
	v_mfma_scale_f32_16x16x128_f8f6f4 v[34:37], v[2:9], v[220:227], v[34:37], v187, v188 op_sel_hi:[0,0,0]
	s_setprio 0
	s_barrier
	s_add_i32 s74, 0, 0x18000
	s_add_i32 s75, 0, 0x1c000
	v_add_u32_e32 v14, s74, v183
	v_add_u32_e32 v30, s75, v183
	ds_read_b128 v[2:5], v14
	ds_read_b128 v[6:9], v14 offset:1024
	ds_read_b128 v[10:13], v14 offset:2048
	ds_read_b128 v[14:17], v14 offset:3072
	ds_read_b128 v[18:21], v30
	ds_read_b128 v[22:25], v30 offset:1024
	ds_read_b128 v[26:29], v30 offset:2048
	ds_read_b128 v[30:33], v30 offset:3072
	s_add_u32 s26, s72, 0x40000
	s_addc_u32 s27, s73, 0
	s_mov_b32 m0, s83
	v_lshl_add_u64 v[214:215], s[26:27], 0, v[164:165]
	ds_read_b128 v[190:193], v186 offset:32768
	ds_read_b128 v[194:197], v186 offset:33792
	ds_read_b128 v[198:201], v186 offset:34816
	ds_read_b128 v[202:205], v186 offset:35840
	ds_read_b128 v[206:209], v186 offset:36864
	ds_read_b128 v[210:213], v186 offset:37888
	ds_read_b128 v[220:223], v186 offset:38912
	ds_read_b128 v[224:227], v186 offset:39936
	global_load_lds_dwordx4 v[214:215], off
	v_lshl_add_u64 v[214:215], s[26:27], 0, v[166:167]
	s_mov_b32 m0, s84
	s_nop 0
	global_load_lds_dwordx4 v[214:215], off
	s_waitcnt vmcnt(8)
	s_waitcnt lgkmcnt(0)
	v_mfma_scale_f32_16x16x128_f8f6f4 v[158:161], v[2:9], v[190:197], v[158:161], v187, v188 op_sel_hi:[0,0,0]
	v_mfma_scale_f32_16x16x128_f8f6f4 v[154:157], v[10:17], v[190:197], v[154:157], v187, v188 op_sel_hi:[0,0,0]
	s_barrier
	s_setprio 1
	s_waitcnt lgkmcnt(0)
	v_mfma_scale_f32_16x16x128_f8f6f4 v[150:153], v[2:9], v[198:205], v[150:153], v187, v188 op_sel_hi:[0,0,0]
	v_mfma_scale_f32_16x16x128_f8f6f4 v[142:145], v[10:17], v[198:205], v[142:145], v187, v188 op_sel_hi:[0,0,0]
	v_mfma_scale_f32_16x16x128_f8f6f4 v[134:137], v[2:9], v[206:213], v[134:137], v187, v188 op_sel_hi:[0,0,0]
	v_mfma_scale_f32_16x16x128_f8f6f4 v[126:129], v[10:17], v[206:213], v[126:129], v187, v188 op_sel_hi:[0,0,0]
	v_mfma_scale_f32_16x16x128_f8f6f4 v[118:121], v[2:9], v[220:227], v[118:121], v187, v188 op_sel_hi:[0,0,0]
	v_mfma_scale_f32_16x16x128_f8f6f4 v[110:113], v[10:17], v[220:227], v[110:113], v187, v188 op_sel_hi:[0,0,0]
	s_setprio 0
	s_setprio 1
	v_mfma_scale_f32_16x16x128_f8f6f4 v[146:149], v[18:25], v[190:197], v[146:149], v187, v188 op_sel_hi:[0,0,0]
	v_mfma_scale_f32_16x16x128_f8f6f4 v[138:141], v[26:33], v[190:197], v[138:141], v187, v188 op_sel_hi:[0,0,0]
	v_mfma_scale_f32_16x16x128_f8f6f4 v[130:133], v[18:25], v[198:205], v[130:133], v187, v188 op_sel_hi:[0,0,0]
	v_mfma_scale_f32_16x16x128_f8f6f4 v[122:125], v[26:33], v[198:205], v[122:125], v187, v188 op_sel_hi:[0,0,0]
	v_mfma_scale_f32_16x16x128_f8f6f4 v[114:117], v[18:25], v[206:213], v[114:117], v187, v188 op_sel_hi:[0,0,0]
	v_mfma_scale_f32_16x16x128_f8f6f4 v[106:109], v[26:33], v[206:213], v[106:109], v187, v188 op_sel_hi:[0,0,0]
	v_mfma_scale_f32_16x16x128_f8f6f4 v[102:105], v[18:25], v[220:227], v[102:105], v187, v188 op_sel_hi:[0,0,0]
	v_mfma_scale_f32_16x16x128_f8f6f4 v[98:101], v[26:33], v[220:227], v[98:101], v187, v188 op_sel_hi:[0,0,0]
	s_setprio 0
	s_barrier
	s_add_i32 s26, s74, s80
	v_lshl_add_u64 v[214:215], v[176:177], 0, s[16:17]
	s_mov_b32 m0, s26
	ds_read_b128 v[190:193], v186 offset:49152
	ds_read_b128 v[194:197], v186 offset:50176
	ds_read_b128 v[198:201], v186 offset:51200
	ds_read_b128 v[202:205], v186 offset:52224
	ds_read_b128 v[206:209], v186 offset:53248
	ds_read_b128 v[210:213], v186 offset:54272
	ds_read_b128 v[220:223], v186 offset:55296
	ds_read_b128 v[224:227], v186 offset:56320
	global_load_lds_dwordx4 v[214:215], off
	v_lshl_add_u64 v[214:215], v[176:177], 0, s[18:19]
	s_add_i32 m0, s26, 0x2000
	s_add_i32 s26, s75, s80
	global_load_lds_dwordx4 v[214:215], off
	v_lshl_add_u64 v[214:215], v[176:177], 0, s[22:23]
	s_mov_b32 m0, s26
	v_lshl_add_u64 v[176:177], v[176:177], 0, s[24:25]
	global_load_lds_dwordx4 v[214:215], off
	s_add_i32 m0, s26, 0x2000
	s_nop 0
	global_load_lds_dwordx4 v[176:177], off
	v_lshl_add_u64 v[176:177], v[178:179], 0, s[20:21]
	s_mov_b32 m0, s86
	s_nop 0
	global_load_lds_dwordx4 v[176:177], off
	v_lshl_add_u64 v[176:177], v[180:181], 0, s[20:21]
	s_mov_b32 m0, s87
	s_nop 0
	global_load_lds_dwordx4 v[176:177], off
	s_waitcnt vmcnt(8)
	s_waitcnt lgkmcnt(0)
	v_mfma_scale_f32_16x16x128_f8f6f4 v[94:97], v[2:9], v[190:197], v[94:97], v187, v188 op_sel_hi:[0,0,0]
	v_mfma_scale_f32_16x16x128_f8f6f4 v[90:93], v[10:17], v[190:197], v[90:93], v187, v188 op_sel_hi:[0,0,0]
	s_barrier
	s_setprio 1
	s_waitcnt lgkmcnt(0)
	v_mfma_scale_f32_16x16x128_f8f6f4 v[86:89], v[2:9], v[198:205], v[86:89], v187, v188 op_sel_hi:[0,0,0]
	v_mfma_scale_f32_16x16x128_f8f6f4 v[78:81], v[10:17], v[198:205], v[78:81], v187, v188 op_sel_hi:[0,0,0]
	v_mfma_scale_f32_16x16x128_f8f6f4 v[70:73], v[2:9], v[206:213], v[70:73], v187, v188 op_sel_hi:[0,0,0]
	v_mfma_scale_f32_16x16x128_f8f6f4 v[62:65], v[10:17], v[206:213], v[62:65], v187, v188 op_sel_hi:[0,0,0]
	v_mfma_scale_f32_16x16x128_f8f6f4 v[54:57], v[2:9], v[220:227], v[54:57], v187, v188 op_sel_hi:[0,0,0]
	v_mfma_scale_f32_16x16x128_f8f6f4 v[46:49], v[10:17], v[220:227], v[46:49], v187, v188 op_sel_hi:[0,0,0]
	s_setprio 0
	s_setprio 1
	v_mfma_scale_f32_16x16x128_f8f6f4 v[82:85], v[18:25], v[190:197], v[82:85], v187, v188 op_sel_hi:[0,0,0]
	v_mfma_scale_f32_16x16x128_f8f6f4 v[74:77], v[26:33], v[190:197], v[74:77], v187, v188 op_sel_hi:[0,0,0]
	v_mfma_scale_f32_16x16x128_f8f6f4 v[66:69], v[18:25], v[198:205], v[66:69], v187, v188 op_sel_hi:[0,0,0]
	v_mfma_scale_f32_16x16x128_f8f6f4 v[58:61], v[26:33], v[198:205], v[58:61], v187, v188 op_sel_hi:[0,0,0]
	v_mfma_scale_f32_16x16x128_f8f6f4 v[50:53], v[18:25], v[206:213], v[50:53], v187, v188 op_sel_hi:[0,0,0]
	v_mfma_scale_f32_16x16x128_f8f6f4 v[42:45], v[26:33], v[206:213], v[42:45], v187, v188 op_sel_hi:[0,0,0]
	v_mfma_scale_f32_16x16x128_f8f6f4 v[38:41], v[18:25], v[220:227], v[38:41], v187, v188 op_sel_hi:[0,0,0]
	v_mfma_scale_f32_16x16x128_f8f6f4 v[34:37], v[26:33], v[220:227], v[34:37], v187, v188 op_sel_hi:[0,0,0]
	s_setprio 0
	s_barrier
	s_add_i32 s94, s94, 2
	s_add_u32 s92, s92, 0x10000
	s_addc_u32 s93, s93, 0
	s_add_u32 s70, s70, 0x100
	s_addc_u32 s71, s71, 0
	s_cmp_gt_u32 s94, 13
	s_cbranch_scc0 .LBB0_285
	s_and_b64 vcc, exec, s[40:41]
	s_cbranch_vccz .LBB0_288
	s_barrier

.LBB0_660:
	ds_read_b128 v[130:133], v222
	ds_read_b128 v[134:137], v222 offset:1024
	ds_read_b128 v[138:141], v222 offset:2048
	ds_read_b128 v[142:145], v222 offset:3072
	ds_read_b128 v[146:149], v223
	ds_read_b128 v[150:153], v223 offset:1024
	ds_read_b128 v[154:157], v223 offset:2048
	ds_read_b128 v[158:161], v223 offset:3072
	s_add_u32 s26, s58, 0xfff80080
	s_addc_u32 s27, s59, -1
	s_cmp_eq_u32 s80, 28
	s_cselect_b32 s61, s45, s27
	s_cselect_b32 s60, s72, s26
	s_cselect_b32 s27, s41, s75
	s_cselect_b32 s26, s73, s74
	v_lshl_add_u64 v[208:209], s[58:59], 0, v[200:201]
	s_add_i32 m0, s57, 0xc000
	ds_read_b128 v[162:165], v224
	ds_read_b128 v[166:169], v224 offset:1024
	ds_read_b128 v[170:173], v224 offset:2048
	ds_read_b128 v[174:177], v224 offset:3072
	ds_read_b128 v[178:181], v224 offset:4096
	ds_read_b128 v[182:185], v224 offset:5120
	ds_read_b128 v[186:189], v224 offset:6144
	ds_read_b128 v[190:193], v224 offset:7168
	global_load_lds_dwordx4 v[208:209], off
	v_lshl_add_u64 v[208:209], s[58:59], 0, v[202:203]
	s_add_i32 m0, s57, 0xe000
	s_nop 0
	global_load_lds_dwordx4 v[208:209], off
	s_waitcnt vmcnt(8)
	s_waitcnt lgkmcnt(0)
	v_mfma_f32_16x16x32_bf16 v[126:129], v[130:133], v[162:165], v[126:129]
	v_mfma_f32_16x16x32_bf16 v[122:125], v[138:141], v[162:165], v[122:125]
	v_mfma_f32_16x16x32_bf16 v[118:121], v[130:133], v[170:173], v[118:121]
	v_mfma_f32_16x16x32_bf16 v[114:117], v[138:141], v[170:173], v[114:117]
	s_barrier
	s_setprio 1
	s_waitcnt lgkmcnt(0)
	v_mfma_f32_16x16x32_bf16 v[110:113], v[130:133], v[178:181], v[110:113]
	v_mfma_f32_16x16x32_bf16 v[102:105], v[138:141], v[178:181], v[102:105]
	v_mfma_f32_16x16x32_bf16 v[94:97], v[130:133], v[186:189], v[94:97]
	v_mfma_f32_16x16x32_bf16 v[74:77], v[138:141], v[186:189], v[74:77]
	v_mfma_f32_16x16x32_bf16 v[126:129], v[134:137], v[166:169], v[126:129]
	v_mfma_f32_16x16x32_bf16 v[122:125], v[142:145], v[166:169], v[122:125]
	v_mfma_f32_16x16x32_bf16 v[118:121], v[134:137], v[174:177], v[118:121]
	v_mfma_f32_16x16x32_bf16 v[114:117], v[142:145], v[174:177], v[114:117]
	v_mfma_f32_16x16x32_bf16 v[110:113], v[134:137], v[182:185], v[110:113]
	v_mfma_f32_16x16x32_bf16 v[102:105], v[142:145], v[182:185], v[102:105]
	v_mfma_f32_16x16x32_bf16 v[94:97], v[134:137], v[190:193], v[94:97]
	v_mfma_f32_16x16x32_bf16 v[74:77], v[142:145], v[190:193], v[74:77]
	s_setprio 0
	s_setprio 1
	v_mfma_f32_16x16x32_bf16 v[106:109], v[146:149], v[162:165], v[106:109]
	v_mfma_f32_16x16x32_bf16 v[98:101], v[154:157], v[162:165], v[98:101]
	v_mfma_f32_16x16x32_bf16 v[90:93], v[146:149], v[170:173], v[90:93]
	v_mfma_f32_16x16x32_bf16 v[86:89], v[154:157], v[170:173], v[86:89]
	v_mfma_f32_16x16x32_bf16 v[82:85], v[146:149], v[178:181], v[82:85]
	v_mfma_f32_16x16x32_bf16 v[78:81], v[154:157], v[178:181], v[78:81]
	v_mfma_f32_16x16x32_bf16 v[70:73], v[146:149], v[186:189], v[70:73]
	v_mfma_f32_16x16x32_bf16 v[66:69], v[154:157], v[186:189], v[66:69]
	v_mfma_f32_16x16x32_bf16 v[106:109], v[150:153], v[166:169], v[106:109]
	v_mfma_f32_16x16x32_bf16 v[98:101], v[158:161], v[166:169], v[98:101]
	v_mfma_f32_16x16x32_bf16 v[90:93], v[150:153], v[174:177], v[90:93]
	v_mfma_f32_16x16x32_bf16 v[86:89], v[158:161], v[174:177], v[86:89]
	v_mfma_f32_16x16x32_bf16 v[82:85], v[150:153], v[182:185], v[82:85]
	v_mfma_f32_16x16x32_bf16 v[78:81], v[158:161], v[182:185], v[78:81]
	v_mfma_f32_16x16x32_bf16 v[70:73], v[150:153], v[190:193], v[70:73]
	v_mfma_f32_16x16x32_bf16 v[66:69], v[158:161], v[190:193], v[66:69]
	s_setprio 0
	s_barrier
	v_lshl_add_u64 v[208:209], s[26:27], 0, v[194:195]
	s_add_i32 s26, s70, s35
	s_mov_b32 m0, s26
	ds_read_b128 v[162:165], v224 offset:16384
	ds_read_b128 v[166:169], v224 offset:17408
	ds_read_b128 v[170:173], v224 offset:18432
	ds_read_b128 v[174:177], v224 offset:19456
	ds_read_b128 v[178:181], v224 offset:20480
	ds_read_b128 v[182:185], v224 offset:21504
	ds_read_b128 v[186:189], v224 offset:22528
	ds_read_b128 v[190:193], v224 offset:23552
	global_load_lds_dwordx4 v[208:209], off
	v_lshl_add_u64 v[210:211], v[208:209], 0, s[6:7]
	s_add_i32 m0, s26, 0x2000
	s_add_i32 s26, s71, s35
	global_load_lds_dwordx4 v[210:211], off
	v_lshl_add_u64 v[210:211], v[208:209], 0, s[8:9]
	s_mov_b32 m0, s26
	v_lshl_add_u64 v[212:213], s[60:61], 0, v[198:199]
	global_load_lds_dwordx4 v[210:211], off
	v_lshl_add_u64 v[210:211], v[208:209], 0, s[10:11]
	s_add_i32 m0, s26, 0x2000
	s_nop 0
	global_load_lds_dwordx4 v[210:211], off
	v_lshl_add_u64 v[210:211], s[60:61], 0, v[196:197]
	s_mov_b32 m0, s57
	s_nop 0
	global_load_lds_dwordx4 v[210:211], off
	s_mov_b32 m0, s63
	s_nop 0
	global_load_lds_dwordx4 v[212:213], off
	s_waitcnt vmcnt(8)
	s_waitcnt lgkmcnt(0)
	v_mfma_f32_16x16x32_bf16 v[62:65], v[130:133], v[162:165], v[62:65]
	v_mfma_f32_16x16x32_bf16 v[58:61], v[138:141], v[162:165], v[58:61]
	v_mfma_f32_16x16x32_bf16 v[54:57], v[130:133], v[170:173], v[54:57]
	v_mfma_f32_16x16x32_bf16 v[50:53], v[138:141], v[170:173], v[50:53]
	s_barrier
	s_setprio 1
	s_waitcnt lgkmcnt(0)
	v_mfma_f32_16x16x32_bf16 v[46:49], v[130:133], v[178:181], v[46:49]
	v_mfma_f32_16x16x32_bf16 v[38:41], v[138:141], v[178:181], v[38:41]
	v_mfma_f32_16x16x32_bf16 v[30:33], v[130:133], v[186:189], v[30:33]
	v_mfma_f32_16x16x32_bf16 v[10:13], v[138:141], v[186:189], v[10:13]
	v_mfma_f32_16x16x32_bf16 v[62:65], v[134:137], v[166:169], v[62:65]
	v_mfma_f32_16x16x32_bf16 v[58:61], v[142:145], v[166:169], v[58:61]
	v_mfma_f32_16x16x32_bf16 v[54:57], v[134:137], v[174:177], v[54:57]
	v_mfma_f32_16x16x32_bf16 v[50:53], v[142:145], v[174:177], v[50:53]
	v_mfma_f32_16x16x32_bf16 v[46:49], v[134:137], v[182:185], v[46:49]
	v_mfma_f32_16x16x32_bf16 v[38:41], v[142:145], v[182:185], v[38:41]
	v_mfma_f32_16x16x32_bf16 v[30:33], v[134:137], v[190:193], v[30:33]
	v_mfma_f32_16x16x32_bf16 v[10:13], v[142:145], v[190:193], v[10:13]
	s_setprio 0
	s_setprio 1
	v_mfma_f32_16x16x32_bf16 v[42:45], v[146:149], v[162:165], v[42:45]
	v_mfma_f32_16x16x32_bf16 v[34:37], v[154:157], v[162:165], v[34:37]
	v_mfma_f32_16x16x32_bf16 v[26:29], v[146:149], v[170:173], v[26:29]
	v_mfma_f32_16x16x32_bf16 v[22:25], v[154:157], v[170:173], v[22:25]
	v_mfma_f32_16x16x32_bf16 v[18:21], v[146:149], v[178:181], v[18:21]
	v_mfma_f32_16x16x32_bf16 v[14:17], v[154:157], v[178:181], v[14:17]
	v_mfma_f32_16x16x32_bf16 v[6:9], v[146:149], v[186:189], v[6:9]
	v_mfma_f32_16x16x32_bf16 v[2:5], v[154:157], v[186:189], v[2:5]
	v_mfma_f32_16x16x32_bf16 v[42:45], v[150:153], v[166:169], v[42:45]
	v_mfma_f32_16x16x32_bf16 v[34:37], v[158:161], v[166:169], v[34:37]
	v_mfma_f32_16x16x32_bf16 v[26:29], v[150:153], v[174:177], v[26:29]
	v_mfma_f32_16x16x32_bf16 v[22:25], v[158:161], v[174:177], v[22:25]
	v_mfma_f32_16x16x32_bf16 v[18:21], v[150:153], v[182:185], v[18:21]
	v_mfma_f32_16x16x32_bf16 v[14:17], v[158:161], v[182:185], v[14:17]
	v_mfma_f32_16x16x32_bf16 v[6:9], v[150:153], v[190:193], v[6:9]
	v_mfma_f32_16x16x32_bf16 v[2:5], v[158:161], v[190:193], v[2:5]
	s_setprio 0
	s_barrier
	s_add_i32 s81, 0, 0x18000
	s_add_i32 s82, 0, 0x1c000
	v_add_u32_e32 v142, s81, v220
	v_add_u32_e32 v158, s82, v220
	ds_read_b128 v[130:133], v142
	ds_read_b128 v[134:137], v142 offset:1024
	ds_read_b128 v[138:141], v142 offset:2048
	ds_read_b128 v[142:145], v142 offset:3072
	ds_read_b128 v[146:149], v158
	ds_read_b128 v[150:153], v158 offset:1024
	ds_read_b128 v[154:157], v158 offset:2048
	ds_read_b128 v[158:161], v158 offset:3072
	s_add_u32 s26, s60, 0x80000
	s_addc_u32 s27, s61, 0
	s_mov_b32 m0, s64
	v_lshl_add_u64 v[214:215], s[26:27], 0, v[196:197]
	ds_read_b128 v[162:165], v224 offset:32768
	ds_read_b128 v[166:169], v224 offset:33792
	ds_read_b128 v[170:173], v224 offset:34816
	ds_read_b128 v[174:177], v224 offset:35840
	ds_read_b128 v[178:181], v224 offset:36864
	ds_read_b128 v[182:185], v224 offset:37888
	ds_read_b128 v[186:189], v224 offset:38912
	ds_read_b128 v[190:193], v224 offset:39936
	global_load_lds_dwordx4 v[214:215], off
	v_lshl_add_u64 v[214:215], s[26:27], 0, v[198:199]
	s_mov_b32 m0, s65
	s_nop 0
	global_load_lds_dwordx4 v[214:215], off
	s_waitcnt vmcnt(8)
	s_waitcnt lgkmcnt(0)
	v_mfma_f32_16x16x32_bf16 v[126:129], v[130:133], v[162:165], v[126:129]
	v_mfma_f32_16x16x32_bf16 v[122:125], v[138:141], v[162:165], v[122:125]
	v_mfma_f32_16x16x32_bf16 v[118:121], v[130:133], v[170:173], v[118:121]
	v_mfma_f32_16x16x32_bf16 v[114:117], v[138:141], v[170:173], v[114:117]
	s_barrier
	s_setprio 1
	s_waitcnt lgkmcnt(0)
	v_mfma_f32_16x16x32_bf16 v[110:113], v[130:133], v[178:181], v[110:113]
	v_mfma_f32_16x16x32_bf16 v[102:105], v[138:141], v[178:181], v[102:105]
	v_mfma_f32_16x16x32_bf16 v[94:97], v[130:133], v[186:189], v[94:97]
	v_mfma_f32_16x16x32_bf16 v[74:77], v[138:141], v[186:189], v[74:77]
	v_mfma_f32_16x16x32_bf16 v[126:129], v[134:137], v[166:169], v[126:129]
	v_mfma_f32_16x16x32_bf16 v[122:125], v[142:145], v[166:169], v[122:125]
	v_mfma_f32_16x16x32_bf16 v[118:121], v[134:137], v[174:177], v[118:121]
	v_mfma_f32_16x16x32_bf16 v[114:117], v[142:145], v[174:177], v[114:117]
	v_mfma_f32_16x16x32_bf16 v[110:113], v[134:137], v[182:185], v[110:113]
	v_mfma_f32_16x16x32_bf16 v[102:105], v[142:145], v[182:185], v[102:105]
	v_mfma_f32_16x16x32_bf16 v[94:97], v[134:137], v[190:193], v[94:97]
	v_mfma_f32_16x16x32_bf16 v[74:77], v[142:145], v[190:193], v[74:77]
	s_setprio 0
	s_setprio 1
	v_mfma_f32_16x16x32_bf16 v[106:109], v[146:149], v[162:165], v[106:109]
	v_mfma_f32_16x16x32_bf16 v[98:101], v[154:157], v[162:165], v[98:101]
	v_mfma_f32_16x16x32_bf16 v[90:93], v[146:149], v[170:173], v[90:93]
	v_mfma_f32_16x16x32_bf16 v[86:89], v[154:157], v[170:173], v[86:89]
	v_mfma_f32_16x16x32_bf16 v[82:85], v[146:149], v[178:181], v[82:85]
	v_mfma_f32_16x16x32_bf16 v[78:81], v[154:157], v[178:181], v[78:81]
	v_mfma_f32_16x16x32_bf16 v[70:73], v[146:149], v[186:189], v[70:73]
	v_mfma_f32_16x16x32_bf16 v[66:69], v[154:157], v[186:189], v[66:69]
	v_mfma_f32_16x16x32_bf16 v[106:109], v[150:153], v[166:169], v[106:109]
	v_mfma_f32_16x16x32_bf16 v[98:101], v[158:161], v[166:169], v[98:101]
	v_mfma_f32_16x16x32_bf16 v[90:93], v[150:153], v[174:177], v[90:93]
	v_mfma_f32_16x16x32_bf16 v[86:89], v[158:161], v[174:177], v[86:89]
	v_mfma_f32_16x16x32_bf16 v[82:85], v[150:153], v[182:185], v[82:85]
	v_mfma_f32_16x16x32_bf16 v[78:81], v[158:161], v[182:185], v[78:81]
	v_mfma_f32_16x16x32_bf16 v[70:73], v[150:153], v[190:193], v[70:73]
	v_mfma_f32_16x16x32_bf16 v[66:69], v[158:161], v[190:193], v[66:69]
	s_setprio 0
	s_barrier
	s_add_i32 s26, s81, s35
	v_lshl_add_u64 v[214:215], v[208:209], 0, s[14:15]
	s_mov_b32 m0, s26
	ds_read_b128 v[162:165], v224 offset:49152
	ds_read_b128 v[166:169], v224 offset:50176
	ds_read_b128 v[170:173], v224 offset:51200
	ds_read_b128 v[174:177], v224 offset:52224
	ds_read_b128 v[178:181], v224 offset:53248
	ds_read_b128 v[182:185], v224 offset:54272
	ds_read_b128 v[186:189], v224 offset:55296
	ds_read_b128 v[190:193], v224 offset:56320
	global_load_lds_dwordx4 v[214:215], off
	v_lshl_add_u64 v[214:215], v[208:209], 0, s[16:17]
	s_add_i32 m0, s26, 0x2000
	s_add_i32 s26, s82, s35
	global_load_lds_dwordx4 v[214:215], off
	v_lshl_add_u64 v[214:215], v[208:209], 0, s[20:21]
	s_mov_b32 m0, s26
	v_lshl_add_u64 v[208:209], v[208:209], 0, s[22:23]
	global_load_lds_dwordx4 v[214:215], off
	s_add_i32 m0, s26, 0x2000
	s_nop 0
	global_load_lds_dwordx4 v[208:209], off
	v_lshl_add_u64 v[208:209], v[210:211], 0, s[18:19]
	s_mov_b32 m0, s67
	s_nop 0
	global_load_lds_dwordx4 v[208:209], off
	v_lshl_add_u64 v[208:209], v[212:213], 0, s[18:19]
	s_mov_b32 m0, s68
	s_nop 0
	global_load_lds_dwordx4 v[208:209], off
	s_waitcnt vmcnt(8)
	s_waitcnt lgkmcnt(0)
	v_mfma_f32_16x16x32_bf16 v[62:65], v[130:133], v[162:165], v[62:65]
	v_mfma_f32_16x16x32_bf16 v[58:61], v[138:141], v[162:165], v[58:61]
	v_mfma_f32_16x16x32_bf16 v[54:57], v[130:133], v[170:173], v[54:57]
	v_mfma_f32_16x16x32_bf16 v[50:53], v[138:141], v[170:173], v[50:53]
	s_barrier
	s_setprio 1
	s_waitcnt lgkmcnt(0)
	v_mfma_f32_16x16x32_bf16 v[46:49], v[130:133], v[178:181], v[46:49]
	v_mfma_f32_16x16x32_bf16 v[38:41], v[138:141], v[178:181], v[38:41]
	v_mfma_f32_16x16x32_bf16 v[30:33], v[130:133], v[186:189], v[30:33]
	v_mfma_f32_16x16x32_bf16 v[10:13], v[138:141], v[186:189], v[10:13]
	v_mfma_f32_16x16x32_bf16 v[62:65], v[134:137], v[166:169], v[62:65]
	v_mfma_f32_16x16x32_bf16 v[58:61], v[142:145], v[166:169], v[58:61]
	v_mfma_f32_16x16x32_bf16 v[54:57], v[134:137], v[174:177], v[54:57]
	v_mfma_f32_16x16x32_bf16 v[50:53], v[142:145], v[174:177], v[50:53]
	v_mfma_f32_16x16x32_bf16 v[46:49], v[134:137], v[182:185], v[46:49]
	v_mfma_f32_16x16x32_bf16 v[38:41], v[142:145], v[182:185], v[38:41]
	v_mfma_f32_16x16x32_bf16 v[30:33], v[134:137], v[190:193], v[30:33]
	v_mfma_f32_16x16x32_bf16 v[10:13], v[142:145], v[190:193], v[10:13]
	s_setprio 0
	s_setprio 1
	v_mfma_f32_16x16x32_bf16 v[42:45], v[146:149], v[162:165], v[42:45]
	v_mfma_f32_16x16x32_bf16 v[34:37], v[154:157], v[162:165], v[34:37]
	v_mfma_f32_16x16x32_bf16 v[26:29], v[146:149], v[170:173], v[26:29]
	v_mfma_f32_16x16x32_bf16 v[22:25], v[154:157], v[170:173], v[22:25]
	v_mfma_f32_16x16x32_bf16 v[18:21], v[146:149], v[178:181], v[18:21]
	v_mfma_f32_16x16x32_bf16 v[14:17], v[154:157], v[178:181], v[14:17]
	v_mfma_f32_16x16x32_bf16 v[6:9], v[146:149], v[186:189], v[6:9]
	v_mfma_f32_16x16x32_bf16 v[2:5], v[154:157], v[186:189], v[2:5]
	v_mfma_f32_16x16x32_bf16 v[42:45], v[150:153], v[166:169], v[42:45]
	v_mfma_f32_16x16x32_bf16 v[34:37], v[158:161], v[166:169], v[34:37]
	v_mfma_f32_16x16x32_bf16 v[26:29], v[150:153], v[174:177], v[26:29]
	v_mfma_f32_16x16x32_bf16 v[22:25], v[158:161], v[174:177], v[22:25]
	v_mfma_f32_16x16x32_bf16 v[18:21], v[150:153], v[182:185], v[18:21]
	v_mfma_f32_16x16x32_bf16 v[14:17], v[158:161], v[182:185], v[14:17]
	v_mfma_f32_16x16x32_bf16 v[6:9], v[150:153], v[190:193], v[6:9]
	v_mfma_f32_16x16x32_bf16 v[2:5], v[158:161], v[190:193], v[2:5]
	s_setprio 0
	s_barrier
	s_add_i32 s80, s80, 2
	s_add_u32 s74, s74, 0x10000
	s_addc_u32 s75, s75, 0
	s_add_u32 s58, s58, 0x100
	s_addc_u32 s59, s59, 0
	s_cmp_gt_u32 s80, 29
	s_cbranch_scc0 .LBB0_660
	s_and_b64 vcc, exec, s[24:25]
	s_cbranch_vccz .LBB0_663
	s_barrier

.LBB0_783:
	ds_read_b128 v[144:147], v151
	ds_read_b128 v[156:159], v151 offset:1024
	ds_read_b128 v[160:163], v151 offset:2048
	ds_read_b128 v[164:167], v151 offset:3072
	ds_read_b128 v[168:171], v152
	ds_read_b128 v[172:175], v152 offset:1024
	ds_read_b128 v[176:179], v152 offset:2048
	ds_read_b128 v[180:183], v152 offset:3072
	s_add_u32 s26, s62, 0xfff80080
	s_addc_u32 s27, s63, -1
	s_cmp_eq_u32 s85, 28
	s_cselect_b32 s65, s55, s27
	s_cselect_b32 s64, s81, s26
	s_cselect_b32 s27, s53, s84
	s_cselect_b32 s26, s82, s83
	v_lshl_add_u64 v[216:217], s[62:63], 0, v[136:137]
	s_add_i32 m0, s61, 0xc000
	ds_read_b128 v[184:187], v153
	ds_read_b128 v[188:191], v153 offset:1024
	ds_read_b128 v[192:195], v153 offset:2048
	ds_read_b128 v[196:199], v153 offset:3072
	ds_read_b128 v[200:203], v153 offset:4096
	ds_read_b128 v[204:207], v153 offset:5120
	ds_read_b128 v[208:211], v153 offset:6144
	ds_read_b128 v[212:215], v153 offset:7168
	global_load_lds_dwordx4 v[216:217], off
	v_lshl_add_u64 v[216:217], s[62:63], 0, v[138:139]
	s_add_i32 m0, s61, 0xe000
	s_nop 0
	global_load_lds_dwordx4 v[216:217], off
	s_waitcnt vmcnt(8)
	s_waitcnt lgkmcnt(0)
	v_mfma_f32_16x16x32_bf16 v[126:129], v[144:147], v[184:187], v[126:129]
	v_mfma_f32_16x16x32_bf16 v[118:121], v[160:163], v[184:187], v[118:121]
	v_mfma_f32_16x16x32_bf16 v[110:113], v[144:147], v[192:195], v[110:113]
	v_mfma_f32_16x16x32_bf16 v[102:105], v[160:163], v[192:195], v[102:105]
	s_barrier
	s_setprio 1
	s_waitcnt lgkmcnt(0)
	v_mfma_f32_16x16x32_bf16 v[94:97], v[144:147], v[200:203], v[94:97]
	v_mfma_f32_16x16x32_bf16 v[86:89], v[160:163], v[200:203], v[86:89]
	v_mfma_f32_16x16x32_bf16 v[78:81], v[144:147], v[208:211], v[78:81]
	v_mfma_f32_16x16x32_bf16 v[70:73], v[160:163], v[208:211], v[70:73]
	v_mfma_f32_16x16x32_bf16 v[126:129], v[156:159], v[188:191], v[126:129]
	v_mfma_f32_16x16x32_bf16 v[118:121], v[164:167], v[188:191], v[118:121]
	v_mfma_f32_16x16x32_bf16 v[110:113], v[156:159], v[196:199], v[110:113]
	v_mfma_f32_16x16x32_bf16 v[102:105], v[164:167], v[196:199], v[102:105]
	v_mfma_f32_16x16x32_bf16 v[94:97], v[156:159], v[204:207], v[94:97]
	v_mfma_f32_16x16x32_bf16 v[86:89], v[164:167], v[204:207], v[86:89]
	v_mfma_f32_16x16x32_bf16 v[78:81], v[156:159], v[212:215], v[78:81]
	v_mfma_f32_16x16x32_bf16 v[70:73], v[164:167], v[212:215], v[70:73]
	s_setprio 0
	s_setprio 1
	v_mfma_f32_16x16x32_bf16 v[122:125], v[168:171], v[184:187], v[122:125]
	v_mfma_f32_16x16x32_bf16 v[114:117], v[176:179], v[184:187], v[114:117]
	v_mfma_f32_16x16x32_bf16 v[106:109], v[168:171], v[192:195], v[106:109]
	v_mfma_f32_16x16x32_bf16 v[98:101], v[176:179], v[192:195], v[98:101]
	v_mfma_f32_16x16x32_bf16 v[90:93], v[168:171], v[200:203], v[90:93]
	v_mfma_f32_16x16x32_bf16 v[82:85], v[176:179], v[200:203], v[82:85]
	v_mfma_f32_16x16x32_bf16 v[74:77], v[168:171], v[208:211], v[74:77]
	v_mfma_f32_16x16x32_bf16 v[66:69], v[176:179], v[208:211], v[66:69]
	v_mfma_f32_16x16x32_bf16 v[122:125], v[172:175], v[188:191], v[122:125]
	v_mfma_f32_16x16x32_bf16 v[114:117], v[180:183], v[188:191], v[114:117]
	v_mfma_f32_16x16x32_bf16 v[106:109], v[172:175], v[196:199], v[106:109]
	v_mfma_f32_16x16x32_bf16 v[98:101], v[180:183], v[196:199], v[98:101]
	v_mfma_f32_16x16x32_bf16 v[90:93], v[172:175], v[204:207], v[90:93]
	v_mfma_f32_16x16x32_bf16 v[82:85], v[180:183], v[204:207], v[82:85]
	v_mfma_f32_16x16x32_bf16 v[74:77], v[172:175], v[212:215], v[74:77]
	v_mfma_f32_16x16x32_bf16 v[66:69], v[180:183], v[212:215], v[66:69]
	s_setprio 0
	s_barrier
	v_lshl_add_u64 v[216:217], s[26:27], 0, v[130:131]
	s_add_i32 s26, s73, s35
	s_mov_b32 m0, s26
	ds_read_b128 v[184:187], v153 offset:16384
	ds_read_b128 v[188:191], v153 offset:17408
	ds_read_b128 v[192:195], v153 offset:18432
	ds_read_b128 v[196:199], v153 offset:19456
	ds_read_b128 v[200:203], v153 offset:20480
	ds_read_b128 v[204:207], v153 offset:21504
	ds_read_b128 v[208:211], v153 offset:22528
	ds_read_b128 v[212:215], v153 offset:23552
	global_load_lds_dwordx4 v[216:217], off
	v_lshl_add_u64 v[220:221], v[216:217], 0, s[6:7]
	s_add_i32 m0, s26, 0x2000
	s_add_i32 s26, s74, s35
	global_load_lds_dwordx4 v[220:221], off
	v_lshl_add_u64 v[220:221], v[216:217], 0, s[8:9]
	s_mov_b32 m0, s26
	v_lshl_add_u64 v[222:223], s[64:65], 0, v[134:135]
	global_load_lds_dwordx4 v[220:221], off
	v_lshl_add_u64 v[220:221], v[216:217], 0, s[10:11]
	s_add_i32 m0, s26, 0x2000
	s_nop 0
	global_load_lds_dwordx4 v[220:221], off
	v_lshl_add_u64 v[220:221], s[64:65], 0, v[132:133]
	s_mov_b32 m0, s61
	s_nop 0
	global_load_lds_dwordx4 v[220:221], off
	s_mov_b32 m0, s66
	s_nop 0
	global_load_lds_dwordx4 v[222:223], off
	s_waitcnt vmcnt(8)
	s_waitcnt lgkmcnt(0)
	v_mfma_f32_16x16x32_bf16 v[62:65], v[144:147], v[184:187], v[62:65]
	v_mfma_f32_16x16x32_bf16 v[54:57], v[160:163], v[184:187], v[54:57]
	v_mfma_f32_16x16x32_bf16 v[46:49], v[144:147], v[192:195], v[46:49]
	v_mfma_f32_16x16x32_bf16 v[38:41], v[160:163], v[192:195], v[38:41]
	s_barrier
	s_setprio 1
	s_waitcnt lgkmcnt(0)
	v_mfma_f32_16x16x32_bf16 v[30:33], v[144:147], v[200:203], v[30:33]
	v_mfma_f32_16x16x32_bf16 v[22:25], v[160:163], v[200:203], v[22:25]
	v_mfma_f32_16x16x32_bf16 v[14:17], v[144:147], v[208:211], v[14:17]
	v_mfma_f32_16x16x32_bf16 v[6:9], v[160:163], v[208:211], v[6:9]
	v_mfma_f32_16x16x32_bf16 v[62:65], v[156:159], v[188:191], v[62:65]
	v_mfma_f32_16x16x32_bf16 v[54:57], v[164:167], v[188:191], v[54:57]
	v_mfma_f32_16x16x32_bf16 v[46:49], v[156:159], v[196:199], v[46:49]
	v_mfma_f32_16x16x32_bf16 v[38:41], v[164:167], v[196:199], v[38:41]
	v_mfma_f32_16x16x32_bf16 v[30:33], v[156:159], v[204:207], v[30:33]
	v_mfma_f32_16x16x32_bf16 v[22:25], v[164:167], v[204:207], v[22:25]
	v_mfma_f32_16x16x32_bf16 v[14:17], v[156:159], v[212:215], v[14:17]
	v_mfma_f32_16x16x32_bf16 v[6:9], v[164:167], v[212:215], v[6:9]
	s_setprio 0
	s_setprio 1
	v_mfma_f32_16x16x32_bf16 v[58:61], v[168:171], v[184:187], v[58:61]
	v_mfma_f32_16x16x32_bf16 v[50:53], v[176:179], v[184:187], v[50:53]
	v_mfma_f32_16x16x32_bf16 v[42:45], v[168:171], v[192:195], v[42:45]
	v_mfma_f32_16x16x32_bf16 v[34:37], v[176:179], v[192:195], v[34:37]
	v_mfma_f32_16x16x32_bf16 v[26:29], v[168:171], v[200:203], v[26:29]
	v_mfma_f32_16x16x32_bf16 v[18:21], v[176:179], v[200:203], v[18:21]
	v_mfma_f32_16x16x32_bf16 v[10:13], v[168:171], v[208:211], v[10:13]
	v_mfma_f32_16x16x32_bf16 v[2:5], v[176:179], v[208:211], v[2:5]
	v_mfma_f32_16x16x32_bf16 v[58:61], v[172:175], v[188:191], v[58:61]
	v_mfma_f32_16x16x32_bf16 v[50:53], v[180:183], v[188:191], v[50:53]
	v_mfma_f32_16x16x32_bf16 v[42:45], v[172:175], v[196:199], v[42:45]
	v_mfma_f32_16x16x32_bf16 v[34:37], v[180:183], v[196:199], v[34:37]
	v_mfma_f32_16x16x32_bf16 v[26:29], v[172:175], v[204:207], v[26:29]
	v_mfma_f32_16x16x32_bf16 v[18:21], v[180:183], v[204:207], v[18:21]
	v_mfma_f32_16x16x32_bf16 v[10:13], v[172:175], v[212:215], v[10:13]
	v_mfma_f32_16x16x32_bf16 v[2:5], v[180:183], v[212:215], v[2:5]
	s_setprio 0
	s_barrier
	s_add_i32 s86, 0, 0x18000
	v_add_u32_e32 v155, s86, v149
	s_add_i32 s87, 0, 0x1c000
	ds_read_b128 v[144:147], v155
	ds_read_b128 v[156:159], v155 offset:1024
	ds_read_b128 v[160:163], v155 offset:2048
	ds_read_b128 v[164:167], v155 offset:3072
	v_add_u32_e32 v155, s87, v149
	ds_read_b128 v[168:171], v155
	ds_read_b128 v[172:175], v155 offset:1024
	ds_read_b128 v[176:179], v155 offset:2048
	ds_read_b128 v[180:183], v155 offset:3072
	s_add_u32 s26, s64, 0x80000
	s_addc_u32 s27, s65, 0
	s_mov_b32 m0, s67
	v_lshl_add_u64 v[224:225], s[26:27], 0, v[132:133]
	ds_read_b128 v[184:187], v153 offset:32768
	ds_read_b128 v[188:191], v153 offset:33792
	ds_read_b128 v[192:195], v153 offset:34816
	ds_read_b128 v[196:199], v153 offset:35840
	ds_read_b128 v[200:203], v153 offset:36864
	ds_read_b128 v[204:207], v153 offset:37888
	ds_read_b128 v[208:211], v153 offset:38912
	ds_read_b128 v[212:215], v153 offset:39936
	global_load_lds_dwordx4 v[224:225], off
	v_lshl_add_u64 v[224:225], s[26:27], 0, v[134:135]
	s_mov_b32 m0, s68
	s_nop 0
	global_load_lds_dwordx4 v[224:225], off
	s_waitcnt vmcnt(8)
	s_waitcnt lgkmcnt(0)
	v_mfma_f32_16x16x32_bf16 v[126:129], v[144:147], v[184:187], v[126:129]
	v_mfma_f32_16x16x32_bf16 v[118:121], v[160:163], v[184:187], v[118:121]
	v_mfma_f32_16x16x32_bf16 v[110:113], v[144:147], v[192:195], v[110:113]
	v_mfma_f32_16x16x32_bf16 v[102:105], v[160:163], v[192:195], v[102:105]
	s_barrier
	s_setprio 1
	s_waitcnt lgkmcnt(0)
	v_mfma_f32_16x16x32_bf16 v[94:97], v[144:147], v[200:203], v[94:97]
	v_mfma_f32_16x16x32_bf16 v[86:89], v[160:163], v[200:203], v[86:89]
	v_mfma_f32_16x16x32_bf16 v[78:81], v[144:147], v[208:211], v[78:81]
	v_mfma_f32_16x16x32_bf16 v[70:73], v[160:163], v[208:211], v[70:73]
	v_mfma_f32_16x16x32_bf16 v[126:129], v[156:159], v[188:191], v[126:129]
	v_mfma_f32_16x16x32_bf16 v[118:121], v[164:167], v[188:191], v[118:121]
	v_mfma_f32_16x16x32_bf16 v[110:113], v[156:159], v[196:199], v[110:113]
	v_mfma_f32_16x16x32_bf16 v[102:105], v[164:167], v[196:199], v[102:105]
	v_mfma_f32_16x16x32_bf16 v[94:97], v[156:159], v[204:207], v[94:97]
	v_mfma_f32_16x16x32_bf16 v[86:89], v[164:167], v[204:207], v[86:89]
	v_mfma_f32_16x16x32_bf16 v[78:81], v[156:159], v[212:215], v[78:81]
	v_mfma_f32_16x16x32_bf16 v[70:73], v[164:167], v[212:215], v[70:73]
	s_setprio 0
	s_setprio 1
	v_mfma_f32_16x16x32_bf16 v[122:125], v[168:171], v[184:187], v[122:125]
	v_mfma_f32_16x16x32_bf16 v[114:117], v[176:179], v[184:187], v[114:117]
	v_mfma_f32_16x16x32_bf16 v[106:109], v[168:171], v[192:195], v[106:109]
	v_mfma_f32_16x16x32_bf16 v[98:101], v[176:179], v[192:195], v[98:101]
	v_mfma_f32_16x16x32_bf16 v[90:93], v[168:171], v[200:203], v[90:93]
	v_mfma_f32_16x16x32_bf16 v[82:85], v[176:179], v[200:203], v[82:85]
	v_mfma_f32_16x16x32_bf16 v[74:77], v[168:171], v[208:211], v[74:77]
	v_mfma_f32_16x16x32_bf16 v[66:69], v[176:179], v[208:211], v[66:69]
	v_mfma_f32_16x16x32_bf16 v[122:125], v[172:175], v[188:191], v[122:125]
	v_mfma_f32_16x16x32_bf16 v[114:117], v[180:183], v[188:191], v[114:117]
	v_mfma_f32_16x16x32_bf16 v[106:109], v[172:175], v[196:199], v[106:109]
	v_mfma_f32_16x16x32_bf16 v[98:101], v[180:183], v[196:199], v[98:101]
	v_mfma_f32_16x16x32_bf16 v[90:93], v[172:175], v[204:207], v[90:93]
	v_mfma_f32_16x16x32_bf16 v[82:85], v[180:183], v[204:207], v[82:85]
	v_mfma_f32_16x16x32_bf16 v[74:77], v[172:175], v[212:215], v[74:77]
	v_mfma_f32_16x16x32_bf16 v[66:69], v[180:183], v[212:215], v[66:69]
	s_setprio 0
	s_barrier
	s_add_i32 s26, s86, s35
	v_lshl_add_u64 v[224:225], v[216:217], 0, s[16:17]
	s_mov_b32 m0, s26
	ds_read_b128 v[184:187], v153 offset:49152
	ds_read_b128 v[188:191], v153 offset:50176
	ds_read_b128 v[192:195], v153 offset:51200
	ds_read_b128 v[196:199], v153 offset:52224
	ds_read_b128 v[200:203], v153 offset:53248
	ds_read_b128 v[204:207], v153 offset:54272
	ds_read_b128 v[208:211], v153 offset:55296
	ds_read_b128 v[212:215], v153 offset:56320
	global_load_lds_dwordx4 v[224:225], off
	v_lshl_add_u64 v[224:225], v[216:217], 0, s[18:19]
	s_add_i32 m0, s26, 0x2000
	s_add_i32 s26, s87, s35
	global_load_lds_dwordx4 v[224:225], off
	v_lshl_add_u64 v[224:225], v[216:217], 0, s[22:23]
	s_mov_b32 m0, s26
	v_lshl_add_u64 v[216:217], v[216:217], 0, s[24:25]
	global_load_lds_dwordx4 v[224:225], off
	s_add_i32 m0, s26, 0x2000
	s_nop 0
	global_load_lds_dwordx4 v[216:217], off
	v_lshl_add_u64 v[216:217], v[220:221], 0, s[20:21]
	s_mov_b32 m0, s70
	s_nop 0
	global_load_lds_dwordx4 v[216:217], off
	v_lshl_add_u64 v[216:217], v[222:223], 0, s[20:21]
	s_mov_b32 m0, s71
	s_nop 0
	global_load_lds_dwordx4 v[216:217], off
	s_waitcnt vmcnt(8)
	s_waitcnt lgkmcnt(0)
	v_mfma_f32_16x16x32_bf16 v[62:65], v[144:147], v[184:187], v[62:65]
	v_mfma_f32_16x16x32_bf16 v[54:57], v[160:163], v[184:187], v[54:57]
	v_mfma_f32_16x16x32_bf16 v[46:49], v[144:147], v[192:195], v[46:49]
	v_mfma_f32_16x16x32_bf16 v[38:41], v[160:163], v[192:195], v[38:41]
	s_barrier
	s_setprio 1
	s_waitcnt lgkmcnt(0)
	v_mfma_f32_16x16x32_bf16 v[30:33], v[144:147], v[200:203], v[30:33]
	v_mfma_f32_16x16x32_bf16 v[22:25], v[160:163], v[200:203], v[22:25]
	v_mfma_f32_16x16x32_bf16 v[14:17], v[144:147], v[208:211], v[14:17]
	v_mfma_f32_16x16x32_bf16 v[6:9], v[160:163], v[208:211], v[6:9]
	v_mfma_f32_16x16x32_bf16 v[62:65], v[156:159], v[188:191], v[62:65]
	v_mfma_f32_16x16x32_bf16 v[54:57], v[164:167], v[188:191], v[54:57]
	v_mfma_f32_16x16x32_bf16 v[46:49], v[156:159], v[196:199], v[46:49]
	v_mfma_f32_16x16x32_bf16 v[38:41], v[164:167], v[196:199], v[38:41]
	v_mfma_f32_16x16x32_bf16 v[30:33], v[156:159], v[204:207], v[30:33]
	v_mfma_f32_16x16x32_bf16 v[22:25], v[164:167], v[204:207], v[22:25]
	v_mfma_f32_16x16x32_bf16 v[14:17], v[156:159], v[212:215], v[14:17]
	v_mfma_f32_16x16x32_bf16 v[6:9], v[164:167], v[212:215], v[6:9]
	s_setprio 0
	s_setprio 1
	v_mfma_f32_16x16x32_bf16 v[58:61], v[168:171], v[184:187], v[58:61]
	v_mfma_f32_16x16x32_bf16 v[50:53], v[176:179], v[184:187], v[50:53]
	v_mfma_f32_16x16x32_bf16 v[42:45], v[168:171], v[192:195], v[42:45]
	v_mfma_f32_16x16x32_bf16 v[34:37], v[176:179], v[192:195], v[34:37]
	v_mfma_f32_16x16x32_bf16 v[26:29], v[168:171], v[200:203], v[26:29]
	v_mfma_f32_16x16x32_bf16 v[18:21], v[176:179], v[200:203], v[18:21]
	v_mfma_f32_16x16x32_bf16 v[10:13], v[168:171], v[208:211], v[10:13]
	v_mfma_f32_16x16x32_bf16 v[2:5], v[176:179], v[208:211], v[2:5]
	v_mfma_f32_16x16x32_bf16 v[58:61], v[172:175], v[188:191], v[58:61]
	v_mfma_f32_16x16x32_bf16 v[50:53], v[180:183], v[188:191], v[50:53]
	v_mfma_f32_16x16x32_bf16 v[42:45], v[172:175], v[196:199], v[42:45]
	v_mfma_f32_16x16x32_bf16 v[34:37], v[180:183], v[196:199], v[34:37]
	v_mfma_f32_16x16x32_bf16 v[26:29], v[172:175], v[204:207], v[26:29]
	v_mfma_f32_16x16x32_bf16 v[18:21], v[180:183], v[204:207], v[18:21]
	v_mfma_f32_16x16x32_bf16 v[10:13], v[172:175], v[212:215], v[10:13]
	v_mfma_f32_16x16x32_bf16 v[2:5], v[180:183], v[212:215], v[2:5]
	s_setprio 0
	s_barrier
	s_add_i32 s85, s85, 2
	s_add_u32 s83, s83, 0x10000
	s_addc_u32 s84, s84, 0
	s_add_u32 s62, s62, 0x100
	s_addc_u32 s63, s63, 0
	s_cmp_gt_u32 s85, 29
	s_cbranch_scc0 .LBB0_783
	s_and_b64 vcc, exec, s[40:41]
	s_cbranch_vccz .LBB0_786
	s_barrier

.LBB0_858:
	ds_read_b128 v[26:29], v185
	ds_read_b128 v[30:33], v185 offset:1024
	ds_read_b128 v[18:21], v185 offset:2048
	ds_read_b128 v[22:25], v185 offset:3072
	ds_read_b128 v[10:13], v186
	ds_read_b128 v[14:17], v186 offset:1024
	ds_read_b128 v[2:5], v186 offset:2048
	ds_read_b128 v[6:9], v186 offset:3072
	s_add_u32 s26, s50, 0xfff50080
	s_addc_u32 s27, s51, -1
	s_cmp_eq_u32 s74, 40
	s_cselect_b32 s53, s5, s27
	s_cselect_b32 s52, s4, s26
	s_cselect_b32 s55, s45, s73
	s_cselect_b32 s54, s44, s72
	v_lshl_add_u64 v[176:177], s[50:51], 0, v[168:169]
	s_add_i32 m0, s59, 0xc000
	ds_read_b128 v[190:193], v187
	ds_read_b128 v[194:197], v187 offset:1024
	ds_read_b128 v[198:201], v187 offset:2048
	ds_read_b128 v[202:205], v187 offset:3072
	ds_read_b128 v[206:209], v187 offset:4096
	ds_read_b128 v[210:213], v187 offset:5120
	ds_read_b128 v[220:223], v187 offset:6144
	ds_read_b128 v[224:227], v187 offset:7168
	global_load_lds_dwordx4 v[176:177], off
	v_lshl_add_u64 v[176:177], s[50:51], 0, v[170:171]
	s_add_i32 m0, s59, 0xe000
	s_nop 0
	global_load_lds_dwordx4 v[176:177], off
	s_waitcnt vmcnt(8)
	s_waitcnt lgkmcnt(0)
	v_mfma_scale_f32_16x16x128_f8f6f4 v[158:161], v[26:33], v[190:197], v[158:161], v188, v189 op_sel_hi:[0,0,0]
	v_mfma_scale_f32_16x16x128_f8f6f4 v[154:157], v[18:25], v[190:197], v[154:157], v188, v189 op_sel_hi:[0,0,0]
	s_barrier
	s_setprio 1
	s_waitcnt lgkmcnt(0)
	v_mfma_scale_f32_16x16x128_f8f6f4 v[150:153], v[26:33], v[198:205], v[150:153], v188, v189 op_sel_hi:[0,0,0]
	v_mfma_scale_f32_16x16x128_f8f6f4 v[146:149], v[18:25], v[198:205], v[146:149], v188, v189 op_sel_hi:[0,0,0]
	v_mfma_scale_f32_16x16x128_f8f6f4 v[138:141], v[26:33], v[206:213], v[138:141], v188, v189 op_sel_hi:[0,0,0]
	v_mfma_scale_f32_16x16x128_f8f6f4 v[130:133], v[18:25], v[206:213], v[130:133], v188, v189 op_sel_hi:[0,0,0]
	v_mfma_scale_f32_16x16x128_f8f6f4 v[122:125], v[26:33], v[220:227], v[122:125], v188, v189 op_sel_hi:[0,0,0]
	v_mfma_scale_f32_16x16x128_f8f6f4 v[114:117], v[18:25], v[220:227], v[114:117], v188, v189 op_sel_hi:[0,0,0]
	s_setprio 0
	s_setprio 1
	v_mfma_scale_f32_16x16x128_f8f6f4 v[142:145], v[10:17], v[190:197], v[142:145], v188, v189 op_sel_hi:[0,0,0]
	v_mfma_scale_f32_16x16x128_f8f6f4 v[134:137], v[2:9], v[190:197], v[134:137], v188, v189 op_sel_hi:[0,0,0]
	v_mfma_scale_f32_16x16x128_f8f6f4 v[126:129], v[10:17], v[198:205], v[126:129], v188, v189 op_sel_hi:[0,0,0]
	v_mfma_scale_f32_16x16x128_f8f6f4 v[118:121], v[2:9], v[198:205], v[118:121], v188, v189 op_sel_hi:[0,0,0]
	v_mfma_scale_f32_16x16x128_f8f6f4 v[110:113], v[10:17], v[206:213], v[110:113], v188, v189 op_sel_hi:[0,0,0]
	v_mfma_scale_f32_16x16x128_f8f6f4 v[106:109], v[2:9], v[206:213], v[106:109], v188, v189 op_sel_hi:[0,0,0]
	v_mfma_scale_f32_16x16x128_f8f6f4 v[102:105], v[10:17], v[220:227], v[102:105], v188, v189 op_sel_hi:[0,0,0]
	v_mfma_scale_f32_16x16x128_f8f6f4 v[98:101], v[2:9], v[220:227], v[98:101], v188, v189 op_sel_hi:[0,0,0]
	s_setprio 0
	s_barrier
	s_add_i32 s26, s67, s57
	v_lshl_add_u64 v[176:177], s[54:55], 0, v[162:163]
	s_mov_b32 m0, s26
	ds_read_b128 v[190:193], v187 offset:16384
	ds_read_b128 v[194:197], v187 offset:17408
	ds_read_b128 v[198:201], v187 offset:18432
	ds_read_b128 v[202:205], v187 offset:19456
	ds_read_b128 v[206:209], v187 offset:20480
	ds_read_b128 v[210:213], v187 offset:21504
	ds_read_b128 v[220:223], v187 offset:22528
	ds_read_b128 v[224:227], v187 offset:23552
	global_load_lds_dwordx4 v[176:177], off
	v_lshl_add_u64 v[178:179], v[176:177], 0, s[8:9]
	s_add_i32 m0, s26, 0x2000
	s_add_i32 s26, s68, s57
	global_load_lds_dwordx4 v[178:179], off
	v_lshl_add_u64 v[178:179], v[176:177], 0, s[10:11]
	s_mov_b32 m0, s26
	v_lshl_add_u64 v[180:181], s[52:53], 0, v[166:167]
	global_load_lds_dwordx4 v[178:179], off
	v_lshl_add_u64 v[178:179], v[176:177], 0, s[12:13]
	s_add_i32 m0, s26, 0x2000
	s_nop 0
	global_load_lds_dwordx4 v[178:179], off
	v_lshl_add_u64 v[178:179], s[52:53], 0, v[164:165]
	s_mov_b32 m0, s59
	s_nop 0
	global_load_lds_dwordx4 v[178:179], off
	s_mov_b32 m0, s60
	s_nop 0
	global_load_lds_dwordx4 v[180:181], off
	s_waitcnt vmcnt(8)
	s_waitcnt lgkmcnt(0)
	v_mfma_scale_f32_16x16x128_f8f6f4 v[94:97], v[26:33], v[190:197], v[94:97], v188, v189 op_sel_hi:[0,0,0]
	v_mfma_scale_f32_16x16x128_f8f6f4 v[90:93], v[18:25], v[190:197], v[90:93], v188, v189 op_sel_hi:[0,0,0]
	s_barrier
	s_setprio 1
	s_waitcnt lgkmcnt(0)
	v_mfma_scale_f32_16x16x128_f8f6f4 v[86:89], v[26:33], v[198:205], v[86:89], v188, v189 op_sel_hi:[0,0,0]
	v_mfma_scale_f32_16x16x128_f8f6f4 v[78:81], v[18:25], v[198:205], v[78:81], v188, v189 op_sel_hi:[0,0,0]
	v_mfma_scale_f32_16x16x128_f8f6f4 v[70:73], v[26:33], v[206:213], v[70:73], v188, v189 op_sel_hi:[0,0,0]
	v_mfma_scale_f32_16x16x128_f8f6f4 v[62:65], v[18:25], v[206:213], v[62:65], v188, v189 op_sel_hi:[0,0,0]
	v_mfma_scale_f32_16x16x128_f8f6f4 v[54:57], v[26:33], v[220:227], v[54:57], v188, v189 op_sel_hi:[0,0,0]
	v_mfma_scale_f32_16x16x128_f8f6f4 v[46:49], v[18:25], v[220:227], v[46:49], v188, v189 op_sel_hi:[0,0,0]
	s_setprio 0
	s_setprio 1
	v_mfma_scale_f32_16x16x128_f8f6f4 v[82:85], v[10:17], v[190:197], v[82:85], v188, v189 op_sel_hi:[0,0,0]
	v_mfma_scale_f32_16x16x128_f8f6f4 v[74:77], v[2:9], v[190:197], v[74:77], v188, v189 op_sel_hi:[0,0,0]
	v_mfma_scale_f32_16x16x128_f8f6f4 v[66:69], v[10:17], v[198:205], v[66:69], v188, v189 op_sel_hi:[0,0,0]
	v_mfma_scale_f32_16x16x128_f8f6f4 v[58:61], v[2:9], v[198:205], v[58:61], v188, v189 op_sel_hi:[0,0,0]
	v_mfma_scale_f32_16x16x128_f8f6f4 v[50:53], v[10:17], v[206:213], v[50:53], v188, v189 op_sel_hi:[0,0,0]
	v_mfma_scale_f32_16x16x128_f8f6f4 v[42:45], v[2:9], v[206:213], v[42:45], v188, v189 op_sel_hi:[0,0,0]
	v_mfma_scale_f32_16x16x128_f8f6f4 v[38:41], v[10:17], v[220:227], v[38:41], v188, v189 op_sel_hi:[0,0,0]
	v_mfma_scale_f32_16x16x128_f8f6f4 v[34:37], v[2:9], v[220:227], v[34:37], v188, v189 op_sel_hi:[0,0,0]
	s_setprio 0
	s_barrier
	s_add_i32 s54, 0, 0x18000
	s_add_i32 s55, 0, 0x1c000
	v_add_u32_e32 v14, s54, v183
	v_add_u32_e32 v30, s55, v183
	ds_read_b128 v[2:5], v14
	ds_read_b128 v[6:9], v14 offset:1024
	ds_read_b128 v[10:13], v14 offset:2048
	ds_read_b128 v[14:17], v14 offset:3072
	ds_read_b128 v[18:21], v30
	ds_read_b128 v[22:25], v30 offset:1024
	ds_read_b128 v[26:29], v30 offset:2048
	ds_read_b128 v[30:33], v30 offset:3072
	s_add_u32 s26, s52, 0xb0000
	s_addc_u32 s27, s53, 0
	s_mov_b32 m0, s61
	v_lshl_add_u64 v[214:215], s[26:27], 0, v[164:165]
	ds_read_b128 v[190:193], v187 offset:32768
	ds_read_b128 v[194:197], v187 offset:33792
	ds_read_b128 v[198:201], v187 offset:34816
	ds_read_b128 v[202:205], v187 offset:35840
	ds_read_b128 v[206:209], v187 offset:36864
	ds_read_b128 v[210:213], v187 offset:37888
	ds_read_b128 v[220:223], v187 offset:38912
	ds_read_b128 v[224:227], v187 offset:39936
	global_load_lds_dwordx4 v[214:215], off
	v_lshl_add_u64 v[214:215], s[26:27], 0, v[166:167]
	s_mov_b32 m0, s62
	s_nop 0
	global_load_lds_dwordx4 v[214:215], off
	s_waitcnt vmcnt(8)
	s_waitcnt lgkmcnt(0)
	v_mfma_scale_f32_16x16x128_f8f6f4 v[158:161], v[2:9], v[190:197], v[158:161], v188, v189 op_sel_hi:[0,0,0]
	v_mfma_scale_f32_16x16x128_f8f6f4 v[154:157], v[10:17], v[190:197], v[154:157], v188, v189 op_sel_hi:[0,0,0]
	s_barrier
	s_setprio 1
	s_waitcnt lgkmcnt(0)
	v_mfma_scale_f32_16x16x128_f8f6f4 v[150:153], v[2:9], v[198:205], v[150:153], v188, v189 op_sel_hi:[0,0,0]
	v_mfma_scale_f32_16x16x128_f8f6f4 v[146:149], v[10:17], v[198:205], v[146:149], v188, v189 op_sel_hi:[0,0,0]
	v_mfma_scale_f32_16x16x128_f8f6f4 v[138:141], v[2:9], v[206:213], v[138:141], v188, v189 op_sel_hi:[0,0,0]
	v_mfma_scale_f32_16x16x128_f8f6f4 v[130:133], v[10:17], v[206:213], v[130:133], v188, v189 op_sel_hi:[0,0,0]
	v_mfma_scale_f32_16x16x128_f8f6f4 v[122:125], v[2:9], v[220:227], v[122:125], v188, v189 op_sel_hi:[0,0,0]
	v_mfma_scale_f32_16x16x128_f8f6f4 v[114:117], v[10:17], v[220:227], v[114:117], v188, v189 op_sel_hi:[0,0,0]
	s_setprio 0
	s_setprio 1
	v_mfma_scale_f32_16x16x128_f8f6f4 v[142:145], v[18:25], v[190:197], v[142:145], v188, v189 op_sel_hi:[0,0,0]
	v_mfma_scale_f32_16x16x128_f8f6f4 v[134:137], v[26:33], v[190:197], v[134:137], v188, v189 op_sel_hi:[0,0,0]
	v_mfma_scale_f32_16x16x128_f8f6f4 v[126:129], v[18:25], v[198:205], v[126:129], v188, v189 op_sel_hi:[0,0,0]
	v_mfma_scale_f32_16x16x128_f8f6f4 v[118:121], v[26:33], v[198:205], v[118:121], v188, v189 op_sel_hi:[0,0,0]
	v_mfma_scale_f32_16x16x128_f8f6f4 v[110:113], v[18:25], v[206:213], v[110:113], v188, v189 op_sel_hi:[0,0,0]
	v_mfma_scale_f32_16x16x128_f8f6f4 v[106:109], v[26:33], v[206:213], v[106:109], v188, v189 op_sel_hi:[0,0,0]
	v_mfma_scale_f32_16x16x128_f8f6f4 v[102:105], v[18:25], v[220:227], v[102:105], v188, v189 op_sel_hi:[0,0,0]
	v_mfma_scale_f32_16x16x128_f8f6f4 v[98:101], v[26:33], v[220:227], v[98:101], v188, v189 op_sel_hi:[0,0,0]
	s_setprio 0
	s_barrier
	s_add_i32 s26, s54, s57
	v_lshl_add_u64 v[214:215], v[176:177], 0, s[16:17]
	s_mov_b32 m0, s26
	ds_read_b128 v[190:193], v187 offset:49152
	ds_read_b128 v[194:197], v187 offset:50176
	ds_read_b128 v[198:201], v187 offset:51200
	ds_read_b128 v[202:205], v187 offset:52224
	ds_read_b128 v[206:209], v187 offset:53248
	ds_read_b128 v[210:213], v187 offset:54272
	ds_read_b128 v[220:223], v187 offset:55296
	ds_read_b128 v[224:227], v187 offset:56320
	global_load_lds_dwordx4 v[214:215], off
	v_lshl_add_u64 v[214:215], v[176:177], 0, s[18:19]
	s_add_i32 m0, s26, 0x2000
	s_add_i32 s26, s55, s57
	global_load_lds_dwordx4 v[214:215], off
	v_lshl_add_u64 v[214:215], v[176:177], 0, s[22:23]
	s_mov_b32 m0, s26
	v_lshl_add_u64 v[176:177], v[176:177], 0, s[24:25]
	global_load_lds_dwordx4 v[214:215], off
	s_add_i32 m0, s26, 0x2000
	s_nop 0
	global_load_lds_dwordx4 v[176:177], off
	v_lshl_add_u64 v[176:177], v[178:179], 0, s[20:21]
	s_mov_b32 m0, s64
	s_nop 0
	global_load_lds_dwordx4 v[176:177], off
	v_lshl_add_u64 v[176:177], v[180:181], 0, s[20:21]
	s_mov_b32 m0, s65
	s_nop 0
	global_load_lds_dwordx4 v[176:177], off
	s_waitcnt vmcnt(8)
	s_waitcnt lgkmcnt(0)
	v_mfma_scale_f32_16x16x128_f8f6f4 v[94:97], v[2:9], v[190:197], v[94:97], v188, v189 op_sel_hi:[0,0,0]
	v_mfma_scale_f32_16x16x128_f8f6f4 v[90:93], v[10:17], v[190:197], v[90:93], v188, v189 op_sel_hi:[0,0,0]
	s_barrier
	s_setprio 1
	s_waitcnt lgkmcnt(0)
	v_mfma_scale_f32_16x16x128_f8f6f4 v[86:89], v[2:9], v[198:205], v[86:89], v188, v189 op_sel_hi:[0,0,0]
	v_mfma_scale_f32_16x16x128_f8f6f4 v[78:81], v[10:17], v[198:205], v[78:81], v188, v189 op_sel_hi:[0,0,0]
	v_mfma_scale_f32_16x16x128_f8f6f4 v[70:73], v[2:9], v[206:213], v[70:73], v188, v189 op_sel_hi:[0,0,0]
	v_mfma_scale_f32_16x16x128_f8f6f4 v[62:65], v[10:17], v[206:213], v[62:65], v188, v189 op_sel_hi:[0,0,0]
	v_mfma_scale_f32_16x16x128_f8f6f4 v[54:57], v[2:9], v[220:227], v[54:57], v188, v189 op_sel_hi:[0,0,0]
	v_mfma_scale_f32_16x16x128_f8f6f4 v[46:49], v[10:17], v[220:227], v[46:49], v188, v189 op_sel_hi:[0,0,0]
	s_setprio 0
	s_setprio 1
	v_mfma_scale_f32_16x16x128_f8f6f4 v[82:85], v[18:25], v[190:197], v[82:85], v188, v189 op_sel_hi:[0,0,0]
	v_mfma_scale_f32_16x16x128_f8f6f4 v[74:77], v[26:33], v[190:197], v[74:77], v188, v189 op_sel_hi:[0,0,0]
	v_mfma_scale_f32_16x16x128_f8f6f4 v[66:69], v[18:25], v[198:205], v[66:69], v188, v189 op_sel_hi:[0,0,0]
	v_mfma_scale_f32_16x16x128_f8f6f4 v[58:61], v[26:33], v[198:205], v[58:61], v188, v189 op_sel_hi:[0,0,0]
	v_mfma_scale_f32_16x16x128_f8f6f4 v[50:53], v[18:25], v[206:213], v[50:53], v188, v189 op_sel_hi:[0,0,0]
	v_mfma_scale_f32_16x16x128_f8f6f4 v[42:45], v[26:33], v[206:213], v[42:45], v188, v189 op_sel_hi:[0,0,0]
	v_mfma_scale_f32_16x16x128_f8f6f4 v[38:41], v[18:25], v[220:227], v[38:41], v188, v189 op_sel_hi:[0,0,0]
	v_mfma_scale_f32_16x16x128_f8f6f4 v[34:37], v[26:33], v[220:227], v[34:37], v188, v189 op_sel_hi:[0,0,0]
	s_setprio 0
	s_barrier
	s_add_i32 s74, s74, 2
	s_add_u32 s72, s72, 0x10000
	s_addc_u32 s73, s73, 0
	s_add_u32 s50, s50, 0x100
	s_addc_u32 s51, s51, 0
	s_cmp_gt_u32 s74, 41
	s_cbranch_scc0 .LBB0_858
	s_and_b64 vcc, exec, s[40:41]
	s_cbranch_vccz .LBB0_861
	s_barrier

.LBB0_985:
	ds_read_b128 v[26:29], v185
	ds_read_b128 v[30:33], v185 offset:1024
	ds_read_b128 v[18:21], v185 offset:2048
	ds_read_b128 v[22:25], v185 offset:3072
	ds_read_b128 v[10:13], v186
	ds_read_b128 v[14:17], v186 offset:1024
	ds_read_b128 v[2:5], v186 offset:2048
	ds_read_b128 v[6:9], v186 offset:3072
	s_add_u32 s26, s56, 0xfffc0080
	s_addc_u32 s27, s57, -1
	s_cmp_eq_u32 s80, 12
	s_cselect_b32 s59, s45, s27
	s_cselect_b32 s58, s72, s26
	s_cselect_b32 s61, s41, s75
	s_cselect_b32 s60, s73, s74
	v_lshl_add_u64 v[176:177], s[56:57], 0, v[168:169]
	s_add_i32 m0, s55, 0xc000
	ds_read_b128 v[192:195], v187
	ds_read_b128 v[196:199], v187 offset:1024
	ds_read_b128 v[200:203], v187 offset:2048
	ds_read_b128 v[204:207], v187 offset:3072
	ds_read_b128 v[208:211], v187 offset:4096
	ds_read_b128 v[212:215], v187 offset:5120
	ds_read_b128 v[220:223], v187 offset:6144
	ds_read_b128 v[224:227], v187 offset:7168
	global_load_lds_dwordx4 v[176:177], off
	v_lshl_add_u64 v[176:177], s[56:57], 0, v[170:171]
	s_add_i32 m0, s55, 0xe000
	s_nop 0
	global_load_lds_dwordx4 v[176:177], off
	s_waitcnt vmcnt(8)
	s_waitcnt lgkmcnt(0)
	v_mfma_scale_f32_16x16x128_f8f6f4 v[158:161], v[26:33], v[192:199], v[158:161], v188, v189 op_sel_hi:[0,0,0]
	v_mfma_scale_f32_16x16x128_f8f6f4 v[154:157], v[18:25], v[192:199], v[154:157], v188, v189 op_sel_hi:[0,0,0]
	s_barrier
	s_setprio 1
	s_waitcnt lgkmcnt(0)
	v_mfma_scale_f32_16x16x128_f8f6f4 v[146:149], v[26:33], v[200:207], v[146:149], v188, v189 op_sel_hi:[0,0,0]
	v_mfma_scale_f32_16x16x128_f8f6f4 v[138:141], v[18:25], v[200:207], v[138:141], v188, v189 op_sel_hi:[0,0,0]
	v_mfma_scale_f32_16x16x128_f8f6f4 v[130:133], v[26:33], v[208:215], v[130:133], v188, v189 op_sel_hi:[0,0,0]
	v_mfma_scale_f32_16x16x128_f8f6f4 v[122:125], v[18:25], v[208:215], v[122:125], v188, v189 op_sel_hi:[0,0,0]
	v_mfma_scale_f32_16x16x128_f8f6f4 v[114:117], v[26:33], v[220:227], v[114:117], v188, v189 op_sel_hi:[0,0,0]
	v_mfma_scale_f32_16x16x128_f8f6f4 v[106:109], v[18:25], v[220:227], v[106:109], v188, v189 op_sel_hi:[0,0,0]
	s_setprio 0
	s_setprio 1
	v_mfma_scale_f32_16x16x128_f8f6f4 v[150:153], v[10:17], v[192:199], v[150:153], v188, v189 op_sel_hi:[0,0,0]
	v_mfma_scale_f32_16x16x128_f8f6f4 v[142:145], v[2:9], v[192:199], v[142:145], v188, v189 op_sel_hi:[0,0,0]
	v_mfma_scale_f32_16x16x128_f8f6f4 v[134:137], v[10:17], v[200:207], v[134:137], v188, v189 op_sel_hi:[0,0,0]
	v_mfma_scale_f32_16x16x128_f8f6f4 v[126:129], v[2:9], v[200:207], v[126:129], v188, v189 op_sel_hi:[0,0,0]
	v_mfma_scale_f32_16x16x128_f8f6f4 v[118:121], v[10:17], v[208:215], v[118:121], v188, v189 op_sel_hi:[0,0,0]
	v_mfma_scale_f32_16x16x128_f8f6f4 v[110:113], v[2:9], v[208:215], v[110:113], v188, v189 op_sel_hi:[0,0,0]
	v_mfma_scale_f32_16x16x128_f8f6f4 v[102:105], v[10:17], v[220:227], v[102:105], v188, v189 op_sel_hi:[0,0,0]
	v_mfma_scale_f32_16x16x128_f8f6f4 v[98:101], v[2:9], v[220:227], v[98:101], v188, v189 op_sel_hi:[0,0,0]
	s_setprio 0
	s_barrier
	s_add_i32 s26, s70, s35
	v_lshl_add_u64 v[176:177], s[60:61], 0, v[162:163]
	s_mov_b32 m0, s26
	ds_read_b128 v[192:195], v187 offset:16384
	ds_read_b128 v[196:199], v187 offset:17408
	ds_read_b128 v[200:203], v187 offset:18432
	ds_read_b128 v[204:207], v187 offset:19456
	ds_read_b128 v[208:211], v187 offset:20480
	ds_read_b128 v[212:215], v187 offset:21504
	ds_read_b128 v[220:223], v187 offset:22528
	ds_read_b128 v[224:227], v187 offset:23552
	global_load_lds_dwordx4 v[176:177], off
	v_lshl_add_u64 v[178:179], v[176:177], 0, s[6:7]
	s_add_i32 m0, s26, 0x2000
	s_add_i32 s26, s71, s35
	global_load_lds_dwordx4 v[178:179], off
	v_lshl_add_u64 v[178:179], v[176:177], 0, s[8:9]
	s_mov_b32 m0, s26
	v_lshl_add_u64 v[180:181], s[58:59], 0, v[166:167]
	global_load_lds_dwordx4 v[178:179], off
	v_lshl_add_u64 v[178:179], v[176:177], 0, s[10:11]
	s_add_i32 m0, s26, 0x2000
	s_nop 0
	global_load_lds_dwordx4 v[178:179], off
	v_lshl_add_u64 v[178:179], s[58:59], 0, v[164:165]
	s_mov_b32 m0, s55
	s_nop 0
	global_load_lds_dwordx4 v[178:179], off
	s_mov_b32 m0, s63
	s_nop 0
	global_load_lds_dwordx4 v[180:181], off
	s_waitcnt vmcnt(8)
	s_waitcnt lgkmcnt(0)
	v_mfma_scale_f32_16x16x128_f8f6f4 v[94:97], v[26:33], v[192:199], v[94:97], v188, v189 op_sel_hi:[0,0,0]
	v_mfma_scale_f32_16x16x128_f8f6f4 v[90:93], v[18:25], v[192:199], v[90:93], v188, v189 op_sel_hi:[0,0,0]
	s_barrier
	s_setprio 1
	s_waitcnt lgkmcnt(0)
	v_mfma_scale_f32_16x16x128_f8f6f4 v[82:85], v[26:33], v[200:207], v[82:85], v188, v189 op_sel_hi:[0,0,0]
	v_mfma_scale_f32_16x16x128_f8f6f4 v[74:77], v[18:25], v[200:207], v[74:77], v188, v189 op_sel_hi:[0,0,0]
	v_mfma_scale_f32_16x16x128_f8f6f4 v[66:69], v[26:33], v[208:215], v[66:69], v188, v189 op_sel_hi:[0,0,0]
	v_mfma_scale_f32_16x16x128_f8f6f4 v[58:61], v[18:25], v[208:215], v[58:61], v188, v189 op_sel_hi:[0,0,0]
	v_mfma_scale_f32_16x16x128_f8f6f4 v[50:53], v[26:33], v[220:227], v[50:53], v188, v189 op_sel_hi:[0,0,0]
	v_mfma_scale_f32_16x16x128_f8f6f4 v[42:45], v[18:25], v[220:227], v[42:45], v188, v189 op_sel_hi:[0,0,0]
	s_setprio 0
	s_setprio 1
	v_mfma_scale_f32_16x16x128_f8f6f4 v[86:89], v[10:17], v[192:199], v[86:89], v188, v189 op_sel_hi:[0,0,0]
	v_mfma_scale_f32_16x16x128_f8f6f4 v[78:81], v[2:9], v[192:199], v[78:81], v188, v189 op_sel_hi:[0,0,0]
	v_mfma_scale_f32_16x16x128_f8f6f4 v[70:73], v[10:17], v[200:207], v[70:73], v188, v189 op_sel_hi:[0,0,0]
	v_mfma_scale_f32_16x16x128_f8f6f4 v[62:65], v[2:9], v[200:207], v[62:65], v188, v189 op_sel_hi:[0,0,0]
	v_mfma_scale_f32_16x16x128_f8f6f4 v[54:57], v[10:17], v[208:215], v[54:57], v188, v189 op_sel_hi:[0,0,0]
	v_mfma_scale_f32_16x16x128_f8f6f4 v[46:49], v[2:9], v[208:215], v[46:49], v188, v189 op_sel_hi:[0,0,0]
	v_mfma_scale_f32_16x16x128_f8f6f4 v[38:41], v[10:17], v[220:227], v[38:41], v188, v189 op_sel_hi:[0,0,0]
	v_mfma_scale_f32_16x16x128_f8f6f4 v[34:37], v[2:9], v[220:227], v[34:37], v188, v189 op_sel_hi:[0,0,0]
	s_setprio 0
	s_barrier
	s_add_i32 s60, 0, 0x18000
	s_add_i32 s61, 0, 0x1c000
	v_add_u32_e32 v14, s60, v183
	v_add_u32_e32 v30, s61, v183
	ds_read_b128 v[2:5], v14
	ds_read_b128 v[6:9], v14 offset:1024
	ds_read_b128 v[10:13], v14 offset:2048
	ds_read_b128 v[14:17], v14 offset:3072
	ds_read_b128 v[18:21], v30
	ds_read_b128 v[22:25], v30 offset:1024
	ds_read_b128 v[26:29], v30 offset:2048
	ds_read_b128 v[30:33], v30 offset:3072
	s_add_u32 s26, s58, 0x40000
	s_addc_u32 s27, s59, 0
	s_mov_b32 m0, s64
	v_lshl_add_u64 v[216:217], s[26:27], 0, v[164:165]
	ds_read_b128 v[192:195], v187 offset:32768
	ds_read_b128 v[196:199], v187 offset:33792
	ds_read_b128 v[200:203], v187 offset:34816
	ds_read_b128 v[204:207], v187 offset:35840
	ds_read_b128 v[208:211], v187 offset:36864
	ds_read_b128 v[212:215], v187 offset:37888
	ds_read_b128 v[220:223], v187 offset:38912
	ds_read_b128 v[224:227], v187 offset:39936
	global_load_lds_dwordx4 v[216:217], off
	v_lshl_add_u64 v[216:217], s[26:27], 0, v[166:167]
	s_mov_b32 m0, s65
	s_nop 0
	global_load_lds_dwordx4 v[216:217], off
	s_waitcnt vmcnt(8)
	s_waitcnt lgkmcnt(0)
	v_mfma_scale_f32_16x16x128_f8f6f4 v[158:161], v[2:9], v[192:199], v[158:161], v188, v189 op_sel_hi:[0,0,0]
	v_mfma_scale_f32_16x16x128_f8f6f4 v[154:157], v[10:17], v[192:199], v[154:157], v188, v189 op_sel_hi:[0,0,0]
	s_barrier
	s_setprio 1
	s_waitcnt lgkmcnt(0)
	v_mfma_scale_f32_16x16x128_f8f6f4 v[146:149], v[2:9], v[200:207], v[146:149], v188, v189 op_sel_hi:[0,0,0]
	v_mfma_scale_f32_16x16x128_f8f6f4 v[138:141], v[10:17], v[200:207], v[138:141], v188, v189 op_sel_hi:[0,0,0]
	v_mfma_scale_f32_16x16x128_f8f6f4 v[130:133], v[2:9], v[208:215], v[130:133], v188, v189 op_sel_hi:[0,0,0]
	v_mfma_scale_f32_16x16x128_f8f6f4 v[122:125], v[10:17], v[208:215], v[122:125], v188, v189 op_sel_hi:[0,0,0]
	v_mfma_scale_f32_16x16x128_f8f6f4 v[114:117], v[2:9], v[220:227], v[114:117], v188, v189 op_sel_hi:[0,0,0]
	v_mfma_scale_f32_16x16x128_f8f6f4 v[106:109], v[10:17], v[220:227], v[106:109], v188, v189 op_sel_hi:[0,0,0]
	s_setprio 0
	s_setprio 1
	v_mfma_scale_f32_16x16x128_f8f6f4 v[150:153], v[18:25], v[192:199], v[150:153], v188, v189 op_sel_hi:[0,0,0]
	v_mfma_scale_f32_16x16x128_f8f6f4 v[142:145], v[26:33], v[192:199], v[142:145], v188, v189 op_sel_hi:[0,0,0]
	v_mfma_scale_f32_16x16x128_f8f6f4 v[134:137], v[18:25], v[200:207], v[134:137], v188, v189 op_sel_hi:[0,0,0]
	v_mfma_scale_f32_16x16x128_f8f6f4 v[126:129], v[26:33], v[200:207], v[126:129], v188, v189 op_sel_hi:[0,0,0]
	v_mfma_scale_f32_16x16x128_f8f6f4 v[118:121], v[18:25], v[208:215], v[118:121], v188, v189 op_sel_hi:[0,0,0]
	v_mfma_scale_f32_16x16x128_f8f6f4 v[110:113], v[26:33], v[208:215], v[110:113], v188, v189 op_sel_hi:[0,0,0]
	v_mfma_scale_f32_16x16x128_f8f6f4 v[102:105], v[18:25], v[220:227], v[102:105], v188, v189 op_sel_hi:[0,0,0]
	v_mfma_scale_f32_16x16x128_f8f6f4 v[98:101], v[26:33], v[220:227], v[98:101], v188, v189 op_sel_hi:[0,0,0]
	s_setprio 0
	s_barrier
	s_add_i32 s26, s60, s35
	v_lshl_add_u64 v[216:217], v[176:177], 0, s[14:15]
	s_mov_b32 m0, s26
	ds_read_b128 v[192:195], v187 offset:49152
	ds_read_b128 v[196:199], v187 offset:50176
	ds_read_b128 v[200:203], v187 offset:51200
	ds_read_b128 v[204:207], v187 offset:52224
	ds_read_b128 v[208:211], v187 offset:53248
	ds_read_b128 v[212:215], v187 offset:54272
	ds_read_b128 v[220:223], v187 offset:55296
	ds_read_b128 v[224:227], v187 offset:56320
	global_load_lds_dwordx4 v[216:217], off
	v_lshl_add_u64 v[216:217], v[176:177], 0, s[16:17]
	s_add_i32 m0, s26, 0x2000
	s_add_i32 s26, s61, s35
	global_load_lds_dwordx4 v[216:217], off
	v_lshl_add_u64 v[216:217], v[176:177], 0, s[20:21]
	s_mov_b32 m0, s26
	v_lshl_add_u64 v[176:177], v[176:177], 0, s[22:23]
	global_load_lds_dwordx4 v[216:217], off
	s_add_i32 m0, s26, 0x2000
	s_nop 0
	global_load_lds_dwordx4 v[176:177], off
	v_lshl_add_u64 v[176:177], v[178:179], 0, s[18:19]
	s_mov_b32 m0, s67
	s_nop 0
	global_load_lds_dwordx4 v[176:177], off
	v_lshl_add_u64 v[176:177], v[180:181], 0, s[18:19]
	s_mov_b32 m0, s68
	s_nop 0
	global_load_lds_dwordx4 v[176:177], off
	s_waitcnt vmcnt(8)
	s_waitcnt lgkmcnt(0)
	v_mfma_scale_f32_16x16x128_f8f6f4 v[94:97], v[2:9], v[192:199], v[94:97], v188, v189 op_sel_hi:[0,0,0]
	v_mfma_scale_f32_16x16x128_f8f6f4 v[90:93], v[10:17], v[192:199], v[90:93], v188, v189 op_sel_hi:[0,0,0]
	s_barrier
	s_setprio 1
	s_waitcnt lgkmcnt(0)
	v_mfma_scale_f32_16x16x128_f8f6f4 v[82:85], v[2:9], v[200:207], v[82:85], v188, v189 op_sel_hi:[0,0,0]
	v_mfma_scale_f32_16x16x128_f8f6f4 v[74:77], v[10:17], v[200:207], v[74:77], v188, v189 op_sel_hi:[0,0,0]
	v_mfma_scale_f32_16x16x128_f8f6f4 v[66:69], v[2:9], v[208:215], v[66:69], v188, v189 op_sel_hi:[0,0,0]
	v_mfma_scale_f32_16x16x128_f8f6f4 v[58:61], v[10:17], v[208:215], v[58:61], v188, v189 op_sel_hi:[0,0,0]
	v_mfma_scale_f32_16x16x128_f8f6f4 v[50:53], v[2:9], v[220:227], v[50:53], v188, v189 op_sel_hi:[0,0,0]
	v_mfma_scale_f32_16x16x128_f8f6f4 v[42:45], v[10:17], v[220:227], v[42:45], v188, v189 op_sel_hi:[0,0,0]
	s_setprio 0
	s_setprio 1
	v_mfma_scale_f32_16x16x128_f8f6f4 v[86:89], v[18:25], v[192:199], v[86:89], v188, v189 op_sel_hi:[0,0,0]
	v_mfma_scale_f32_16x16x128_f8f6f4 v[78:81], v[26:33], v[192:199], v[78:81], v188, v189 op_sel_hi:[0,0,0]
	v_mfma_scale_f32_16x16x128_f8f6f4 v[70:73], v[18:25], v[200:207], v[70:73], v188, v189 op_sel_hi:[0,0,0]
	v_mfma_scale_f32_16x16x128_f8f6f4 v[62:65], v[26:33], v[200:207], v[62:65], v188, v189 op_sel_hi:[0,0,0]
	v_mfma_scale_f32_16x16x128_f8f6f4 v[54:57], v[18:25], v[208:215], v[54:57], v188, v189 op_sel_hi:[0,0,0]
	v_mfma_scale_f32_16x16x128_f8f6f4 v[46:49], v[26:33], v[208:215], v[46:49], v188, v189 op_sel_hi:[0,0,0]
	v_mfma_scale_f32_16x16x128_f8f6f4 v[38:41], v[18:25], v[220:227], v[38:41], v188, v189 op_sel_hi:[0,0,0]
	v_mfma_scale_f32_16x16x128_f8f6f4 v[34:37], v[26:33], v[220:227], v[34:37], v188, v189 op_sel_hi:[0,0,0]
	s_setprio 0
	s_barrier
	s_add_i32 s80, s80, 2
	s_add_u32 s74, s74, 0x10000
	s_addc_u32 s75, s75, 0
	s_add_u32 s56, s56, 0x100
	s_addc_u32 s57, s57, 0
	s_cmp_gt_u32 s80, 13
	s_cbranch_scc0 .LBB0_985
	s_and_b64 vcc, exec, s[24:25]
	s_cbranch_vccz .LBB0_988
	s_barrier

.LBB0_1192:
	ds_read_b128 v[66:69], v199
	ds_read_b128 v[70:73], v199 offset:1024
	ds_read_b128 v[82:85], v199 offset:2048
	ds_read_b128 v[86:89], v199 offset:3072
	ds_read_b128 v[146:149], v200
	ds_read_b128 v[150:153], v200 offset:1024
	ds_read_b128 v[154:157], v200 offset:2048
	ds_read_b128 v[158:161], v200 offset:3072
	s_add_u32 s26, s56, 0xfffc0080
	s_addc_u32 s27, s57, -1
	s_cmp_eq_u32 s73, 12
	s_cselect_b32 s59, s45, s27
	s_cselect_b32 s58, s69, s26
	s_cselect_b32 s27, s41, s72
	s_cselect_b32 s26, s70, s71
	v_lshl_add_u64 v[214:215], s[56:57], 0, v[176:177]
	s_add_i32 m0, s55, 0xc000
	ds_read_b128 v[162:165], v201
	ds_read_b128 v[166:169], v201 offset:1024
	ds_read_b128 v[184:187], v201 offset:2048
	ds_read_b128 v[188:191], v201 offset:3072
	ds_read_b128 v[192:195], v201 offset:4096
	ds_read_b128 v[202:205], v201 offset:5120
	ds_read_b128 v[206:209], v201 offset:6144
	ds_read_b128 v[210:213], v201 offset:7168
	global_load_lds_dwordx4 v[214:215], off
	v_lshl_add_u64 v[214:215], s[56:57], 0, v[178:179]
	s_add_i32 m0, s55, 0xe000
	s_nop 0
	global_load_lds_dwordx4 v[214:215], off
	s_waitcnt vmcnt(8)
	s_waitcnt lgkmcnt(0)
	v_mfma_f32_16x16x32_bf16 v[142:145], v[66:69], v[162:165], v[142:145]
	v_mfma_f32_16x16x32_bf16 v[138:141], v[82:85], v[162:165], v[138:141]
	v_mfma_f32_16x16x32_bf16 v[126:129], v[66:69], v[184:187], v[126:129]
	v_mfma_f32_16x16x32_bf16 v[122:125], v[82:85], v[184:187], v[122:125]
	s_barrier
	s_setprio 1
	s_waitcnt lgkmcnt(0)
	v_mfma_f32_16x16x32_bf16 v[110:113], v[66:69], v[192:195], v[110:113]
	v_mfma_f32_16x16x32_bf16 v[106:109], v[82:85], v[192:195], v[106:109]
	v_mfma_f32_16x16x32_bf16 v[94:97], v[66:69], v[206:209], v[94:97]
	v_mfma_f32_16x16x32_bf16 v[90:93], v[82:85], v[206:209], v[90:93]
	v_mfma_f32_16x16x32_bf16 v[142:145], v[70:73], v[166:169], v[142:145]
	v_mfma_f32_16x16x32_bf16 v[138:141], v[86:89], v[166:169], v[138:141]
	v_mfma_f32_16x16x32_bf16 v[126:129], v[70:73], v[188:191], v[126:129]
	v_mfma_f32_16x16x32_bf16 v[122:125], v[86:89], v[188:191], v[122:125]
	v_mfma_f32_16x16x32_bf16 v[110:113], v[70:73], v[202:205], v[110:113]
	v_mfma_f32_16x16x32_bf16 v[106:109], v[86:89], v[202:205], v[106:109]
	v_mfma_f32_16x16x32_bf16 v[94:97], v[70:73], v[210:213], v[94:97]
	v_mfma_f32_16x16x32_bf16 v[90:93], v[86:89], v[210:213], v[90:93]
	s_setprio 0
	s_setprio 1
	v_mfma_f32_16x16x32_bf16 v[134:137], v[146:149], v[162:165], v[134:137]
	v_mfma_f32_16x16x32_bf16 v[130:133], v[154:157], v[162:165], v[130:133]
	v_mfma_f32_16x16x32_bf16 v[118:121], v[146:149], v[184:187], v[118:121]
	v_mfma_f32_16x16x32_bf16 v[114:117], v[154:157], v[184:187], v[114:117]
	v_mfma_f32_16x16x32_bf16 v[102:105], v[146:149], v[192:195], v[102:105]
	v_mfma_f32_16x16x32_bf16 v[98:101], v[154:157], v[192:195], v[98:101]
	v_mfma_f32_16x16x32_bf16 v[78:81], v[146:149], v[206:209], v[78:81]
	v_mfma_f32_16x16x32_bf16 v[74:77], v[154:157], v[206:209], v[74:77]
	v_mfma_f32_16x16x32_bf16 v[134:137], v[150:153], v[166:169], v[134:137]
	v_mfma_f32_16x16x32_bf16 v[130:133], v[158:161], v[166:169], v[130:133]
	v_mfma_f32_16x16x32_bf16 v[118:121], v[150:153], v[188:191], v[118:121]
	v_mfma_f32_16x16x32_bf16 v[114:117], v[158:161], v[188:191], v[114:117]
	v_mfma_f32_16x16x32_bf16 v[102:105], v[150:153], v[202:205], v[102:105]
	v_mfma_f32_16x16x32_bf16 v[98:101], v[158:161], v[202:205], v[98:101]
	v_mfma_f32_16x16x32_bf16 v[78:81], v[150:153], v[210:213], v[78:81]
	v_mfma_f32_16x16x32_bf16 v[74:77], v[158:161], v[210:213], v[74:77]
	s_setprio 0
	s_barrier
	v_lshl_add_u64 v[214:215], s[26:27], 0, v[170:171]
	s_add_i32 s26, s67, s35
	s_mov_b32 m0, s26
	ds_read_b128 v[162:165], v201 offset:16384
	ds_read_b128 v[166:169], v201 offset:17408
	ds_read_b128 v[184:187], v201 offset:18432
	ds_read_b128 v[188:191], v201 offset:19456
	ds_read_b128 v[192:195], v201 offset:20480
	ds_read_b128 v[202:205], v201 offset:21504
	ds_read_b128 v[206:209], v201 offset:22528
	ds_read_b128 v[210:213], v201 offset:23552
	global_load_lds_dwordx4 v[214:215], off
	v_lshl_add_u64 v[216:217], v[214:215], 0, s[6:7]
	s_add_i32 m0, s26, 0x2000
	s_add_i32 s26, s68, s35
	global_load_lds_dwordx4 v[216:217], off
	v_lshl_add_u64 v[216:217], v[214:215], 0, s[10:11]
	s_mov_b32 m0, s26
	v_lshl_add_u64 v[220:221], s[58:59], 0, v[174:175]
	global_load_lds_dwordx4 v[216:217], off
	v_lshl_add_u64 v[216:217], v[214:215], 0, s[12:13]
	s_add_i32 m0, s26, 0x2000
	s_nop 0
	global_load_lds_dwordx4 v[216:217], off
	v_lshl_add_u64 v[216:217], s[58:59], 0, v[172:173]
	s_mov_b32 m0, s55
	s_nop 0
	global_load_lds_dwordx4 v[216:217], off
	s_mov_b32 m0, s60
	s_nop 0
	global_load_lds_dwordx4 v[220:221], off
	s_waitcnt vmcnt(8)
	s_waitcnt lgkmcnt(0)
	v_mfma_f32_16x16x32_bf16 v[62:65], v[66:69], v[162:165], v[62:65]
	v_mfma_f32_16x16x32_bf16 v[58:61], v[82:85], v[162:165], v[58:61]
	v_mfma_f32_16x16x32_bf16 v[46:49], v[66:69], v[184:187], v[46:49]
	v_mfma_f32_16x16x32_bf16 v[42:45], v[82:85], v[184:187], v[42:45]
	s_barrier
	s_setprio 1
	s_waitcnt lgkmcnt(0)
	v_mfma_f32_16x16x32_bf16 v[30:33], v[66:69], v[192:195], v[30:33]
	v_mfma_f32_16x16x32_bf16 v[26:29], v[82:85], v[192:195], v[26:29]
	v_mfma_f32_16x16x32_bf16 v[14:17], v[66:69], v[206:209], v[14:17]
	v_mfma_f32_16x16x32_bf16 v[10:13], v[82:85], v[206:209], v[10:13]
	v_mfma_f32_16x16x32_bf16 v[62:65], v[70:73], v[166:169], v[62:65]
	v_mfma_f32_16x16x32_bf16 v[58:61], v[86:89], v[166:169], v[58:61]
	v_mfma_f32_16x16x32_bf16 v[46:49], v[70:73], v[188:191], v[46:49]
	v_mfma_f32_16x16x32_bf16 v[42:45], v[86:89], v[188:191], v[42:45]
	v_mfma_f32_16x16x32_bf16 v[30:33], v[70:73], v[202:205], v[30:33]
	v_mfma_f32_16x16x32_bf16 v[26:29], v[86:89], v[202:205], v[26:29]
	v_mfma_f32_16x16x32_bf16 v[14:17], v[70:73], v[210:213], v[14:17]
	v_mfma_f32_16x16x32_bf16 v[10:13], v[86:89], v[210:213], v[10:13]
	s_setprio 0
	s_setprio 1
	v_mfma_f32_16x16x32_bf16 v[54:57], v[146:149], v[162:165], v[54:57]
	v_mfma_f32_16x16x32_bf16 v[50:53], v[154:157], v[162:165], v[50:53]
	v_mfma_f32_16x16x32_bf16 v[38:41], v[146:149], v[184:187], v[38:41]
	v_mfma_f32_16x16x32_bf16 v[34:37], v[154:157], v[184:187], v[34:37]
	v_mfma_f32_16x16x32_bf16 v[22:25], v[146:149], v[192:195], v[22:25]
	v_mfma_f32_16x16x32_bf16 v[18:21], v[154:157], v[192:195], v[18:21]
	v_mfma_f32_16x16x32_bf16 v[6:9], v[146:149], v[206:209], v[6:9]
	v_mfma_f32_16x16x32_bf16 v[2:5], v[154:157], v[206:209], v[2:5]
	v_mfma_f32_16x16x32_bf16 v[54:57], v[150:153], v[166:169], v[54:57]
	v_mfma_f32_16x16x32_bf16 v[50:53], v[158:161], v[166:169], v[50:53]
	v_mfma_f32_16x16x32_bf16 v[38:41], v[150:153], v[188:191], v[38:41]
	v_mfma_f32_16x16x32_bf16 v[34:37], v[158:161], v[188:191], v[34:37]
	v_mfma_f32_16x16x32_bf16 v[22:25], v[150:153], v[202:205], v[22:25]
	v_mfma_f32_16x16x32_bf16 v[18:21], v[158:161], v[202:205], v[18:21]
	v_mfma_f32_16x16x32_bf16 v[6:9], v[150:153], v[210:213], v[6:9]
	v_mfma_f32_16x16x32_bf16 v[2:5], v[158:161], v[210:213], v[2:5]
	s_setprio 0
	s_barrier
	s_add_i32 s74, 0, 0x18000
	s_add_i32 s75, 0, 0x1c000
	v_add_u32_e32 v86, s74, v197
	v_add_u32_e32 v158, s75, v197
	ds_read_b128 v[66:69], v86
	ds_read_b128 v[70:73], v86 offset:1024
	ds_read_b128 v[82:85], v86 offset:2048
	ds_read_b128 v[86:89], v86 offset:3072
	ds_read_b128 v[146:149], v158
	ds_read_b128 v[150:153], v158 offset:1024
	ds_read_b128 v[154:157], v158 offset:2048
	ds_read_b128 v[158:161], v158 offset:3072
	s_add_u32 s26, s58, 0x40000
	s_addc_u32 s27, s59, 0
	s_mov_b32 m0, s61
	v_lshl_add_u64 v[222:223], s[26:27], 0, v[172:173]
	ds_read_b128 v[162:165], v201 offset:32768
	ds_read_b128 v[166:169], v201 offset:33792
	ds_read_b128 v[184:187], v201 offset:34816
	ds_read_b128 v[188:191], v201 offset:35840
	ds_read_b128 v[192:195], v201 offset:36864
	ds_read_b128 v[202:205], v201 offset:37888
	ds_read_b128 v[206:209], v201 offset:38912
	ds_read_b128 v[210:213], v201 offset:39936
	global_load_lds_dwordx4 v[222:223], off
	v_lshl_add_u64 v[222:223], s[26:27], 0, v[174:175]
	s_mov_b32 m0, s62
	s_nop 0
	global_load_lds_dwordx4 v[222:223], off
	s_waitcnt vmcnt(8)
	s_waitcnt lgkmcnt(0)
	v_mfma_f32_16x16x32_bf16 v[142:145], v[66:69], v[162:165], v[142:145]
	v_mfma_f32_16x16x32_bf16 v[138:141], v[82:85], v[162:165], v[138:141]
	v_mfma_f32_16x16x32_bf16 v[126:129], v[66:69], v[184:187], v[126:129]
	v_mfma_f32_16x16x32_bf16 v[122:125], v[82:85], v[184:187], v[122:125]
	s_barrier
	s_setprio 1
	s_waitcnt lgkmcnt(0)
	v_mfma_f32_16x16x32_bf16 v[110:113], v[66:69], v[192:195], v[110:113]
	v_mfma_f32_16x16x32_bf16 v[106:109], v[82:85], v[192:195], v[106:109]
	v_mfma_f32_16x16x32_bf16 v[94:97], v[66:69], v[206:209], v[94:97]
	v_mfma_f32_16x16x32_bf16 v[90:93], v[82:85], v[206:209], v[90:93]
	v_mfma_f32_16x16x32_bf16 v[142:145], v[70:73], v[166:169], v[142:145]
	v_mfma_f32_16x16x32_bf16 v[138:141], v[86:89], v[166:169], v[138:141]
	v_mfma_f32_16x16x32_bf16 v[126:129], v[70:73], v[188:191], v[126:129]
	v_mfma_f32_16x16x32_bf16 v[122:125], v[86:89], v[188:191], v[122:125]
	v_mfma_f32_16x16x32_bf16 v[110:113], v[70:73], v[202:205], v[110:113]
	v_mfma_f32_16x16x32_bf16 v[106:109], v[86:89], v[202:205], v[106:109]
	v_mfma_f32_16x16x32_bf16 v[94:97], v[70:73], v[210:213], v[94:97]
	v_mfma_f32_16x16x32_bf16 v[90:93], v[86:89], v[210:213], v[90:93]
	s_setprio 0
	s_setprio 1
	v_mfma_f32_16x16x32_bf16 v[134:137], v[146:149], v[162:165], v[134:137]
	v_mfma_f32_16x16x32_bf16 v[130:133], v[154:157], v[162:165], v[130:133]
	v_mfma_f32_16x16x32_bf16 v[118:121], v[146:149], v[184:187], v[118:121]
	v_mfma_f32_16x16x32_bf16 v[114:117], v[154:157], v[184:187], v[114:117]
	v_mfma_f32_16x16x32_bf16 v[102:105], v[146:149], v[192:195], v[102:105]
	v_mfma_f32_16x16x32_bf16 v[98:101], v[154:157], v[192:195], v[98:101]
	v_mfma_f32_16x16x32_bf16 v[78:81], v[146:149], v[206:209], v[78:81]
	v_mfma_f32_16x16x32_bf16 v[74:77], v[154:157], v[206:209], v[74:77]
	v_mfma_f32_16x16x32_bf16 v[134:137], v[150:153], v[166:169], v[134:137]
	v_mfma_f32_16x16x32_bf16 v[130:133], v[158:161], v[166:169], v[130:133]
	v_mfma_f32_16x16x32_bf16 v[118:121], v[150:153], v[188:191], v[118:121]
	v_mfma_f32_16x16x32_bf16 v[114:117], v[158:161], v[188:191], v[114:117]
	v_mfma_f32_16x16x32_bf16 v[102:105], v[150:153], v[202:205], v[102:105]
	v_mfma_f32_16x16x32_bf16 v[98:101], v[158:161], v[202:205], v[98:101]
	v_mfma_f32_16x16x32_bf16 v[78:81], v[150:153], v[210:213], v[78:81]
	v_mfma_f32_16x16x32_bf16 v[74:77], v[158:161], v[210:213], v[74:77]
	s_setprio 0
	s_barrier
	s_add_i32 s26, s74, s35
	v_lshl_add_u64 v[222:223], v[214:215], 0, s[16:17]
	s_mov_b32 m0, s26
	ds_read_b128 v[162:165], v201 offset:49152
	ds_read_b128 v[166:169], v201 offset:50176
	ds_read_b128 v[184:187], v201 offset:51200
	ds_read_b128 v[188:191], v201 offset:52224
	ds_read_b128 v[192:195], v201 offset:53248
	ds_read_b128 v[202:205], v201 offset:54272
	ds_read_b128 v[206:209], v201 offset:55296
	ds_read_b128 v[210:213], v201 offset:56320
	global_load_lds_dwordx4 v[222:223], off
	v_lshl_add_u64 v[222:223], v[214:215], 0, s[18:19]
	s_add_i32 m0, s26, 0x2000
	s_add_i32 s26, s75, s35
	global_load_lds_dwordx4 v[222:223], off
	v_lshl_add_u64 v[222:223], v[214:215], 0, s[22:23]
	s_mov_b32 m0, s26
	v_lshl_add_u64 v[214:215], v[214:215], 0, s[24:25]
	global_load_lds_dwordx4 v[222:223], off
	s_add_i32 m0, s26, 0x2000
	s_nop 0
	global_load_lds_dwordx4 v[214:215], off
	v_lshl_add_u64 v[214:215], v[216:217], 0, s[20:21]
	s_mov_b32 m0, s64
	s_nop 0
	global_load_lds_dwordx4 v[214:215], off
	v_lshl_add_u64 v[214:215], v[220:221], 0, s[20:21]
	s_mov_b32 m0, s65
	s_nop 0
	global_load_lds_dwordx4 v[214:215], off
	s_waitcnt vmcnt(8)
	s_waitcnt lgkmcnt(0)
	v_mfma_f32_16x16x32_bf16 v[62:65], v[66:69], v[162:165], v[62:65]
	v_mfma_f32_16x16x32_bf16 v[58:61], v[82:85], v[162:165], v[58:61]
	v_mfma_f32_16x16x32_bf16 v[46:49], v[66:69], v[184:187], v[46:49]
	v_mfma_f32_16x16x32_bf16 v[42:45], v[82:85], v[184:187], v[42:45]
	s_barrier
	s_setprio 1
	s_waitcnt lgkmcnt(0)
	v_mfma_f32_16x16x32_bf16 v[30:33], v[66:69], v[192:195], v[30:33]
	v_mfma_f32_16x16x32_bf16 v[26:29], v[82:85], v[192:195], v[26:29]
	v_mfma_f32_16x16x32_bf16 v[14:17], v[66:69], v[206:209], v[14:17]
	v_mfma_f32_16x16x32_bf16 v[10:13], v[82:85], v[206:209], v[10:13]
	v_mfma_f32_16x16x32_bf16 v[62:65], v[70:73], v[166:169], v[62:65]
	v_mfma_f32_16x16x32_bf16 v[58:61], v[86:89], v[166:169], v[58:61]
	v_mfma_f32_16x16x32_bf16 v[46:49], v[70:73], v[188:191], v[46:49]
	v_mfma_f32_16x16x32_bf16 v[42:45], v[86:89], v[188:191], v[42:45]
	v_mfma_f32_16x16x32_bf16 v[30:33], v[70:73], v[202:205], v[30:33]
	v_mfma_f32_16x16x32_bf16 v[26:29], v[86:89], v[202:205], v[26:29]
	v_mfma_f32_16x16x32_bf16 v[14:17], v[70:73], v[210:213], v[14:17]
	v_mfma_f32_16x16x32_bf16 v[10:13], v[86:89], v[210:213], v[10:13]
	s_setprio 0
	s_setprio 1
	v_mfma_f32_16x16x32_bf16 v[54:57], v[146:149], v[162:165], v[54:57]
	v_mfma_f32_16x16x32_bf16 v[50:53], v[154:157], v[162:165], v[50:53]
	v_mfma_f32_16x16x32_bf16 v[38:41], v[146:149], v[184:187], v[38:41]
	v_mfma_f32_16x16x32_bf16 v[34:37], v[154:157], v[184:187], v[34:37]
	v_mfma_f32_16x16x32_bf16 v[22:25], v[146:149], v[192:195], v[22:25]
	v_mfma_f32_16x16x32_bf16 v[18:21], v[154:157], v[192:195], v[18:21]
	v_mfma_f32_16x16x32_bf16 v[6:9], v[146:149], v[206:209], v[6:9]
	v_mfma_f32_16x16x32_bf16 v[2:5], v[154:157], v[206:209], v[2:5]
	v_mfma_f32_16x16x32_bf16 v[54:57], v[150:153], v[166:169], v[54:57]
	v_mfma_f32_16x16x32_bf16 v[50:53], v[158:161], v[166:169], v[50:53]
	v_mfma_f32_16x16x32_bf16 v[38:41], v[150:153], v[188:191], v[38:41]
	v_mfma_f32_16x16x32_bf16 v[34:37], v[158:161], v[188:191], v[34:37]
	v_mfma_f32_16x16x32_bf16 v[22:25], v[150:153], v[202:205], v[22:25]
	v_mfma_f32_16x16x32_bf16 v[18:21], v[158:161], v[202:205], v[18:21]
	v_mfma_f32_16x16x32_bf16 v[6:9], v[150:153], v[210:213], v[6:9]
	v_mfma_f32_16x16x32_bf16 v[2:5], v[158:161], v[210:213], v[2:5]
	s_setprio 0
	s_barrier
	s_add_i32 s73, s73, 2
	s_add_u32 s71, s71, 0x10000
	s_addc_u32 s72, s72, 0
	s_add_u32 s56, s56, 0x100
	s_addc_u32 s57, s57, 0
	s_cmp_gt_u32 s73, 13
	s_cbranch_scc0 .LBB0_1192
	s_and_b64 vcc, exec, s[36:37]
	s_cbranch_vccz .LBB0_1195
	s_barrier

.LBB0_1271:
	ds_read_b128 v[144:147], v158
	ds_read_b128 v[148:151], v158 offset:1024
	ds_read_b128 v[152:155], v158 offset:2048
	ds_read_b128 v[162:165], v158 offset:3072
	ds_read_b128 v[166:169], v159
	ds_read_b128 v[170:173], v159 offset:1024
	ds_read_b128 v[174:177], v159 offset:2048
	ds_read_b128 v[178:181], v159 offset:3072
	s_add_u32 s26, s58, 0xfff80080
	s_addc_u32 s27, s59, -1
	s_cmp_eq_u32 s80, 28
	s_cselect_b32 s61, s51, s27
	s_cselect_b32 s60, s57, s26
	s_cselect_b32 s27, s45, s75
	s_cselect_b32 s26, s73, s74
	v_lshl_add_u64 v[214:215], s[58:59], 0, v[136:137]
	s_add_i32 m0, s63, 0xc000
	ds_read_b128 v[182:185], v160
	ds_read_b128 v[186:189], v160 offset:1024
	ds_read_b128 v[190:193], v160 offset:2048
	ds_read_b128 v[194:197], v160 offset:3072
	ds_read_b128 v[198:201], v160 offset:4096
	ds_read_b128 v[202:205], v160 offset:5120
	ds_read_b128 v[206:209], v160 offset:6144
	ds_read_b128 v[210:213], v160 offset:7168
	global_load_lds_dwordx4 v[214:215], off
	v_lshl_add_u64 v[214:215], s[58:59], 0, v[138:139]
	s_add_i32 m0, s63, 0xe000
	s_nop 0
	global_load_lds_dwordx4 v[214:215], off
	s_waitcnt vmcnt(8)
	s_waitcnt lgkmcnt(0)
	v_mfma_f32_16x16x32_bf16 v[126:129], v[144:147], v[182:185], v[126:129]
	v_mfma_f32_16x16x32_bf16 v[122:125], v[152:155], v[182:185], v[122:125]
	v_mfma_f32_16x16x32_bf16 v[118:121], v[144:147], v[190:193], v[118:121]
	v_mfma_f32_16x16x32_bf16 v[114:117], v[152:155], v[190:193], v[114:117]
	s_barrier
	s_setprio 1
	s_waitcnt lgkmcnt(0)
	v_mfma_f32_16x16x32_bf16 v[106:109], v[144:147], v[198:201], v[106:109]
	v_mfma_f32_16x16x32_bf16 v[98:101], v[152:155], v[198:201], v[98:101]
	v_mfma_f32_16x16x32_bf16 v[90:93], v[144:147], v[206:209], v[90:93]
	v_mfma_f32_16x16x32_bf16 v[82:85], v[152:155], v[206:209], v[82:85]
	v_mfma_f32_16x16x32_bf16 v[126:129], v[148:151], v[186:189], v[126:129]
	v_mfma_f32_16x16x32_bf16 v[122:125], v[162:165], v[186:189], v[122:125]
	v_mfma_f32_16x16x32_bf16 v[118:121], v[148:151], v[194:197], v[118:121]
	v_mfma_f32_16x16x32_bf16 v[114:117], v[162:165], v[194:197], v[114:117]
	v_mfma_f32_16x16x32_bf16 v[106:109], v[148:151], v[202:205], v[106:109]
	v_mfma_f32_16x16x32_bf16 v[98:101], v[162:165], v[202:205], v[98:101]
	v_mfma_f32_16x16x32_bf16 v[90:93], v[148:151], v[210:213], v[90:93]
	v_mfma_f32_16x16x32_bf16 v[82:85], v[162:165], v[210:213], v[82:85]
	s_setprio 0
	s_setprio 1
	v_mfma_f32_16x16x32_bf16 v[110:113], v[166:169], v[182:185], v[110:113]
	v_mfma_f32_16x16x32_bf16 v[102:105], v[174:177], v[182:185], v[102:105]
	v_mfma_f32_16x16x32_bf16 v[94:97], v[166:169], v[190:193], v[94:97]
	v_mfma_f32_16x16x32_bf16 v[86:89], v[174:177], v[190:193], v[86:89]
	v_mfma_f32_16x16x32_bf16 v[78:81], v[166:169], v[198:201], v[78:81]
	v_mfma_f32_16x16x32_bf16 v[74:77], v[174:177], v[198:201], v[74:77]
	v_mfma_f32_16x16x32_bf16 v[70:73], v[166:169], v[206:209], v[70:73]
	v_mfma_f32_16x16x32_bf16 v[66:69], v[174:177], v[206:209], v[66:69]
	v_mfma_f32_16x16x32_bf16 v[110:113], v[170:173], v[186:189], v[110:113]
	v_mfma_f32_16x16x32_bf16 v[102:105], v[178:181], v[186:189], v[102:105]
	v_mfma_f32_16x16x32_bf16 v[94:97], v[170:173], v[194:197], v[94:97]
	v_mfma_f32_16x16x32_bf16 v[86:89], v[178:181], v[194:197], v[86:89]
	v_mfma_f32_16x16x32_bf16 v[78:81], v[170:173], v[202:205], v[78:81]
	v_mfma_f32_16x16x32_bf16 v[74:77], v[178:181], v[202:205], v[74:77]
	v_mfma_f32_16x16x32_bf16 v[70:73], v[170:173], v[210:213], v[70:73]
	v_mfma_f32_16x16x32_bf16 v[66:69], v[178:181], v[210:213], v[66:69]
	s_setprio 0
	s_barrier
	v_lshl_add_u64 v[214:215], s[26:27], 0, v[130:131]
	s_add_i32 s26, s71, s35
	s_mov_b32 m0, s26
	ds_read_b128 v[182:185], v160 offset:16384
	ds_read_b128 v[186:189], v160 offset:17408
	ds_read_b128 v[190:193], v160 offset:18432
	ds_read_b128 v[194:197], v160 offset:19456
	ds_read_b128 v[198:201], v160 offset:20480
	ds_read_b128 v[202:205], v160 offset:21504
	ds_read_b128 v[206:209], v160 offset:22528
	ds_read_b128 v[210:213], v160 offset:23552
	global_load_lds_dwordx4 v[214:215], off
	v_lshl_add_u64 v[216:217], v[214:215], 0, s[6:7]
	s_add_i32 m0, s26, 0x2000
	s_add_i32 s26, s72, s35
	global_load_lds_dwordx4 v[216:217], off
	v_lshl_add_u64 v[216:217], v[214:215], 0, s[8:9]
	s_mov_b32 m0, s26
	v_lshl_add_u64 v[220:221], s[60:61], 0, v[134:135]
	global_load_lds_dwordx4 v[216:217], off
	v_lshl_add_u64 v[216:217], v[214:215], 0, s[10:11]
	s_add_i32 m0, s26, 0x2000
	s_nop 0
	global_load_lds_dwordx4 v[216:217], off
	v_lshl_add_u64 v[216:217], s[60:61], 0, v[132:133]
	s_mov_b32 m0, s63
	s_nop 0
	global_load_lds_dwordx4 v[216:217], off
	s_mov_b32 m0, s64
	s_nop 0
	global_load_lds_dwordx4 v[220:221], off
	s_waitcnt vmcnt(8)
	s_waitcnt lgkmcnt(0)
	v_mfma_f32_16x16x32_bf16 v[62:65], v[144:147], v[182:185], v[62:65]
	v_mfma_f32_16x16x32_bf16 v[58:61], v[152:155], v[182:185], v[58:61]
	v_mfma_f32_16x16x32_bf16 v[54:57], v[144:147], v[190:193], v[54:57]
	v_mfma_f32_16x16x32_bf16 v[46:49], v[152:155], v[190:193], v[46:49]
	s_barrier
	s_setprio 1
	s_waitcnt lgkmcnt(0)
	v_mfma_f32_16x16x32_bf16 v[38:41], v[144:147], v[198:201], v[38:41]
	v_mfma_f32_16x16x32_bf16 v[30:33], v[152:155], v[198:201], v[30:33]
	v_mfma_f32_16x16x32_bf16 v[22:25], v[144:147], v[206:209], v[22:25]
	v_mfma_f32_16x16x32_bf16 v[14:17], v[152:155], v[206:209], v[14:17]
	v_mfma_f32_16x16x32_bf16 v[62:65], v[148:151], v[186:189], v[62:65]
	v_mfma_f32_16x16x32_bf16 v[58:61], v[162:165], v[186:189], v[58:61]
	v_mfma_f32_16x16x32_bf16 v[54:57], v[148:151], v[194:197], v[54:57]
	v_mfma_f32_16x16x32_bf16 v[46:49], v[162:165], v[194:197], v[46:49]
	v_mfma_f32_16x16x32_bf16 v[38:41], v[148:151], v[202:205], v[38:41]
	v_mfma_f32_16x16x32_bf16 v[30:33], v[162:165], v[202:205], v[30:33]
	v_mfma_f32_16x16x32_bf16 v[22:25], v[148:151], v[210:213], v[22:25]
	v_mfma_f32_16x16x32_bf16 v[14:17], v[162:165], v[210:213], v[14:17]
	s_setprio 0
	s_setprio 1
	v_mfma_f32_16x16x32_bf16 v[50:53], v[166:169], v[182:185], v[50:53]
	v_mfma_f32_16x16x32_bf16 v[42:45], v[174:177], v[182:185], v[42:45]
	v_mfma_f32_16x16x32_bf16 v[34:37], v[166:169], v[190:193], v[34:37]
	v_mfma_f32_16x16x32_bf16 v[26:29], v[174:177], v[190:193], v[26:29]
	v_mfma_f32_16x16x32_bf16 v[18:21], v[166:169], v[198:201], v[18:21]
	v_mfma_f32_16x16x32_bf16 v[10:13], v[174:177], v[198:201], v[10:13]
	v_mfma_f32_16x16x32_bf16 v[6:9], v[166:169], v[206:209], v[6:9]
	v_mfma_f32_16x16x32_bf16 v[2:5], v[174:177], v[206:209], v[2:5]
	v_mfma_f32_16x16x32_bf16 v[50:53], v[170:173], v[186:189], v[50:53]
	v_mfma_f32_16x16x32_bf16 v[42:45], v[178:181], v[186:189], v[42:45]
	v_mfma_f32_16x16x32_bf16 v[34:37], v[170:173], v[194:197], v[34:37]
	v_mfma_f32_16x16x32_bf16 v[26:29], v[178:181], v[194:197], v[26:29]
	v_mfma_f32_16x16x32_bf16 v[18:21], v[170:173], v[202:205], v[18:21]
	v_mfma_f32_16x16x32_bf16 v[10:13], v[178:181], v[202:205], v[10:13]
	v_mfma_f32_16x16x32_bf16 v[6:9], v[170:173], v[210:213], v[6:9]
	v_mfma_f32_16x16x32_bf16 v[2:5], v[178:181], v[210:213], v[2:5]
	s_setprio 0
	s_barrier
	s_add_i32 s81, 0, 0x18000
	v_add_u32_e32 v161, s81, v156
	s_add_i32 s82, 0, 0x1c000
	ds_read_b128 v[144:147], v161
	ds_read_b128 v[148:151], v161 offset:1024
	ds_read_b128 v[152:155], v161 offset:2048
	ds_read_b128 v[162:165], v161 offset:3072
	v_add_u32_e32 v161, s82, v156
	ds_read_b128 v[166:169], v161
	ds_read_b128 v[170:173], v161 offset:1024
	ds_read_b128 v[174:177], v161 offset:2048
	ds_read_b128 v[178:181], v161 offset:3072
	s_add_u32 s26, s60, 0x80000
	s_addc_u32 s27, s61, 0
	s_mov_b32 m0, s65
	v_lshl_add_u64 v[222:223], s[26:27], 0, v[132:133]
	ds_read_b128 v[182:185], v160 offset:32768
	ds_read_b128 v[186:189], v160 offset:33792
	ds_read_b128 v[190:193], v160 offset:34816
	ds_read_b128 v[194:197], v160 offset:35840
	ds_read_b128 v[198:201], v160 offset:36864
	ds_read_b128 v[202:205], v160 offset:37888
	ds_read_b128 v[206:209], v160 offset:38912
	ds_read_b128 v[210:213], v160 offset:39936
	global_load_lds_dwordx4 v[222:223], off
	v_lshl_add_u64 v[222:223], s[26:27], 0, v[134:135]
	s_mov_b32 m0, s66
	s_nop 0
	global_load_lds_dwordx4 v[222:223], off
	s_waitcnt vmcnt(8)
	s_waitcnt lgkmcnt(0)
	v_mfma_f32_16x16x32_bf16 v[126:129], v[144:147], v[182:185], v[126:129]
	v_mfma_f32_16x16x32_bf16 v[122:125], v[152:155], v[182:185], v[122:125]
	v_mfma_f32_16x16x32_bf16 v[118:121], v[144:147], v[190:193], v[118:121]
	v_mfma_f32_16x16x32_bf16 v[114:117], v[152:155], v[190:193], v[114:117]
	s_barrier
	s_setprio 1
	s_waitcnt lgkmcnt(0)
	v_mfma_f32_16x16x32_bf16 v[106:109], v[144:147], v[198:201], v[106:109]
	v_mfma_f32_16x16x32_bf16 v[98:101], v[152:155], v[198:201], v[98:101]
	v_mfma_f32_16x16x32_bf16 v[90:93], v[144:147], v[206:209], v[90:93]
	v_mfma_f32_16x16x32_bf16 v[82:85], v[152:155], v[206:209], v[82:85]
	v_mfma_f32_16x16x32_bf16 v[126:129], v[148:151], v[186:189], v[126:129]
	v_mfma_f32_16x16x32_bf16 v[122:125], v[162:165], v[186:189], v[122:125]
	v_mfma_f32_16x16x32_bf16 v[118:121], v[148:151], v[194:197], v[118:121]
	v_mfma_f32_16x16x32_bf16 v[114:117], v[162:165], v[194:197], v[114:117]
	v_mfma_f32_16x16x32_bf16 v[106:109], v[148:151], v[202:205], v[106:109]
	v_mfma_f32_16x16x32_bf16 v[98:101], v[162:165], v[202:205], v[98:101]
	v_mfma_f32_16x16x32_bf16 v[90:93], v[148:151], v[210:213], v[90:93]
	v_mfma_f32_16x16x32_bf16 v[82:85], v[162:165], v[210:213], v[82:85]
	s_setprio 0
	s_setprio 1
	v_mfma_f32_16x16x32_bf16 v[110:113], v[166:169], v[182:185], v[110:113]
	v_mfma_f32_16x16x32_bf16 v[102:105], v[174:177], v[182:185], v[102:105]
	v_mfma_f32_16x16x32_bf16 v[94:97], v[166:169], v[190:193], v[94:97]
	v_mfma_f32_16x16x32_bf16 v[86:89], v[174:177], v[190:193], v[86:89]
	v_mfma_f32_16x16x32_bf16 v[78:81], v[166:169], v[198:201], v[78:81]
	v_mfma_f32_16x16x32_bf16 v[74:77], v[174:177], v[198:201], v[74:77]
	v_mfma_f32_16x16x32_bf16 v[70:73], v[166:169], v[206:209], v[70:73]
	v_mfma_f32_16x16x32_bf16 v[66:69], v[174:177], v[206:209], v[66:69]
	v_mfma_f32_16x16x32_bf16 v[110:113], v[170:173], v[186:189], v[110:113]
	v_mfma_f32_16x16x32_bf16 v[102:105], v[178:181], v[186:189], v[102:105]
	v_mfma_f32_16x16x32_bf16 v[94:97], v[170:173], v[194:197], v[94:97]
	v_mfma_f32_16x16x32_bf16 v[86:89], v[178:181], v[194:197], v[86:89]
	v_mfma_f32_16x16x32_bf16 v[78:81], v[170:173], v[202:205], v[78:81]
	v_mfma_f32_16x16x32_bf16 v[74:77], v[178:181], v[202:205], v[74:77]
	v_mfma_f32_16x16x32_bf16 v[70:73], v[170:173], v[210:213], v[70:73]
	v_mfma_f32_16x16x32_bf16 v[66:69], v[178:181], v[210:213], v[66:69]
	s_setprio 0
	s_barrier
	s_add_i32 s26, s81, s35
	v_lshl_add_u64 v[222:223], v[214:215], 0, s[14:15]
	s_mov_b32 m0, s26
	ds_read_b128 v[182:185], v160 offset:49152
	ds_read_b128 v[186:189], v160 offset:50176
	ds_read_b128 v[190:193], v160 offset:51200
	ds_read_b128 v[194:197], v160 offset:52224
	ds_read_b128 v[198:201], v160 offset:53248
	ds_read_b128 v[202:205], v160 offset:54272
	ds_read_b128 v[206:209], v160 offset:55296
	ds_read_b128 v[210:213], v160 offset:56320
	global_load_lds_dwordx4 v[222:223], off
	v_lshl_add_u64 v[222:223], v[214:215], 0, s[16:17]
	s_add_i32 m0, s26, 0x2000
	s_add_i32 s26, s82, s35
	global_load_lds_dwordx4 v[222:223], off
	v_lshl_add_u64 v[222:223], v[214:215], 0, s[20:21]
	s_mov_b32 m0, s26
	v_lshl_add_u64 v[214:215], v[214:215], 0, s[22:23]
	global_load_lds_dwordx4 v[222:223], off
	s_add_i32 m0, s26, 0x2000
	s_nop 0
	global_load_lds_dwordx4 v[214:215], off
	v_lshl_add_u64 v[214:215], v[216:217], 0, s[18:19]
	s_mov_b32 m0, s68
	s_nop 0
	global_load_lds_dwordx4 v[214:215], off
	v_lshl_add_u64 v[214:215], v[220:221], 0, s[18:19]
	s_mov_b32 m0, s69
	s_nop 0
	global_load_lds_dwordx4 v[214:215], off
	s_waitcnt vmcnt(8)
	s_waitcnt lgkmcnt(0)
	v_mfma_f32_16x16x32_bf16 v[62:65], v[144:147], v[182:185], v[62:65]
	v_mfma_f32_16x16x32_bf16 v[58:61], v[152:155], v[182:185], v[58:61]
	v_mfma_f32_16x16x32_bf16 v[54:57], v[144:147], v[190:193], v[54:57]
	v_mfma_f32_16x16x32_bf16 v[46:49], v[152:155], v[190:193], v[46:49]
	s_barrier
	s_setprio 1
	s_waitcnt lgkmcnt(0)
	v_mfma_f32_16x16x32_bf16 v[38:41], v[144:147], v[198:201], v[38:41]
	v_mfma_f32_16x16x32_bf16 v[30:33], v[152:155], v[198:201], v[30:33]
	v_mfma_f32_16x16x32_bf16 v[22:25], v[144:147], v[206:209], v[22:25]
	v_mfma_f32_16x16x32_bf16 v[14:17], v[152:155], v[206:209], v[14:17]
	v_mfma_f32_16x16x32_bf16 v[62:65], v[148:151], v[186:189], v[62:65]
	v_mfma_f32_16x16x32_bf16 v[58:61], v[162:165], v[186:189], v[58:61]
	v_mfma_f32_16x16x32_bf16 v[54:57], v[148:151], v[194:197], v[54:57]
	v_mfma_f32_16x16x32_bf16 v[46:49], v[162:165], v[194:197], v[46:49]
	v_mfma_f32_16x16x32_bf16 v[38:41], v[148:151], v[202:205], v[38:41]
	v_mfma_f32_16x16x32_bf16 v[30:33], v[162:165], v[202:205], v[30:33]
	v_mfma_f32_16x16x32_bf16 v[22:25], v[148:151], v[210:213], v[22:25]
	v_mfma_f32_16x16x32_bf16 v[14:17], v[162:165], v[210:213], v[14:17]
	s_setprio 0
	s_setprio 1
	v_mfma_f32_16x16x32_bf16 v[50:53], v[166:169], v[182:185], v[50:53]
	v_mfma_f32_16x16x32_bf16 v[42:45], v[174:177], v[182:185], v[42:45]
	v_mfma_f32_16x16x32_bf16 v[34:37], v[166:169], v[190:193], v[34:37]
	v_mfma_f32_16x16x32_bf16 v[26:29], v[174:177], v[190:193], v[26:29]
	v_mfma_f32_16x16x32_bf16 v[18:21], v[166:169], v[198:201], v[18:21]
	v_mfma_f32_16x16x32_bf16 v[10:13], v[174:177], v[198:201], v[10:13]
	v_mfma_f32_16x16x32_bf16 v[6:9], v[166:169], v[206:209], v[6:9]
	v_mfma_f32_16x16x32_bf16 v[2:5], v[174:177], v[206:209], v[2:5]
	v_mfma_f32_16x16x32_bf16 v[50:53], v[170:173], v[186:189], v[50:53]
	v_mfma_f32_16x16x32_bf16 v[42:45], v[178:181], v[186:189], v[42:45]
	v_mfma_f32_16x16x32_bf16 v[34:37], v[170:173], v[194:197], v[34:37]
	v_mfma_f32_16x16x32_bf16 v[26:29], v[178:181], v[194:197], v[26:29]
	v_mfma_f32_16x16x32_bf16 v[18:21], v[170:173], v[202:205], v[18:21]
	v_mfma_f32_16x16x32_bf16 v[10:13], v[178:181], v[202:205], v[10:13]
	v_mfma_f32_16x16x32_bf16 v[6:9], v[170:173], v[210:213], v[6:9]
	v_mfma_f32_16x16x32_bf16 v[2:5], v[178:181], v[210:213], v[2:5]
	s_setprio 0
	s_barrier
	s_add_i32 s80, s80, 2
	s_add_u32 s74, s74, 0x10000
	s_addc_u32 s75, s75, 0
	s_add_u32 s58, s58, 0x100
	s_addc_u32 s59, s59, 0
	s_cmp_gt_u32 s80, 29
	s_cbranch_scc0 .LBB0_1271
	s_and_b64 vcc, exec, s[24:25]
	s_cbranch_vccz .LBB0_1274
	s_barrier

.LBB0_1497:
	ds_read_b128 v[26:29], v186
	ds_read_b128 v[30:33], v186 offset:1024
	ds_read_b128 v[18:21], v186 offset:2048
	ds_read_b128 v[22:25], v186 offset:3072
	ds_read_b128 v[10:13], v187
	ds_read_b128 v[14:17], v187 offset:1024
	ds_read_b128 v[2:5], v187 offset:2048
	ds_read_b128 v[6:9], v187 offset:3072
	s_add_u32 s56, s4, 0xfffc0080
	s_addc_u32 s57, s5, -1
	s_cmp_eq_u32 s49, 12
	s_cselect_b64 vcc, -1, 0
	s_cselect_b32 s57, s2, s57
	s_cselect_b32 s56, s47, s56
	v_cndmask_b32_e32 v179, v177, v175, vcc
	v_cndmask_b32_e32 v178, v176, v174, vcc
	v_lshl_add_u64 v[180:181], s[4:5], 0, v[168:169]
	s_add_i32 m0, s62, 0xc000
	ds_read_b128 v[192:195], v188
	ds_read_b128 v[196:199], v188 offset:1024
	ds_read_b128 v[200:203], v188 offset:2048
	ds_read_b128 v[204:207], v188 offset:3072
	ds_read_b128 v[208:211], v188 offset:4096
	ds_read_b128 v[212:215], v188 offset:5120
	ds_read_b128 v[220:223], v188 offset:6144
	ds_read_b128 v[224:227], v188 offset:7168
	global_load_lds_dwordx4 v[180:181], off
	v_lshl_add_u64 v[180:181], s[4:5], 0, v[170:171]
	s_add_i32 m0, s62, 0xe000
	s_nop 0
	global_load_lds_dwordx4 v[180:181], off
	s_waitcnt vmcnt(8)
	s_waitcnt lgkmcnt(0)
	v_mfma_scale_f32_16x16x128_f8f6f4 v[158:161], v[26:33], v[192:199], v[158:161], v189, v190 op_sel_hi:[0,0,0]
	v_mfma_scale_f32_16x16x128_f8f6f4 v[150:153], v[18:25], v[192:199], v[150:153], v189, v190 op_sel_hi:[0,0,0]
	s_barrier
	s_setprio 1
	s_waitcnt lgkmcnt(0)
	v_mfma_scale_f32_16x16x128_f8f6f4 v[142:145], v[26:33], v[200:207], v[142:145], v189, v190 op_sel_hi:[0,0,0]
	v_mfma_scale_f32_16x16x128_f8f6f4 v[134:137], v[18:25], v[200:207], v[134:137], v189, v190 op_sel_hi:[0,0,0]
	v_mfma_scale_f32_16x16x128_f8f6f4 v[126:129], v[26:33], v[208:215], v[126:129], v189, v190 op_sel_hi:[0,0,0]
	v_mfma_scale_f32_16x16x128_f8f6f4 v[118:121], v[18:25], v[208:215], v[118:121], v189, v190 op_sel_hi:[0,0,0]
	v_mfma_scale_f32_16x16x128_f8f6f4 v[110:113], v[26:33], v[220:227], v[110:113], v189, v190 op_sel_hi:[0,0,0]
	v_mfma_scale_f32_16x16x128_f8f6f4 v[102:105], v[18:25], v[220:227], v[102:105], v189, v190 op_sel_hi:[0,0,0]
	s_setprio 0
	s_setprio 1
	v_mfma_scale_f32_16x16x128_f8f6f4 v[154:157], v[10:17], v[192:199], v[154:157], v189, v190 op_sel_hi:[0,0,0]
	v_mfma_scale_f32_16x16x128_f8f6f4 v[146:149], v[2:9], v[192:199], v[146:149], v189, v190 op_sel_hi:[0,0,0]
	v_mfma_scale_f32_16x16x128_f8f6f4 v[138:141], v[10:17], v[200:207], v[138:141], v189, v190 op_sel_hi:[0,0,0]
	v_mfma_scale_f32_16x16x128_f8f6f4 v[130:133], v[2:9], v[200:207], v[130:133], v189, v190 op_sel_hi:[0,0,0]
	v_mfma_scale_f32_16x16x128_f8f6f4 v[122:125], v[10:17], v[208:215], v[122:125], v189, v190 op_sel_hi:[0,0,0]
	v_mfma_scale_f32_16x16x128_f8f6f4 v[114:117], v[2:9], v[208:215], v[114:117], v189, v190 op_sel_hi:[0,0,0]
	v_mfma_scale_f32_16x16x128_f8f6f4 v[106:109], v[10:17], v[220:227], v[106:109], v189, v190 op_sel_hi:[0,0,0]
	v_mfma_scale_f32_16x16x128_f8f6f4 v[98:101], v[2:9], v[220:227], v[98:101], v189, v190 op_sel_hi:[0,0,0]
	s_setprio 0
	s_barrier
	s_add_i32 s73, s69, s61
	v_lshl_add_u64 v[178:179], v[178:179], 0, v[162:163]
	s_mov_b32 m0, s73
	ds_read_b128 v[192:195], v188 offset:16384
	ds_read_b128 v[196:199], v188 offset:17408
	ds_read_b128 v[200:203], v188 offset:18432
	ds_read_b128 v[204:207], v188 offset:19456
	ds_read_b128 v[208:211], v188 offset:20480
	ds_read_b128 v[212:215], v188 offset:21504
	ds_read_b128 v[220:223], v188 offset:22528
	ds_read_b128 v[224:227], v188 offset:23552
	global_load_lds_dwordx4 v[178:179], off
	v_lshl_add_u64 v[180:181], v[178:179], 0, s[10:11]
	s_add_i32 m0, s73, 0x2000
	s_add_i32 s73, s70, s61
	global_load_lds_dwordx4 v[180:181], off
	v_lshl_add_u64 v[180:181], v[178:179], 0, s[12:13]
	s_mov_b32 m0, s73
	v_lshl_add_u64 v[182:183], s[56:57], 0, v[166:167]
	global_load_lds_dwordx4 v[180:181], off
	v_lshl_add_u64 v[180:181], v[178:179], 0, s[14:15]
	s_add_i32 m0, s73, 0x2000
	s_nop 0
	global_load_lds_dwordx4 v[180:181], off
	v_lshl_add_u64 v[180:181], s[56:57], 0, v[164:165]
	s_mov_b32 m0, s62
	s_nop 0
	global_load_lds_dwordx4 v[180:181], off
	s_mov_b32 m0, s53
	s_nop 0
	global_load_lds_dwordx4 v[182:183], off
	s_waitcnt vmcnt(8)
	s_waitcnt lgkmcnt(0)
	v_mfma_scale_f32_16x16x128_f8f6f4 v[94:97], v[26:33], v[192:199], v[94:97], v189, v190 op_sel_hi:[0,0,0]
	v_mfma_scale_f32_16x16x128_f8f6f4 v[86:89], v[18:25], v[192:199], v[86:89], v189, v190 op_sel_hi:[0,0,0]
	s_barrier
	s_setprio 1
	s_waitcnt lgkmcnt(0)
	v_mfma_scale_f32_16x16x128_f8f6f4 v[78:81], v[26:33], v[200:207], v[78:81], v189, v190 op_sel_hi:[0,0,0]
	v_mfma_scale_f32_16x16x128_f8f6f4 v[70:73], v[18:25], v[200:207], v[70:73], v189, v190 op_sel_hi:[0,0,0]
	v_mfma_scale_f32_16x16x128_f8f6f4 v[62:65], v[26:33], v[208:215], v[62:65], v189, v190 op_sel_hi:[0,0,0]
	v_mfma_scale_f32_16x16x128_f8f6f4 v[54:57], v[18:25], v[208:215], v[54:57], v189, v190 op_sel_hi:[0,0,0]
	v_mfma_scale_f32_16x16x128_f8f6f4 v[46:49], v[26:33], v[220:227], v[46:49], v189, v190 op_sel_hi:[0,0,0]
	v_mfma_scale_f32_16x16x128_f8f6f4 v[38:41], v[18:25], v[220:227], v[38:41], v189, v190 op_sel_hi:[0,0,0]
	s_setprio 0
	s_setprio 1
	v_mfma_scale_f32_16x16x128_f8f6f4 v[90:93], v[10:17], v[192:199], v[90:93], v189, v190 op_sel_hi:[0,0,0]
	v_mfma_scale_f32_16x16x128_f8f6f4 v[82:85], v[2:9], v[192:199], v[82:85], v189, v190 op_sel_hi:[0,0,0]
	v_mfma_scale_f32_16x16x128_f8f6f4 v[74:77], v[10:17], v[200:207], v[74:77], v189, v190 op_sel_hi:[0,0,0]
	v_mfma_scale_f32_16x16x128_f8f6f4 v[66:69], v[2:9], v[200:207], v[66:69], v189, v190 op_sel_hi:[0,0,0]
	v_mfma_scale_f32_16x16x128_f8f6f4 v[58:61], v[10:17], v[208:215], v[58:61], v189, v190 op_sel_hi:[0,0,0]
	v_mfma_scale_f32_16x16x128_f8f6f4 v[50:53], v[2:9], v[208:215], v[50:53], v189, v190 op_sel_hi:[0,0,0]
	v_mfma_scale_f32_16x16x128_f8f6f4 v[42:45], v[10:17], v[220:227], v[42:45], v189, v190 op_sel_hi:[0,0,0]
	v_mfma_scale_f32_16x16x128_f8f6f4 v[34:37], v[2:9], v[220:227], v[34:37], v189, v190 op_sel_hi:[0,0,0]
	s_setprio 0
	s_barrier
	s_add_i32 s73, 0, 0x18000
	s_add_i32 s74, 0, 0x1c000
	v_add_u32_e32 v14, s73, v184
	v_add_u32_e32 v30, s74, v184
	ds_read_b128 v[2:5], v14
	ds_read_b128 v[6:9], v14 offset:1024
	ds_read_b128 v[10:13], v14 offset:2048
	ds_read_b128 v[14:17], v14 offset:3072
	ds_read_b128 v[18:21], v30
	ds_read_b128 v[22:25], v30 offset:1024
	ds_read_b128 v[26:29], v30 offset:2048
	ds_read_b128 v[30:33], v30 offset:3072
	s_add_u32 s56, s56, 0x40000
	s_addc_u32 s57, s57, 0
	s_mov_b32 m0, s63
	v_lshl_add_u64 v[216:217], s[56:57], 0, v[164:165]
	ds_read_b128 v[192:195], v188 offset:32768
	ds_read_b128 v[196:199], v188 offset:33792
	ds_read_b128 v[200:203], v188 offset:34816
	ds_read_b128 v[204:207], v188 offset:35840
	ds_read_b128 v[208:211], v188 offset:36864
	ds_read_b128 v[212:215], v188 offset:37888
	ds_read_b128 v[220:223], v188 offset:38912
	ds_read_b128 v[224:227], v188 offset:39936
	global_load_lds_dwordx4 v[216:217], off
	v_lshl_add_u64 v[216:217], s[56:57], 0, v[166:167]
	s_mov_b32 m0, s64
	s_nop 0
	global_load_lds_dwordx4 v[216:217], off
	s_waitcnt vmcnt(8)
	s_waitcnt lgkmcnt(0)
	v_mfma_scale_f32_16x16x128_f8f6f4 v[158:161], v[2:9], v[192:199], v[158:161], v189, v190 op_sel_hi:[0,0,0]
	v_mfma_scale_f32_16x16x128_f8f6f4 v[150:153], v[10:17], v[192:199], v[150:153], v189, v190 op_sel_hi:[0,0,0]
	s_barrier
	s_setprio 1
	s_waitcnt lgkmcnt(0)
	v_mfma_scale_f32_16x16x128_f8f6f4 v[142:145], v[2:9], v[200:207], v[142:145], v189, v190 op_sel_hi:[0,0,0]
	v_mfma_scale_f32_16x16x128_f8f6f4 v[134:137], v[10:17], v[200:207], v[134:137], v189, v190 op_sel_hi:[0,0,0]
	v_mfma_scale_f32_16x16x128_f8f6f4 v[126:129], v[2:9], v[208:215], v[126:129], v189, v190 op_sel_hi:[0,0,0]
	v_mfma_scale_f32_16x16x128_f8f6f4 v[118:121], v[10:17], v[208:215], v[118:121], v189, v190 op_sel_hi:[0,0,0]
	v_mfma_scale_f32_16x16x128_f8f6f4 v[110:113], v[2:9], v[220:227], v[110:113], v189, v190 op_sel_hi:[0,0,0]
	v_mfma_scale_f32_16x16x128_f8f6f4 v[102:105], v[10:17], v[220:227], v[102:105], v189, v190 op_sel_hi:[0,0,0]
	s_setprio 0
	s_setprio 1
	v_mfma_scale_f32_16x16x128_f8f6f4 v[154:157], v[18:25], v[192:199], v[154:157], v189, v190 op_sel_hi:[0,0,0]
	v_mfma_scale_f32_16x16x128_f8f6f4 v[146:149], v[26:33], v[192:199], v[146:149], v189, v190 op_sel_hi:[0,0,0]
	v_mfma_scale_f32_16x16x128_f8f6f4 v[138:141], v[18:25], v[200:207], v[138:141], v189, v190 op_sel_hi:[0,0,0]
	v_mfma_scale_f32_16x16x128_f8f6f4 v[130:133], v[26:33], v[200:207], v[130:133], v189, v190 op_sel_hi:[0,0,0]
	v_mfma_scale_f32_16x16x128_f8f6f4 v[122:125], v[18:25], v[208:215], v[122:125], v189, v190 op_sel_hi:[0,0,0]
	v_mfma_scale_f32_16x16x128_f8f6f4 v[114:117], v[26:33], v[208:215], v[114:117], v189, v190 op_sel_hi:[0,0,0]
	v_mfma_scale_f32_16x16x128_f8f6f4 v[106:109], v[18:25], v[220:227], v[106:109], v189, v190 op_sel_hi:[0,0,0]
	v_mfma_scale_f32_16x16x128_f8f6f4 v[98:101], v[26:33], v[220:227], v[98:101], v189, v190 op_sel_hi:[0,0,0]
	s_setprio 0
	s_barrier
	s_add_i32 s56, s73, s61
	v_lshl_add_u64 v[216:217], v[178:179], 0, s[20:21]
	s_mov_b32 m0, s56
	ds_read_b128 v[192:195], v188 offset:49152
	ds_read_b128 v[196:199], v188 offset:50176
	ds_read_b128 v[200:203], v188 offset:51200
	ds_read_b128 v[204:207], v188 offset:52224
	ds_read_b128 v[208:211], v188 offset:53248
	ds_read_b128 v[212:215], v188 offset:54272
	ds_read_b128 v[220:223], v188 offset:55296
	ds_read_b128 v[224:227], v188 offset:56320
	global_load_lds_dwordx4 v[216:217], off
	v_lshl_add_u64 v[216:217], v[178:179], 0, s[22:23]
	s_add_i32 m0, s56, 0x2000
	s_add_i32 s56, s74, s61
	global_load_lds_dwordx4 v[216:217], off
	v_lshl_add_u64 v[216:217], v[178:179], 0, s[26:27]
	s_mov_b32 m0, s56
	v_lshl_add_u64 v[178:179], v[178:179], 0, s[36:37]
	global_load_lds_dwordx4 v[216:217], off
	s_add_i32 m0, s56, 0x2000
	s_nop 0
	global_load_lds_dwordx4 v[178:179], off
	v_lshl_add_u64 v[178:179], v[180:181], 0, s[24:25]
	s_mov_b32 m0, s66
	s_nop 0
	global_load_lds_dwordx4 v[178:179], off
	v_lshl_add_u64 v[178:179], v[182:183], 0, s[24:25]
	s_mov_b32 m0, s67
	s_nop 0
	global_load_lds_dwordx4 v[178:179], off
	s_waitcnt vmcnt(8)
	s_waitcnt lgkmcnt(0)
	v_mfma_scale_f32_16x16x128_f8f6f4 v[94:97], v[2:9], v[192:199], v[94:97], v189, v190 op_sel_hi:[0,0,0]
	v_mfma_scale_f32_16x16x128_f8f6f4 v[86:89], v[10:17], v[192:199], v[86:89], v189, v190 op_sel_hi:[0,0,0]
	s_barrier
	s_setprio 1
	s_waitcnt lgkmcnt(0)
	v_mfma_scale_f32_16x16x128_f8f6f4 v[78:81], v[2:9], v[200:207], v[78:81], v189, v190 op_sel_hi:[0,0,0]
	v_mfma_scale_f32_16x16x128_f8f6f4 v[70:73], v[10:17], v[200:207], v[70:73], v189, v190 op_sel_hi:[0,0,0]
	v_mfma_scale_f32_16x16x128_f8f6f4 v[62:65], v[2:9], v[208:215], v[62:65], v189, v190 op_sel_hi:[0,0,0]
	v_mfma_scale_f32_16x16x128_f8f6f4 v[54:57], v[10:17], v[208:215], v[54:57], v189, v190 op_sel_hi:[0,0,0]
	v_mfma_scale_f32_16x16x128_f8f6f4 v[46:49], v[2:9], v[220:227], v[46:49], v189, v190 op_sel_hi:[0,0,0]
	v_mfma_scale_f32_16x16x128_f8f6f4 v[38:41], v[10:17], v[220:227], v[38:41], v189, v190 op_sel_hi:[0,0,0]
	s_setprio 0
	s_setprio 1
	v_mfma_scale_f32_16x16x128_f8f6f4 v[90:93], v[18:25], v[192:199], v[90:93], v189, v190 op_sel_hi:[0,0,0]
	v_mfma_scale_f32_16x16x128_f8f6f4 v[82:85], v[26:33], v[192:199], v[82:85], v189, v190 op_sel_hi:[0,0,0]
	v_mfma_scale_f32_16x16x128_f8f6f4 v[74:77], v[18:25], v[200:207], v[74:77], v189, v190 op_sel_hi:[0,0,0]
	v_mfma_scale_f32_16x16x128_f8f6f4 v[66:69], v[26:33], v[200:207], v[66:69], v189, v190 op_sel_hi:[0,0,0]
	v_mfma_scale_f32_16x16x128_f8f6f4 v[58:61], v[18:25], v[208:215], v[58:61], v189, v190 op_sel_hi:[0,0,0]
	v_mfma_scale_f32_16x16x128_f8f6f4 v[50:53], v[26:33], v[208:215], v[50:53], v189, v190 op_sel_hi:[0,0,0]
	v_mfma_scale_f32_16x16x128_f8f6f4 v[42:45], v[18:25], v[220:227], v[42:45], v189, v190 op_sel_hi:[0,0,0]
	v_mfma_scale_f32_16x16x128_f8f6f4 v[34:37], v[26:33], v[220:227], v[34:37], v189, v190 op_sel_hi:[0,0,0]
	s_setprio 0
	s_barrier
	s_add_i32 s49, s49, 2
	s_add_u32 s4, s4, 0x100
	s_addc_u32 s5, s5, 0
	s_cmp_gt_u32 s49, 13
	v_lshl_add_u64 v[176:177], v[176:177], 0, s[40:41]
	s_cbranch_scc0 .LBB0_1497
	s_and_b64 vcc, exec, s[38:39]
	s_cbranch_vccz .LBB0_1500
	s_barrier

.LBB0_1568:
	ds_read_b128 v[26:29], v186
	ds_read_b128 v[30:33], v186 offset:1024
	ds_read_b128 v[18:21], v186 offset:2048
	ds_read_b128 v[22:25], v186 offset:3072
	ds_read_b128 v[10:13], v187
	ds_read_b128 v[14:17], v187 offset:1024
	ds_read_b128 v[2:5], v187 offset:2048
	ds_read_b128 v[6:9], v187 offset:3072
	s_add_u32 s58, s56, 0xfff50080
	s_addc_u32 s59, s57, -1
	s_cmp_eq_u32 s53, 40
	s_cselect_b64 vcc, -1, 0
	s_cselect_b32 s59, s5, s59
	s_cselect_b32 s58, s4, s58
	v_cndmask_b32_e32 v179, v177, v175, vcc
	v_cndmask_b32_e32 v178, v176, v174, vcc
	v_lshl_add_u64 v[180:181], s[56:57], 0, v[170:171]
	s_add_i32 m0, s61, 0xc000
	ds_read_b128 v[192:195], v188
	ds_read_b128 v[196:199], v188 offset:1024
	ds_read_b128 v[200:203], v188 offset:2048
	ds_read_b128 v[204:207], v188 offset:3072
	ds_read_b128 v[208:211], v188 offset:4096
	ds_read_b128 v[212:215], v188 offset:5120
	ds_read_b128 v[220:223], v188 offset:6144
	ds_read_b128 v[224:227], v188 offset:7168
	global_load_lds_dwordx4 v[180:181], off
	v_lshl_add_u64 v[180:181], s[56:57], 0, v[172:173]
	s_add_i32 m0, s61, 0xe000
	s_nop 0
	global_load_lds_dwordx4 v[180:181], off
	s_waitcnt vmcnt(8)
	s_waitcnt lgkmcnt(0)
	v_mfma_scale_f32_16x16x128_f8f6f4 v[158:161], v[26:33], v[192:199], v[158:161], v189, v190 op_sel_hi:[0,0,0]
	v_mfma_scale_f32_16x16x128_f8f6f4 v[154:157], v[18:25], v[192:199], v[154:157], v189, v190 op_sel_hi:[0,0,0]
	s_barrier
	s_setprio 1
	s_waitcnt lgkmcnt(0)
	v_mfma_scale_f32_16x16x128_f8f6f4 v[150:153], v[26:33], v[200:207], v[150:153], v189, v190 op_sel_hi:[0,0,0]
	v_mfma_scale_f32_16x16x128_f8f6f4 v[142:145], v[18:25], v[200:207], v[142:145], v189, v190 op_sel_hi:[0,0,0]
	v_mfma_scale_f32_16x16x128_f8f6f4 v[134:137], v[26:33], v[208:215], v[134:137], v189, v190 op_sel_hi:[0,0,0]
	v_mfma_scale_f32_16x16x128_f8f6f4 v[126:129], v[18:25], v[208:215], v[126:129], v189, v190 op_sel_hi:[0,0,0]
	v_mfma_scale_f32_16x16x128_f8f6f4 v[118:121], v[26:33], v[220:227], v[118:121], v189, v190 op_sel_hi:[0,0,0]
	v_mfma_scale_f32_16x16x128_f8f6f4 v[110:113], v[18:25], v[220:227], v[110:113], v189, v190 op_sel_hi:[0,0,0]
	s_setprio 0
	s_setprio 1
	v_mfma_scale_f32_16x16x128_f8f6f4 v[146:149], v[10:17], v[192:199], v[146:149], v189, v190 op_sel_hi:[0,0,0]
	v_mfma_scale_f32_16x16x128_f8f6f4 v[138:141], v[2:9], v[192:199], v[138:141], v189, v190 op_sel_hi:[0,0,0]
	v_mfma_scale_f32_16x16x128_f8f6f4 v[130:133], v[10:17], v[200:207], v[130:133], v189, v190 op_sel_hi:[0,0,0]
	v_mfma_scale_f32_16x16x128_f8f6f4 v[122:125], v[2:9], v[200:207], v[122:125], v189, v190 op_sel_hi:[0,0,0]
	v_mfma_scale_f32_16x16x128_f8f6f4 v[114:117], v[10:17], v[208:215], v[114:117], v189, v190 op_sel_hi:[0,0,0]
	v_mfma_scale_f32_16x16x128_f8f6f4 v[106:109], v[2:9], v[208:215], v[106:109], v189, v190 op_sel_hi:[0,0,0]
	v_mfma_scale_f32_16x16x128_f8f6f4 v[102:105], v[10:17], v[220:227], v[102:105], v189, v190 op_sel_hi:[0,0,0]
	v_mfma_scale_f32_16x16x128_f8f6f4 v[98:101], v[2:9], v[220:227], v[98:101], v189, v190 op_sel_hi:[0,0,0]
	s_setprio 0
	s_barrier
	s_add_i32 s80, s69, s33
	v_lshl_add_u64 v[178:179], v[178:179], 0, v[164:165]
	s_mov_b32 m0, s80
	ds_read_b128 v[192:195], v188 offset:16384
	ds_read_b128 v[196:199], v188 offset:17408
	ds_read_b128 v[200:203], v188 offset:18432
	ds_read_b128 v[204:207], v188 offset:19456
	ds_read_b128 v[208:211], v188 offset:20480
	ds_read_b128 v[212:215], v188 offset:21504
	ds_read_b128 v[220:223], v188 offset:22528
	ds_read_b128 v[224:227], v188 offset:23552
	global_load_lds_dwordx4 v[178:179], off
	v_lshl_add_u64 v[180:181], v[178:179], 0, s[10:11]
	s_add_i32 m0, s80, 0x2000
	s_add_i32 s80, s70, s33
	global_load_lds_dwordx4 v[180:181], off
	v_lshl_add_u64 v[180:181], v[178:179], 0, s[12:13]
	s_mov_b32 m0, s80
	v_lshl_add_u64 v[182:183], s[58:59], 0, v[168:169]
	global_load_lds_dwordx4 v[180:181], off
	v_lshl_add_u64 v[180:181], v[178:179], 0, s[14:15]
	s_add_i32 m0, s80, 0x2000
	s_nop 0
	global_load_lds_dwordx4 v[180:181], off
	v_lshl_add_u64 v[180:181], s[58:59], 0, v[166:167]
	s_mov_b32 m0, s61
	s_nop 0
	global_load_lds_dwordx4 v[180:181], off
	s_mov_b32 m0, s62
	s_nop 0
	global_load_lds_dwordx4 v[182:183], off
	s_waitcnt vmcnt(8)
	s_waitcnt lgkmcnt(0)
	v_mfma_scale_f32_16x16x128_f8f6f4 v[94:97], v[26:33], v[192:199], v[94:97], v189, v190 op_sel_hi:[0,0,0]
	v_mfma_scale_f32_16x16x128_f8f6f4 v[90:93], v[18:25], v[192:199], v[90:93], v189, v190 op_sel_hi:[0,0,0]
	s_barrier
	s_setprio 1
	s_waitcnt lgkmcnt(0)
	v_mfma_scale_f32_16x16x128_f8f6f4 v[86:89], v[26:33], v[200:207], v[86:89], v189, v190 op_sel_hi:[0,0,0]
	v_mfma_scale_f32_16x16x128_f8f6f4 v[78:81], v[18:25], v[200:207], v[78:81], v189, v190 op_sel_hi:[0,0,0]
	v_mfma_scale_f32_16x16x128_f8f6f4 v[70:73], v[26:33], v[208:215], v[70:73], v189, v190 op_sel_hi:[0,0,0]
	v_mfma_scale_f32_16x16x128_f8f6f4 v[62:65], v[18:25], v[208:215], v[62:65], v189, v190 op_sel_hi:[0,0,0]
	v_mfma_scale_f32_16x16x128_f8f6f4 v[54:57], v[26:33], v[220:227], v[54:57], v189, v190 op_sel_hi:[0,0,0]
	v_mfma_scale_f32_16x16x128_f8f6f4 v[46:49], v[18:25], v[220:227], v[46:49], v189, v190 op_sel_hi:[0,0,0]
	s_setprio 0
	s_setprio 1
	v_mfma_scale_f32_16x16x128_f8f6f4 v[82:85], v[10:17], v[192:199], v[82:85], v189, v190 op_sel_hi:[0,0,0]
	v_mfma_scale_f32_16x16x128_f8f6f4 v[74:77], v[2:9], v[192:199], v[74:77], v189, v190 op_sel_hi:[0,0,0]
	v_mfma_scale_f32_16x16x128_f8f6f4 v[66:69], v[10:17], v[200:207], v[66:69], v189, v190 op_sel_hi:[0,0,0]
	v_mfma_scale_f32_16x16x128_f8f6f4 v[58:61], v[2:9], v[200:207], v[58:61], v189, v190 op_sel_hi:[0,0,0]
	v_mfma_scale_f32_16x16x128_f8f6f4 v[50:53], v[10:17], v[208:215], v[50:53], v189, v190 op_sel_hi:[0,0,0]
	v_mfma_scale_f32_16x16x128_f8f6f4 v[42:45], v[2:9], v[208:215], v[42:45], v189, v190 op_sel_hi:[0,0,0]
	v_mfma_scale_f32_16x16x128_f8f6f4 v[38:41], v[10:17], v[220:227], v[38:41], v189, v190 op_sel_hi:[0,0,0]
	v_mfma_scale_f32_16x16x128_f8f6f4 v[34:37], v[2:9], v[220:227], v[34:37], v189, v190 op_sel_hi:[0,0,0]
	s_setprio 0
	s_barrier
	s_add_i32 s80, 0, 0x18000
	s_add_i32 s81, 0, 0x1c000
	v_add_u32_e32 v14, s80, v184
	v_add_u32_e32 v30, s81, v184
	ds_read_b128 v[2:5], v14
	ds_read_b128 v[6:9], v14 offset:1024
	ds_read_b128 v[10:13], v14 offset:2048
	ds_read_b128 v[14:17], v14 offset:3072
	ds_read_b128 v[18:21], v30
	ds_read_b128 v[22:25], v30 offset:1024
	ds_read_b128 v[26:29], v30 offset:2048
	ds_read_b128 v[30:33], v30 offset:3072
	s_add_u32 s58, s58, 0xb0000
	s_addc_u32 s59, s59, 0
	s_mov_b32 m0, s63
	v_lshl_add_u64 v[216:217], s[58:59], 0, v[166:167]
	ds_read_b128 v[192:195], v188 offset:32768
	ds_read_b128 v[196:199], v188 offset:33792
	ds_read_b128 v[200:203], v188 offset:34816
	ds_read_b128 v[204:207], v188 offset:35840
	ds_read_b128 v[208:211], v188 offset:36864
	ds_read_b128 v[212:215], v188 offset:37888
	ds_read_b128 v[220:223], v188 offset:38912
	ds_read_b128 v[224:227], v188 offset:39936
	global_load_lds_dwordx4 v[216:217], off
	v_lshl_add_u64 v[216:217], s[58:59], 0, v[168:169]
	s_mov_b32 m0, s64
	s_nop 0
	global_load_lds_dwordx4 v[216:217], off
	s_waitcnt vmcnt(8)
	s_waitcnt lgkmcnt(0)
	v_mfma_scale_f32_16x16x128_f8f6f4 v[158:161], v[2:9], v[192:199], v[158:161], v189, v190 op_sel_hi:[0,0,0]
	v_mfma_scale_f32_16x16x128_f8f6f4 v[154:157], v[10:17], v[192:199], v[154:157], v189, v190 op_sel_hi:[0,0,0]
	s_barrier
	s_setprio 1
	s_waitcnt lgkmcnt(0)
	v_mfma_scale_f32_16x16x128_f8f6f4 v[150:153], v[2:9], v[200:207], v[150:153], v189, v190 op_sel_hi:[0,0,0]
	v_mfma_scale_f32_16x16x128_f8f6f4 v[142:145], v[10:17], v[200:207], v[142:145], v189, v190 op_sel_hi:[0,0,0]
	v_mfma_scale_f32_16x16x128_f8f6f4 v[134:137], v[2:9], v[208:215], v[134:137], v189, v190 op_sel_hi:[0,0,0]
	v_mfma_scale_f32_16x16x128_f8f6f4 v[126:129], v[10:17], v[208:215], v[126:129], v189, v190 op_sel_hi:[0,0,0]
	v_mfma_scale_f32_16x16x128_f8f6f4 v[118:121], v[2:9], v[220:227], v[118:121], v189, v190 op_sel_hi:[0,0,0]
	v_mfma_scale_f32_16x16x128_f8f6f4 v[110:113], v[10:17], v[220:227], v[110:113], v189, v190 op_sel_hi:[0,0,0]
	s_setprio 0
	s_setprio 1
	v_mfma_scale_f32_16x16x128_f8f6f4 v[146:149], v[18:25], v[192:199], v[146:149], v189, v190 op_sel_hi:[0,0,0]
	v_mfma_scale_f32_16x16x128_f8f6f4 v[138:141], v[26:33], v[192:199], v[138:141], v189, v190 op_sel_hi:[0,0,0]
	v_mfma_scale_f32_16x16x128_f8f6f4 v[130:133], v[18:25], v[200:207], v[130:133], v189, v190 op_sel_hi:[0,0,0]
	v_mfma_scale_f32_16x16x128_f8f6f4 v[122:125], v[26:33], v[200:207], v[122:125], v189, v190 op_sel_hi:[0,0,0]
	v_mfma_scale_f32_16x16x128_f8f6f4 v[114:117], v[18:25], v[208:215], v[114:117], v189, v190 op_sel_hi:[0,0,0]
	v_mfma_scale_f32_16x16x128_f8f6f4 v[106:109], v[26:33], v[208:215], v[106:109], v189, v190 op_sel_hi:[0,0,0]
	v_mfma_scale_f32_16x16x128_f8f6f4 v[102:105], v[18:25], v[220:227], v[102:105], v189, v190 op_sel_hi:[0,0,0]
	v_mfma_scale_f32_16x16x128_f8f6f4 v[98:101], v[26:33], v[220:227], v[98:101], v189, v190 op_sel_hi:[0,0,0]
	s_setprio 0
	s_barrier
	s_add_i32 s58, s80, s33
	v_lshl_add_u64 v[216:217], v[178:179], 0, s[24:25]
	s_mov_b32 m0, s58
	ds_read_b128 v[192:195], v188 offset:49152
	ds_read_b128 v[196:199], v188 offset:50176
	ds_read_b128 v[200:203], v188 offset:51200
	ds_read_b128 v[204:207], v188 offset:52224
	ds_read_b128 v[208:211], v188 offset:53248
	ds_read_b128 v[212:215], v188 offset:54272
	ds_read_b128 v[220:223], v188 offset:55296
	ds_read_b128 v[224:227], v188 offset:56320
	global_load_lds_dwordx4 v[216:217], off
	v_lshl_add_u64 v[216:217], v[178:179], 0, s[26:27]
	s_add_i32 m0, s58, 0x2000
	s_add_i32 s58, s81, s33
	global_load_lds_dwordx4 v[216:217], off
	v_lshl_add_u64 v[216:217], v[178:179], 0, s[38:39]
	s_mov_b32 m0, s58
	v_lshl_add_u64 v[178:179], v[178:179], 0, s[40:41]
	global_load_lds_dwordx4 v[216:217], off
	s_add_i32 m0, s58, 0x2000
	s_nop 0
	global_load_lds_dwordx4 v[178:179], off
	v_lshl_add_u64 v[178:179], v[180:181], 0, s[36:37]
	s_mov_b32 m0, s66
	s_nop 0
	global_load_lds_dwordx4 v[178:179], off
	v_lshl_add_u64 v[178:179], v[182:183], 0, s[36:37]
	s_mov_b32 m0, s67
	s_nop 0
	global_load_lds_dwordx4 v[178:179], off
	s_waitcnt vmcnt(8)
	s_waitcnt lgkmcnt(0)
	v_mfma_scale_f32_16x16x128_f8f6f4 v[94:97], v[2:9], v[192:199], v[94:97], v189, v190 op_sel_hi:[0,0,0]
	v_mfma_scale_f32_16x16x128_f8f6f4 v[90:93], v[10:17], v[192:199], v[90:93], v189, v190 op_sel_hi:[0,0,0]
	s_barrier
	s_setprio 1
	s_waitcnt lgkmcnt(0)
	v_mfma_scale_f32_16x16x128_f8f6f4 v[86:89], v[2:9], v[200:207], v[86:89], v189, v190 op_sel_hi:[0,0,0]
	v_mfma_scale_f32_16x16x128_f8f6f4 v[78:81], v[10:17], v[200:207], v[78:81], v189, v190 op_sel_hi:[0,0,0]
	v_mfma_scale_f32_16x16x128_f8f6f4 v[70:73], v[2:9], v[208:215], v[70:73], v189, v190 op_sel_hi:[0,0,0]
	v_mfma_scale_f32_16x16x128_f8f6f4 v[62:65], v[10:17], v[208:215], v[62:65], v189, v190 op_sel_hi:[0,0,0]
	v_mfma_scale_f32_16x16x128_f8f6f4 v[54:57], v[2:9], v[220:227], v[54:57], v189, v190 op_sel_hi:[0,0,0]
	v_mfma_scale_f32_16x16x128_f8f6f4 v[46:49], v[10:17], v[220:227], v[46:49], v189, v190 op_sel_hi:[0,0,0]
	s_setprio 0
	s_setprio 1
	v_mfma_scale_f32_16x16x128_f8f6f4 v[82:85], v[18:25], v[192:199], v[82:85], v189, v190 op_sel_hi:[0,0,0]
	v_mfma_scale_f32_16x16x128_f8f6f4 v[74:77], v[26:33], v[192:199], v[74:77], v189, v190 op_sel_hi:[0,0,0]
	v_mfma_scale_f32_16x16x128_f8f6f4 v[66:69], v[18:25], v[200:207], v[66:69], v189, v190 op_sel_hi:[0,0,0]
	v_mfma_scale_f32_16x16x128_f8f6f4 v[58:61], v[26:33], v[200:207], v[58:61], v189, v190 op_sel_hi:[0,0,0]
	v_mfma_scale_f32_16x16x128_f8f6f4 v[50:53], v[18:25], v[208:215], v[50:53], v189, v190 op_sel_hi:[0,0,0]
	v_mfma_scale_f32_16x16x128_f8f6f4 v[42:45], v[26:33], v[208:215], v[42:45], v189, v190 op_sel_hi:[0,0,0]
	v_mfma_scale_f32_16x16x128_f8f6f4 v[38:41], v[18:25], v[220:227], v[38:41], v189, v190 op_sel_hi:[0,0,0]
	v_mfma_scale_f32_16x16x128_f8f6f4 v[34:37], v[26:33], v[220:227], v[34:37], v189, v190 op_sel_hi:[0,0,0]
	s_setprio 0
	s_barrier
	s_add_i32 s53, s53, 2
	s_add_u32 s56, s56, 0x100
	s_addc_u32 s57, s57, 0
	s_cmp_gt_u32 s53, 41
	v_lshl_add_u64 v[176:177], v[176:177], 0, s[44:45]
	s_cbranch_scc0 .LBB0_1568
	s_and_b64 vcc, exec, s[42:43]
	s_cbranch_vccz .LBB0_1571
	s_barrier
